# speedup vs baseline: 1.0281x; 1.0200x over previous
_Z17conv_xproj_kernelPKDF16_PKfS2_S0_PDF16_S3_Pf:
	s_load_dwordx8 s[4:11], s[0:1], 0x0
	s_load_dwordx2 s[14:15], s[0:1], 0x20
	s_lshl_b32 s12, s2, 4
	s_and_b32 s3, s2, 0x7f
	v_lshlrev_b32_e32 v60, 4, v0
	v_lshrrev_b32_e32 v61, 6, v0
	v_and_b32_e32 v59, 63, v0
	v_mul_u32_u24_e32 v58, 0x600, v61
	v_or_b32_e32 v59, v58, v59
	v_lshlrev_b32_e32 v59, 4, v59
	s_waitcnt lgkmcnt(0)
	s_lshl_b32 s13, s2, 17
	s_add_u32 s16, s4, s13
	s_addc_u32 s17, s5, 0
	s_cmp_eq_u32 s3, 0
	s_cbranch_scc1 .Lcx_first
	s_sub_u32 s18, s16, 0x8000
	s_subb_u32 s19, s17, 0
	global_load_dwordx4 v[2:5], v60, s[18:19]
	s_branch .Lcx_go
.Lcx_first:
	v_mov_b32_e32 v2, 0
	v_mov_b32_e32 v3, 0
	v_mov_b32_e32 v4, 0
	v_mov_b32_e32 v5, 0
.Lcx_go:
	global_load_dwordx4 v[6:9], v60, s[16:17]
	s_add_u32 s16, s16, 0x8000
	s_addc_u32 s17, s17, 0
	global_load_dwordx4 v[10:13], v60, s[16:17]
	s_add_u32 s16, s16, 0x8000
	s_addc_u32 s17, s17, 0
	global_load_dwordx4 v[14:17], v60, s[16:17]
	s_add_u32 s16, s16, 0x8000
	s_addc_u32 s17, s17, 0
	global_load_dwordx4 v[18:21], v60, s[16:17]
	v_lshlrev_b32_e32 v61, 5, v0
	v_lshlrev_b32_e32 v58, 3, v0
	global_load_dwordx4 v[26:29], v61, s[6:7]
	global_load_dwordx4 v[30:33], v61, s[6:7] offset:16
	global_load_dwordx2 v[34:35], v58, s[8:9]
	s_lshl_b32 s13, s2, 16
	s_add_u32 s14, s14, s13
	s_addc_u32 s15, s15, 0
	v_lshlrev_b32_e32 v60, 5, v0
	v_lshlrev_b32_e32 v58, 2, v0
	s_mov_b32 s3, 0x42800000
	s_mov_b32 s13, 0xbcb8aa3b
	s_waitcnt vmcnt(0)
	global_load_dwordx4 v[62:65], v59, s[10:11]
	s_add_u32 s10, s10, 0x400
	s_addc_u32 s11, s11, 0
	global_load_dwordx4 v[66:69], v59, s[10:11]
	s_add_u32 s10, s10, 0x400
	s_addc_u32 s11, s11, 0
	global_load_dwordx4 v[70:73], v59, s[10:11]
	s_add_u32 s10, s10, 0x400
	s_addc_u32 s11, s11, 0
	global_load_dwordx4 v[74:77], v59, s[10:11]
	s_add_u32 s10, s10, 0x400
	s_addc_u32 s11, s11, 0
	global_load_dwordx4 v[78:81], v59, s[10:11]
	s_add_u32 s10, s10, 0x400
	s_addc_u32 s11, s11, 0
	global_load_dwordx4 v[82:85], v59, s[10:11]
	s_add_u32 s10, s10, 0x400
	s_addc_u32 s11, s11, 0
	global_load_dwordx4 v[86:89], v59, s[10:11]
	s_add_u32 s10, s10, 0x400
	s_addc_u32 s11, s11, 0
	global_load_dwordx4 v[90:93], v59, s[10:11]
	s_add_u32 s10, s10, 0x400
	s_addc_u32 s11, s11, 0
	global_load_dwordx4 v[94:97], v59, s[10:11]
	s_add_u32 s10, s10, 0x400
	s_addc_u32 s11, s11, 0
	global_load_dwordx4 v[98:101], v59, s[10:11]
	s_add_u32 s10, s10, 0x400
	s_addc_u32 s11, s11, 0
	global_load_dwordx4 v[102:105], v59, s[10:11]
	s_add_u32 s10, s10, 0x400
	s_addc_u32 s11, s11, 0
	global_load_dwordx4 v[106:109], v59, s[10:11]
	s_add_u32 s10, s10, 0x400
	s_addc_u32 s11, s11, 0
	global_load_dwordx4 v[110:113], v59, s[10:11]
	s_add_u32 s10, s10, 0x400
	s_addc_u32 s11, s11, 0
	global_load_dwordx4 v[114:117], v59, s[10:11]
	s_add_u32 s10, s10, 0x400
	s_addc_u32 s11, s11, 0
	global_load_dwordx4 v[118:121], v59, s[10:11]
	s_add_u32 s10, s10, 0x400
	s_addc_u32 s11, s11, 0
	global_load_dwordx4 v[122:125], v59, s[10:11]
	s_add_u32 s10, s10, 0x400
	s_addc_u32 s11, s11, 0
	v_mul_f32_e32 v26, s3, v26
	v_mul_f32_e32 v27, s3, v27
	v_mul_f32_e32 v28, s3, v28
	v_mul_f32_e32 v29, s3, v29
	v_mul_f32_e32 v30, s3, v30
	v_mul_f32_e32 v31, s3, v31
	v_mul_f32_e32 v32, s3, v32
	v_mul_f32_e32 v33, s3, v33
	v_mul_f32_e32 v34, s3, v34
	v_mul_f32_e32 v35, s3, v35
	v_cvt_f32_f16_sdwa v23, v2 dst_sel:DWORD dst_unused:UNUSED_PAD src0_sel:WORD_1
	v_cvt_f32_f16_e32 v24, v3
	v_cvt_f32_f16_sdwa v25, v3 dst_sel:DWORD dst_unused:UNUSED_PAD src0_sel:WORD_1
	v_cvt_f32_f16_sdwa v37, v4 dst_sel:DWORD dst_unused:UNUSED_PAD src0_sel:WORD_1
	v_cvt_f32_f16_e32 v38, v5
	v_cvt_f32_f16_sdwa v39, v5 dst_sel:DWORD dst_unused:UNUSED_PAD src0_sel:WORD_1
	s_nop 0
	v_cvt_f32_f16_e32 v22, v6
	v_fma_f32 v40, v26, v23, v34
	v_fma_f32 v40, v27, v24, v40
	v_fma_f32 v40, v28, v25, v40
	v_fma_f32 v40, v29, v22, v40
	v_mul_f32_e32 v42, s13, v40
	v_exp_f32_e32 v42, v42
	v_cvt_f32_f16_e32 v36, v8
	v_add_f32_e32 v42, 1.0, v42
	v_rcp_f32_e32 v42, v42
	v_fma_f32 v41, v30, v37, v35
	v_mul_f32_e32 v46, v40, v42
	v_fma_f32 v41, v31, v38, v41
	v_fma_f32 v41, v32, v39, v41
	v_fma_f32 v41, v33, v36, v41
	v_mul_f32_e32 v43, s13, v41
	v_exp_f32_e32 v43, v43
	s_nop 0
	v_add_f32_e32 v43, 1.0, v43
	v_rcp_f32_e32 v43, v43
	s_nop 0
	v_mul_f32_e32 v47, v41, v43
	v_cvt_pk_f16_f32 v48, v46, v47
	ds_write_b32 v58, v48
	v_cvt_f32_f16_sdwa v23, v6 dst_sel:DWORD dst_unused:UNUSED_PAD src0_sel:WORD_1
	v_fma_f32 v40, v26, v24, v34
	v_fma_f32 v40, v27, v25, v40
	v_fma_f32 v40, v28, v22, v40
	v_fma_f32 v40, v29, v23, v40
	v_mul_f32_e32 v42, s13, v40
	v_exp_f32_e32 v42, v42
	v_cvt_f32_f16_sdwa v37, v8 dst_sel:DWORD dst_unused:UNUSED_PAD src0_sel:WORD_1
	v_add_f32_e32 v42, 1.0, v42
	v_rcp_f32_e32 v42, v42
	v_fma_f32 v41, v30, v38, v35
	v_mul_f32_e32 v44, v40, v42
	v_fma_f32 v41, v31, v39, v41
	v_fma_f32 v41, v32, v36, v41
	v_fma_f32 v41, v33, v37, v41
	v_mul_f32_e32 v43, s13, v41
	v_exp_f32_e32 v43, v43
	v_cvt_pk_f16_f32 v50, v46, v44
	v_add_f32_e32 v43, 1.0, v43
	v_rcp_f32_e32 v43, v43
	s_nop 0
	v_mul_f32_e32 v45, v41, v43
	v_cvt_pk_f16_f32 v48, v44, v45
	v_cvt_pk_f16_f32 v54, v47, v45
	ds_write_b32 v58, v48 offset:4112
	v_cvt_f32_f16_e32 v24, v7
	v_fma_f32 v40, v26, v25, v34
	v_fma_f32 v40, v27, v22, v40
	v_fma_f32 v40, v28, v23, v40
	v_fma_f32 v40, v29, v24, v40
	v_mul_f32_e32 v42, s13, v40
	v_exp_f32_e32 v42, v42
	v_cvt_f32_f16_e32 v38, v9
	v_add_f32_e32 v42, 1.0, v42
	v_rcp_f32_e32 v42, v42
	v_fma_f32 v41, v30, v39, v35
	v_mul_f32_e32 v46, v40, v42
	v_fma_f32 v41, v31, v36, v41
	v_fma_f32 v41, v32, v37, v41
	v_fma_f32 v41, v33, v38, v41
	v_mul_f32_e32 v43, s13, v41
	v_exp_f32_e32 v43, v43
	s_nop 0
	v_add_f32_e32 v43, 1.0, v43
	v_rcp_f32_e32 v43, v43
	s_nop 0
	v_mul_f32_e32 v47, v41, v43
	v_cvt_pk_f16_f32 v48, v46, v47
	ds_write_b32 v58, v48 offset:8224
	v_cvt_f32_f16_sdwa v25, v7 dst_sel:DWORD dst_unused:UNUSED_PAD src0_sel:WORD_1
	v_fma_f32 v40, v26, v22, v34
	v_fma_f32 v40, v27, v23, v40
	v_fma_f32 v40, v28, v24, v40
	v_fma_f32 v40, v29, v25, v40
	v_mul_f32_e32 v42, s13, v40
	v_exp_f32_e32 v42, v42
	v_cvt_f32_f16_sdwa v39, v9 dst_sel:DWORD dst_unused:UNUSED_PAD src0_sel:WORD_1
	v_add_f32_e32 v42, 1.0, v42
	v_rcp_f32_e32 v42, v42
	v_fma_f32 v41, v30, v36, v35
	v_mul_f32_e32 v44, v40, v42
	v_fma_f32 v41, v31, v37, v41
	v_fma_f32 v41, v32, v38, v41
	v_fma_f32 v41, v33, v39, v41
	v_mul_f32_e32 v43, s13, v41
	v_exp_f32_e32 v43, v43
	v_cvt_pk_f16_f32 v51, v46, v44
	v_add_f32_e32 v43, 1.0, v43
	v_rcp_f32_e32 v43, v43
	s_nop 0
	v_mul_f32_e32 v45, v41, v43
	v_cvt_pk_f16_f32 v48, v44, v45
	v_cvt_pk_f16_f32 v55, v47, v45
	ds_write_b32 v58, v48 offset:12336
	v_cvt_f32_f16_e32 v22, v10
	v_fma_f32 v40, v26, v23, v34
	v_fma_f32 v40, v27, v24, v40
	v_fma_f32 v40, v28, v25, v40
	v_fma_f32 v40, v29, v22, v40
	v_mul_f32_e32 v42, s13, v40
	v_exp_f32_e32 v42, v42
	v_cvt_f32_f16_e32 v36, v12
	v_add_f32_e32 v42, 1.0, v42
	v_rcp_f32_e32 v42, v42
	v_fma_f32 v41, v30, v37, v35
	v_mul_f32_e32 v46, v40, v42
	v_fma_f32 v41, v31, v38, v41
	v_fma_f32 v41, v32, v39, v41
	v_fma_f32 v41, v33, v36, v41
	v_mul_f32_e32 v43, s13, v41
	v_exp_f32_e32 v43, v43
	s_nop 0
	v_add_f32_e32 v43, 1.0, v43
	v_rcp_f32_e32 v43, v43
	s_nop 0
	v_mul_f32_e32 v47, v41, v43
	v_cvt_pk_f16_f32 v48, v46, v47
	ds_write_b32 v58, v48 offset:16448
	v_cvt_f32_f16_sdwa v23, v10 dst_sel:DWORD dst_unused:UNUSED_PAD src0_sel:WORD_1
	v_fma_f32 v40, v26, v24, v34
	v_fma_f32 v40, v27, v25, v40
	v_fma_f32 v40, v28, v22, v40
	v_fma_f32 v40, v29, v23, v40
	v_mul_f32_e32 v42, s13, v40
	v_exp_f32_e32 v42, v42
	v_cvt_f32_f16_sdwa v37, v12 dst_sel:DWORD dst_unused:UNUSED_PAD src0_sel:WORD_1
	v_add_f32_e32 v42, 1.0, v42
	v_rcp_f32_e32 v42, v42
	v_fma_f32 v41, v30, v38, v35
	v_mul_f32_e32 v44, v40, v42
	v_fma_f32 v41, v31, v39, v41
	v_fma_f32 v41, v32, v36, v41
	v_fma_f32 v41, v33, v37, v41
	v_mul_f32_e32 v43, s13, v41
	v_exp_f32_e32 v43, v43
	v_cvt_pk_f16_f32 v52, v46, v44
	v_add_f32_e32 v43, 1.0, v43
	v_rcp_f32_e32 v43, v43
	s_nop 0
	v_mul_f32_e32 v45, v41, v43
	v_cvt_pk_f16_f32 v48, v44, v45
	v_cvt_pk_f16_f32 v56, v47, v45
	ds_write_b32 v58, v48 offset:20560
	v_cvt_f32_f16_e32 v24, v11
	v_fma_f32 v40, v26, v25, v34
	v_fma_f32 v40, v27, v22, v40
	v_fma_f32 v40, v28, v23, v40
	v_fma_f32 v40, v29, v24, v40
	v_mul_f32_e32 v42, s13, v40
	v_exp_f32_e32 v42, v42
	v_cvt_f32_f16_e32 v38, v13
	v_add_f32_e32 v42, 1.0, v42
	v_rcp_f32_e32 v42, v42
	v_fma_f32 v41, v30, v39, v35
	v_mul_f32_e32 v46, v40, v42
	v_fma_f32 v41, v31, v36, v41
	v_fma_f32 v41, v32, v37, v41
	v_fma_f32 v41, v33, v38, v41
	v_mul_f32_e32 v43, s13, v41
	v_exp_f32_e32 v43, v43
	s_nop 0
	v_add_f32_e32 v43, 1.0, v43
	v_rcp_f32_e32 v43, v43
	s_nop 0
	v_mul_f32_e32 v47, v41, v43
	v_cvt_pk_f16_f32 v48, v46, v47
	ds_write_b32 v58, v48 offset:24672
	v_cvt_f32_f16_sdwa v25, v11 dst_sel:DWORD dst_unused:UNUSED_PAD src0_sel:WORD_1
	v_fma_f32 v40, v26, v22, v34
	v_fma_f32 v40, v27, v23, v40
	v_fma_f32 v40, v28, v24, v40
	v_fma_f32 v40, v29, v25, v40
	v_mul_f32_e32 v42, s13, v40
	v_exp_f32_e32 v42, v42
	v_cvt_f32_f16_sdwa v39, v13 dst_sel:DWORD dst_unused:UNUSED_PAD src0_sel:WORD_1
	v_add_f32_e32 v42, 1.0, v42
	v_rcp_f32_e32 v42, v42
	v_fma_f32 v41, v30, v36, v35
	v_mul_f32_e32 v44, v40, v42
	v_fma_f32 v41, v31, v37, v41
	v_fma_f32 v41, v32, v38, v41
	v_fma_f32 v41, v33, v39, v41
	v_mul_f32_e32 v43, s13, v41
	v_exp_f32_e32 v43, v43
	v_cvt_pk_f16_f32 v53, v46, v44
	v_add_f32_e32 v43, 1.0, v43
	v_rcp_f32_e32 v43, v43
	s_nop 0
	v_mul_f32_e32 v45, v41, v43
	v_cvt_pk_f16_f32 v48, v44, v45
	v_cvt_pk_f16_f32 v57, v47, v45
	ds_write_b32 v58, v48 offset:28784
	global_store_dwordx4 v60, v[50:53], s[14:15]
	global_store_dwordx4 v60, v[54:57], s[14:15] offset:16
	s_add_u32 s14, s14, 0x8000
	s_addc_u32 s15, s15, 0
	v_cvt_f32_f16_e32 v22, v14
	v_fma_f32 v40, v26, v23, v34
	v_fma_f32 v40, v27, v24, v40
	v_fma_f32 v40, v28, v25, v40
	v_fma_f32 v40, v29, v22, v40
	v_mul_f32_e32 v42, s13, v40
	v_exp_f32_e32 v42, v42
	v_cvt_f32_f16_e32 v36, v16
	v_add_f32_e32 v42, 1.0, v42
	v_rcp_f32_e32 v42, v42
	v_fma_f32 v41, v30, v37, v35
	v_mul_f32_e32 v46, v40, v42
	v_fma_f32 v41, v31, v38, v41
	v_fma_f32 v41, v32, v39, v41
	v_fma_f32 v41, v33, v36, v41
	v_mul_f32_e32 v43, s13, v41
	v_exp_f32_e32 v43, v43
	s_nop 0
	v_add_f32_e32 v43, 1.0, v43
	v_rcp_f32_e32 v43, v43
	s_nop 0
	v_mul_f32_e32 v47, v41, v43
	v_cvt_pk_f16_f32 v48, v46, v47
	ds_write_b32 v58, v48 offset:32896
	v_cvt_f32_f16_sdwa v23, v14 dst_sel:DWORD dst_unused:UNUSED_PAD src0_sel:WORD_1
	v_fma_f32 v40, v26, v24, v34
	v_fma_f32 v40, v27, v25, v40
	v_fma_f32 v40, v28, v22, v40
	v_fma_f32 v40, v29, v23, v40
	v_mul_f32_e32 v42, s13, v40
	v_exp_f32_e32 v42, v42
	v_cvt_f32_f16_sdwa v37, v16 dst_sel:DWORD dst_unused:UNUSED_PAD src0_sel:WORD_1
	v_add_f32_e32 v42, 1.0, v42
	v_rcp_f32_e32 v42, v42
	v_fma_f32 v41, v30, v38, v35
	v_mul_f32_e32 v44, v40, v42
	v_fma_f32 v41, v31, v39, v41
	v_fma_f32 v41, v32, v36, v41
	v_fma_f32 v41, v33, v37, v41
	v_mul_f32_e32 v43, s13, v41
	v_exp_f32_e32 v43, v43
	v_cvt_pk_f16_f32 v50, v46, v44
	v_add_f32_e32 v43, 1.0, v43
	v_rcp_f32_e32 v43, v43
	s_nop 0
	v_mul_f32_e32 v45, v41, v43
	v_cvt_pk_f16_f32 v48, v44, v45
	v_cvt_pk_f16_f32 v54, v47, v45
	ds_write_b32 v58, v48 offset:37008
	v_cvt_f32_f16_e32 v24, v15
	v_fma_f32 v40, v26, v25, v34
	v_fma_f32 v40, v27, v22, v40
	v_fma_f32 v40, v28, v23, v40
	v_fma_f32 v40, v29, v24, v40
	v_mul_f32_e32 v42, s13, v40
	v_exp_f32_e32 v42, v42
	v_cvt_f32_f16_e32 v38, v17
	v_add_f32_e32 v42, 1.0, v42
	v_rcp_f32_e32 v42, v42
	v_fma_f32 v41, v30, v39, v35
	v_mul_f32_e32 v46, v40, v42
	v_fma_f32 v41, v31, v36, v41
	v_fma_f32 v41, v32, v37, v41
	v_fma_f32 v41, v33, v38, v41
	v_mul_f32_e32 v43, s13, v41
	v_exp_f32_e32 v43, v43
	s_nop 0
	v_add_f32_e32 v43, 1.0, v43
	v_rcp_f32_e32 v43, v43
	s_nop 0
	v_mul_f32_e32 v47, v41, v43
	v_cvt_pk_f16_f32 v48, v46, v47
	ds_write_b32 v58, v48 offset:41120
	v_cvt_f32_f16_sdwa v25, v15 dst_sel:DWORD dst_unused:UNUSED_PAD src0_sel:WORD_1
	v_fma_f32 v40, v26, v22, v34
	v_fma_f32 v40, v27, v23, v40
	v_fma_f32 v40, v28, v24, v40
	v_fma_f32 v40, v29, v25, v40
	v_mul_f32_e32 v42, s13, v40
	v_exp_f32_e32 v42, v42
	v_cvt_f32_f16_sdwa v39, v17 dst_sel:DWORD dst_unused:UNUSED_PAD src0_sel:WORD_1
	v_add_f32_e32 v42, 1.0, v42
	v_rcp_f32_e32 v42, v42
	v_fma_f32 v41, v30, v36, v35
	v_mul_f32_e32 v44, v40, v42
	v_fma_f32 v41, v31, v37, v41
	v_fma_f32 v41, v32, v38, v41
	v_fma_f32 v41, v33, v39, v41
	v_mul_f32_e32 v43, s13, v41
	v_exp_f32_e32 v43, v43
	v_cvt_pk_f16_f32 v51, v46, v44
	v_add_f32_e32 v43, 1.0, v43
	v_rcp_f32_e32 v43, v43
	s_nop 0
	v_mul_f32_e32 v45, v41, v43
	v_cvt_pk_f16_f32 v48, v44, v45
	v_cvt_pk_f16_f32 v55, v47, v45
	ds_write_b32 v58, v48 offset:45232
	v_cvt_f32_f16_e32 v22, v18
	v_fma_f32 v40, v26, v23, v34
	v_fma_f32 v40, v27, v24, v40
	v_fma_f32 v40, v28, v25, v40
	v_fma_f32 v40, v29, v22, v40
	v_mul_f32_e32 v42, s13, v40
	v_exp_f32_e32 v42, v42
	v_cvt_f32_f16_e32 v36, v20
	v_add_f32_e32 v42, 1.0, v42
	v_rcp_f32_e32 v42, v42
	v_fma_f32 v41, v30, v37, v35
	v_mul_f32_e32 v46, v40, v42
	v_fma_f32 v41, v31, v38, v41
	v_fma_f32 v41, v32, v39, v41
	v_fma_f32 v41, v33, v36, v41
	v_mul_f32_e32 v43, s13, v41
	v_exp_f32_e32 v43, v43
	s_nop 0
	v_add_f32_e32 v43, 1.0, v43
	v_rcp_f32_e32 v43, v43
	s_nop 0
	v_mul_f32_e32 v47, v41, v43
	v_cvt_pk_f16_f32 v48, v46, v47
	ds_write_b32 v58, v48 offset:49344
	v_cvt_f32_f16_sdwa v23, v18 dst_sel:DWORD dst_unused:UNUSED_PAD src0_sel:WORD_1
	v_fma_f32 v40, v26, v24, v34
	v_fma_f32 v40, v27, v25, v40
	v_fma_f32 v40, v28, v22, v40
	v_fma_f32 v40, v29, v23, v40
	v_mul_f32_e32 v42, s13, v40
	v_exp_f32_e32 v42, v42
	v_cvt_f32_f16_sdwa v37, v20 dst_sel:DWORD dst_unused:UNUSED_PAD src0_sel:WORD_1
	v_add_f32_e32 v42, 1.0, v42
	v_rcp_f32_e32 v42, v42
	v_fma_f32 v41, v30, v38, v35
	v_mul_f32_e32 v44, v40, v42
	v_fma_f32 v41, v31, v39, v41
	v_fma_f32 v41, v32, v36, v41
	v_fma_f32 v41, v33, v37, v41
	v_mul_f32_e32 v43, s13, v41
	v_exp_f32_e32 v43, v43
	v_cvt_pk_f16_f32 v52, v46, v44
	v_add_f32_e32 v43, 1.0, v43
	v_rcp_f32_e32 v43, v43
	s_nop 0
	v_mul_f32_e32 v45, v41, v43
	v_cvt_pk_f16_f32 v48, v44, v45
	v_cvt_pk_f16_f32 v56, v47, v45
	ds_write_b32 v58, v48 offset:53456
	v_cvt_f32_f16_e32 v24, v19
	v_fma_f32 v40, v26, v25, v34
	v_fma_f32 v40, v27, v22, v40
	v_fma_f32 v40, v28, v23, v40
	v_fma_f32 v40, v29, v24, v40
	v_mul_f32_e32 v42, s13, v40
	v_exp_f32_e32 v42, v42
	v_cvt_f32_f16_e32 v38, v21
	v_add_f32_e32 v42, 1.0, v42
	v_rcp_f32_e32 v42, v42
	v_fma_f32 v41, v30, v39, v35
	v_mul_f32_e32 v46, v40, v42
	v_fma_f32 v41, v31, v36, v41
	v_fma_f32 v41, v32, v37, v41
	v_fma_f32 v41, v33, v38, v41
	v_mul_f32_e32 v43, s13, v41
	v_exp_f32_e32 v43, v43
	s_nop 0
	v_add_f32_e32 v43, 1.0, v43
	v_rcp_f32_e32 v43, v43
	s_nop 0
	v_mul_f32_e32 v47, v41, v43
	v_cvt_pk_f16_f32 v48, v46, v47
	ds_write_b32 v58, v48 offset:57568
	v_cvt_f32_f16_sdwa v25, v19 dst_sel:DWORD dst_unused:UNUSED_PAD src0_sel:WORD_1
	v_fma_f32 v40, v26, v22, v34
	v_fma_f32 v40, v27, v23, v40
	v_fma_f32 v40, v28, v24, v40
	v_fma_f32 v40, v29, v25, v40
	v_mul_f32_e32 v42, s13, v40
	v_exp_f32_e32 v42, v42
	v_cvt_f32_f16_sdwa v39, v21 dst_sel:DWORD dst_unused:UNUSED_PAD src0_sel:WORD_1
	v_add_f32_e32 v42, 1.0, v42
	v_rcp_f32_e32 v42, v42
	v_fma_f32 v41, v30, v36, v35
	v_mul_f32_e32 v44, v40, v42
	v_fma_f32 v41, v31, v37, v41
	v_fma_f32 v41, v32, v38, v41
	v_fma_f32 v41, v33, v39, v41
	v_mul_f32_e32 v43, s13, v41
	v_exp_f32_e32 v43, v43
	v_cvt_pk_f16_f32 v53, v46, v44
	v_add_f32_e32 v43, 1.0, v43
	v_rcp_f32_e32 v43, v43
	s_nop 0
	v_mul_f32_e32 v45, v41, v43
	v_cvt_pk_f16_f32 v48, v44, v45
	v_cvt_pk_f16_f32 v57, v47, v45
	ds_write_b32 v58, v48 offset:61680
	global_store_dwordx4 v60, v[50:53], s[14:15]
	global_store_dwordx4 v60, v[54:57], s[14:15] offset:16
	s_nop 1
	global_load_dwordx4 v[26:29], v59, s[10:11]
	s_add_u32 s10, s10, 0x400
	s_addc_u32 s11, s11, 0
	global_load_dwordx4 v[30:33], v59, s[10:11]
	s_add_u32 s10, s10, 0x400
	s_addc_u32 s11, s11, 0
	global_load_dwordx4 v[34:37], v59, s[10:11]
	s_add_u32 s10, s10, 0x400
	s_addc_u32 s11, s11, 0
	global_load_dwordx4 v[38:41], v59, s[10:11]
	s_add_u32 s10, s10, 0x400
	s_addc_u32 s11, s11, 0
	global_load_dwordx4 v[42:45], v59, s[10:11]
	s_add_u32 s10, s10, 0x400
	s_addc_u32 s11, s11, 0
	global_load_dwordx4 v[46:49], v59, s[10:11]
	s_add_u32 s10, s10, 0x400
	s_addc_u32 s11, s11, 0
	global_load_dwordx4 v[50:53], v59, s[10:11]
	s_add_u32 s10, s10, 0x400
	s_addc_u32 s11, s11, 0
	global_load_dwordx4 v[54:57], v59, s[10:11]
	v_and_b32_e32 v126, 15, v0
	v_mul_u32_u24_e32 v126, 0x1010, v126
	v_lshrrev_b32_e32 v127, 6, v0
	v_lshl_add_u32 v126, v127, 8, v126
	v_bfe_u32 v127, v0, 4, 2
	v_lshl_add_u32 v126, v127, 4, v126
	s_waitcnt lgkmcnt(0)
	ds_read_b128 v[58:61], v126
	s_waitcnt vmcnt(27) lgkmcnt(0)
	v_mfma_f32_16x16x32_f16 v[22:25], v[62:65], v[58:61], 0
	s_waitcnt vmcnt(26)
	v_mfma_f32_16x16x32_f16 v[18:21], v[66:69], v[58:61], 0
	s_waitcnt vmcnt(25)
	v_mfma_f32_16x16x32_f16 v[14:17], v[70:73], v[58:61], 0
	s_waitcnt vmcnt(24)
	v_mfma_f32_16x16x32_f16 v[10:13], v[74:77], v[58:61], 0
	s_waitcnt vmcnt(23)
	v_mfma_f32_16x16x32_f16 v[6:9], v[78:81], v[58:61], 0
	s_waitcnt vmcnt(22)
	v_mfma_f32_16x16x32_f16 v[2:5], v[82:85], v[58:61], 0
	s_nop 3
	ds_read_b128 v[62:65], v126 offset:64
	ds_read_b128 v[66:69], v126 offset:128
	ds_read_b128 v[70:73], v126 offset:192
	s_waitcnt lgkmcnt(0)
	s_waitcnt vmcnt(21)
	v_mfma_f32_16x16x32_f16 v[22:25], v[86:89], v[62:65], v[22:25]
	s_waitcnt vmcnt(20)
	v_mfma_f32_16x16x32_f16 v[18:21], v[90:93], v[62:65], v[18:21]
	s_waitcnt vmcnt(19)
	v_mfma_f32_16x16x32_f16 v[14:17], v[94:97], v[62:65], v[14:17]
	s_waitcnt vmcnt(18)
	v_mfma_f32_16x16x32_f16 v[10:13], v[98:101], v[62:65], v[10:13]
	s_waitcnt vmcnt(17)
	v_mfma_f32_16x16x32_f16 v[6:9], v[102:105], v[62:65], v[6:9]
	s_waitcnt vmcnt(16)
	v_mfma_f32_16x16x32_f16 v[2:5], v[106:109], v[62:65], v[2:5]
	s_waitcnt vmcnt(15)
	v_mfma_f32_16x16x32_f16 v[22:25], v[110:113], v[66:69], v[22:25]
	s_waitcnt vmcnt(14)
	v_mfma_f32_16x16x32_f16 v[18:21], v[114:117], v[66:69], v[18:21]
	s_waitcnt vmcnt(13)
	v_mfma_f32_16x16x32_f16 v[14:17], v[118:121], v[66:69], v[14:17]
	s_waitcnt vmcnt(12)
	v_mfma_f32_16x16x32_f16 v[10:13], v[122:125], v[66:69], v[10:13]
	s_waitcnt vmcnt(7)
	v_mfma_f32_16x16x32_f16 v[6:9], v[26:29], v[66:69], v[6:9]
	s_waitcnt vmcnt(6)
	v_mfma_f32_16x16x32_f16 v[2:5], v[30:33], v[66:69], v[2:5]
	s_waitcnt vmcnt(5)
	v_mfma_f32_16x16x32_f16 v[22:25], v[34:37], v[70:73], v[22:25]
	s_waitcnt vmcnt(4)
	v_mfma_f32_16x16x32_f16 v[18:21], v[38:41], v[70:73], v[18:21]
	s_waitcnt vmcnt(3)
	v_mfma_f32_16x16x32_f16 v[14:17], v[42:45], v[70:73], v[14:17]
	s_waitcnt vmcnt(2)
	v_mfma_f32_16x16x32_f16 v[10:13], v[46:49], v[70:73], v[10:13]
	s_waitcnt vmcnt(1)
	v_mfma_f32_16x16x32_f16 v[6:9], v[50:53], v[70:73], v[6:9]
	s_waitcnt vmcnt(0)
	v_mfma_f32_16x16x32_f16 v[2:5], v[54:57], v[70:73], v[2:5]
	s_nop 7
	s_barrier
	v_lshrrev_b32_e32 v1, 6, v0
	v_and_b32_e32 v26, 15, v0
	v_lshl_add_u32 v1, v1, 4, v26
	v_bfe_u32 v30, v0, 4, 2
	v_lshlrev_b32_e32 v30, 4, v30
	v_cmp_lt_u32_e32 vcc, 0x1ff, v0
	s_and_saveexec_b64 s[2:3], vcc
	s_cbranch_execz .LBB1_5
	s_nop 0
	v_add_u32_e32 v26, 0xffffff80, v1
	s_movk_i32 s4, 0x184
	v_mad_i32_i24 v26, v26, s4, v30
	ds_write2_b32 v26, v22, v23 offset1:1
	ds_write2_b32 v26, v24, v25 offset0:2 offset1:3
	ds_write2_b32 v26, v18, v19 offset0:16 offset1:17
	ds_write2_b32 v26, v20, v21 offset0:18 offset1:19
	ds_write2_b32 v26, v14, v15 offset0:32 offset1:33
	ds_write2_b32 v26, v16, v17 offset0:34 offset1:35
	ds_write2_b32 v26, v10, v11 offset0:48 offset1:49
	ds_write2_b32 v26, v12, v13 offset0:50 offset1:51
	ds_write2_b32 v26, v6, v7 offset0:64 offset1:65
	ds_write2_b32 v26, v8, v9 offset0:66 offset1:67
	ds_write2_b32 v26, v2, v3 offset0:80 offset1:81
	ds_write2_b32 v26, v4, v5 offset0:82 offset1:83

	.amdhsa_kernel _Z17conv_xproj_kernelPKDF16_PKfS2_S0_PDF16_S3_Pf
		.amdhsa_group_segment_fixed_size 65792
		.amdhsa_private_segment_fixed_size 0
		.amdhsa_kernarg_size 56
		.amdhsa_user_sgpr_count 2
		.amdhsa_user_sgpr_dispatch_ptr 0
		.amdhsa_user_sgpr_queue_ptr 0
		.amdhsa_user_sgpr_kernarg_segment_ptr 1
		.amdhsa_user_sgpr_dispatch_id 0
		.amdhsa_user_sgpr_kernarg_preload_length 0
		.amdhsa_user_sgpr_kernarg_preload_offset 0
		.amdhsa_user_sgpr_private_segment_size 0
		.amdhsa_uses_dynamic_stack 0
		.amdhsa_enable_private_segment 0
		.amdhsa_system_sgpr_workgroup_id_x 1
		.amdhsa_system_sgpr_workgroup_id_y 0
		.amdhsa_system_sgpr_workgroup_id_z 0
		.amdhsa_system_sgpr_workgroup_info 0
		.amdhsa_system_vgpr_workitem_id 0
		.amdhsa_next_free_vgpr 128
		.amdhsa_next_free_sgpr 20
		.amdhsa_accum_offset 128
		.amdhsa_reserve_vcc 1
		.amdhsa_float_round_mode_32 0
		.amdhsa_float_round_mode_16_64 0
		.amdhsa_float_denorm_mode_32 3
		.amdhsa_float_denorm_mode_16_64 3
		.amdhsa_dx10_clamp 1
		.amdhsa_ieee_mode 1
		.amdhsa_fp16_overflow 0
		.amdhsa_tg_split 0
		.amdhsa_exception_fp_ieee_invalid_op 0
		.amdhsa_exception_fp_denorm_src 0
		.amdhsa_exception_fp_ieee_div_zero 0
		.amdhsa_exception_fp_ieee_overflow 0
		.amdhsa_exception_fp_ieee_underflow 0
		.amdhsa_exception_fp_ieee_inexact 0
		.amdhsa_exception_int_div_zero 0
	.end_amdhsa_kernel

_Z10scan_pass1PKDF16_S0_PKfS0_S2_S2_PDF16_PfS4_S2_S3_:
	s_load_dwordx16 s[8:23], s[0:1], 0x0
	s_load_dwordx4 s[24:27], s[0:1], 0x40
	s_load_dwordx2 s[28:29], s[0:1], 0x50
	s_mov_b32 s64, 0x3d800000
	s_mov_b32 s65, 0x3fb8aa3b
	s_mov_b32 s66, 0x3f317218
	s_mov_b32 s84, 0x40800000
	s_mov_b32 s86, 0x41800000
	s_lshl_b32 s5, s4, 11
	s_lshl_b32 s6, s3, 5
	s_add_i32 s5, s5, s6
	s_lshl_b32 s6, s4, 6
	s_add_i32 s6, s6, s3
	s_getreg_b32 s7, hwreg(HW_REG_HW_ID, 0, 4)
	s_and_b32 s7, s7, 3
	s_cmp_eq_u32 s7, 0
	s_cbranch_scc1 .Lstag_p1_done
.Lstag_p1_loop:
	s_sleep 56
	s_sub_u32 s7, s7, 1
	s_cmp_lg_u32 s7, 0
	s_cbranch_scc1 .Lstag_p1_loop
.Lstag_p1_done:
	v_lshl_or_b32 v1, s2, 8, v0
	v_and_b32_e32 v127, 63, v0
	v_lshlrev_b32_e32 v127, 4, v127
	v_lshrrev_b32_e32 v98, 6, v0
	v_lshl_or_b32 v98, v98, 13, v127
	v_add_u32_e32 v99, 0x1000, v98
	v_lshlrev_b32_e32 v126, 4, v1
	v_lshlrev_b32_e32 v114, 2, v1
	v_lshlrev_b32_e32 v115, 6, v1
	v_lshlrev_b32_e32 v116, 5, v0
	s_waitcnt lgkmcnt(0)
	s_lshl_b32 s7, s5, 7
	s_add_u32 s70, s16, s7
	s_addc_u32 s71, s17, 0
	s_load_dwordx16 s[32:47], s[70:71], 0x0
	s_lshl_b32 s7, s6, 12
	s_add_u32 s74, s8, s7
	s_addc_u32 s75, s9, 0
	global_load_dwordx4 v[82:85], v127, s[74:75]
	global_load_dwordx4 v[86:89], v127, s[74:75] offset:1024
	global_load_dwordx4 v[90:93], v127, s[74:75] offset:2048
	global_load_dwordx4 v[94:97], v127, s[74:75] offset:3072
	s_lshl_b32 s7, s2, 15
	s_add_u32 s74, s10, s7
	s_addc_u32 s75, s11, 0
	global_load_dwordx4 v[18:21], v99, s[74:75]
	global_load_dwordx4 v[22:25], v99, s[74:75] offset:1024
	global_load_dwordx4 v[26:29], v99, s[74:75] offset:2048
	global_load_dwordx4 v[30:33], v99, s[74:75] offset:3072
	global_load_dwordx4 v[102:105], v98, s[74:75] offset:1024
	global_load_dwordx4 v[106:109], v98, s[74:75] offset:2048
	global_load_dwordx4 v[110:113], v98, s[74:75] offset:3072
	global_load_dwordx4 v[98:101], v98, s[74:75]
	global_load_dword v122, v114, s[12:13]
	global_load_dwordx4 v[2:5], v115, s[18:19]
	global_load_dwordx4 v[6:9], v115, s[18:19] offset:16
	global_load_dwordx4 v[10:13], v115, s[18:19] offset:32
	global_load_dwordx4 v[14:17], v115, s[18:19] offset:48
	s_lshr_b32 s7, s5, 3
	s_lshl_b32 s7, s7, 15
	s_add_u32 s74, s14, s7
	s_addc_u32 s75, s15, 0
	global_load_dwordx4 v[66:69], v126, s[74:75]
	s_add_u32 s82, s74, 0x8000
	s_addc_u32 s83, s75, 0
	s_lshl_b32 s7, s6, 3
	s_add_i32 s7, s7, s2
	s_lshl_b32 s4, s7, 13
	s_add_u32 s74, s26, s4
	s_addc_u32 s75, s27, 0
	s_lshl_b32 s4, s7, 12
	s_add_u32 s80, s28, s4
	s_addc_u32 s81, s29, 0
	s_lshr_b32 s7, s5, 2
	s_lshl_b32 s7, s7, 15
	s_add_u32 s72, s24, s7
	s_addc_u32 s73, s25, 0
	s_lshl_b32 s7, s6, 16
	s_add_u32 s76, s20, s7
	s_addc_u32 s77, s21, 0
	s_lshl_b32 s7, s6, 13
	s_add_u32 s78, s22, s7
	s_addc_u32 s79, s23, 0
	s_waitcnt vmcnt(6)
	global_load_dwordx4 v[70:73], v126, s[82:83]
	s_add_u32 s82, s82, 0x8000
	s_addc_u32 s83, s83, 0
	global_load_dwordx4 v[74:77], v126, s[82:83]
	s_add_u32 s82, s82, 0x8000
	s_addc_u32 s83, s83, 0
	global_load_dwordx4 v[78:81], v126, s[82:83]
	global_load_dwordx4 v[118:121], v116, s[74:75] nt
	global_load_dwordx4 v[114:117], v116, s[74:75] offset:16 nt
	v_mfma_f32_32x32x16_f16 v[34:49], v[82:85], v[98:101], 0
	v_mfma_f32_32x32x16_f16 v[50:65], v[82:85], v[18:21], 0
	v_mfma_f32_32x32x16_f16 v[34:49], v[86:89], v[102:105], v[34:49]
	v_mfma_f32_32x32x16_f16 v[50:65], v[86:89], v[22:25], v[50:65]
	v_mfma_f32_32x32x16_f16 v[34:49], v[90:93], v[106:109], v[34:49]
	v_mfma_f32_32x32x16_f16 v[50:65], v[90:93], v[26:29], v[50:65]
	v_mfma_f32_32x32x16_f16 v[34:49], v[94:97], v[110:113], v[34:49]
	v_mfma_f32_32x32x16_f16 v[50:65], v[94:97], v[30:33], v[50:65]
	v_mov_b32_e32 v123, 0
	s_nop 15
	s_nop 3
	v_permlane32_swap_b32_e32 v34, v50
	v_permlane32_swap_b32_e32 v35, v51
	v_permlane32_swap_b32_e32 v36, v52
	v_permlane32_swap_b32_e32 v37, v53
	v_permlane32_swap_b32_e32 v38, v54
	v_permlane32_swap_b32_e32 v39, v55
	v_permlane32_swap_b32_e32 v40, v56
	v_permlane32_swap_b32_e32 v41, v57
	v_permlane32_swap_b32_e32 v42, v58
	v_permlane32_swap_b32_e32 v43, v59
	v_permlane32_swap_b32_e32 v44, v60
	v_permlane32_swap_b32_e32 v45, v61
	v_permlane32_swap_b32_e32 v46, v62
	v_permlane32_swap_b32_e32 v47, v63
	v_permlane32_swap_b32_e32 v48, v64
	v_permlane32_swap_b32_e32 v49, v65
	s_waitcnt vmcnt(5)
	v_fma_f32 v98, v34, s64, v122
	v_mul_f32_e64 v99, -|v98|, s65
	v_cvt_f32_f16_e32 v125, v66
	v_exp_f32_e32 v99, v99
	v_max_f32_e32 v98, 0, v98
	v_add_f32_e32 v99, 1.0, v99
	v_log_f32_e32 v99, v99
	s_nop 0
	v_fma_f32 v82, v99, s66, v98
	v_add_f32_e32 v123, v123, v82
	v_mul_f32_e32 v124, v82, v125
	s_waitcnt lgkmcnt(0)
	s_load_dwordx16 s[48:63], s[70:71], 0x80
	v_fma_f32 v98, v35, s64, v122
	v_mul_f32_e64 v99, -|v98|, s65
	v_cvt_f32_f16_sdwa v125, v66 dst_sel:DWORD dst_unused:UNUSED_PAD src0_sel:WORD_1
	v_exp_f32_e32 v99, v99
	v_max_f32_e32 v98, 0, v98
	v_add_f32_e32 v99, 1.0, v99
	v_log_f32_e32 v99, v99
	v_pk_mul_f32 v[18:19], v[124:125], s[32:33] op_sel_hi:[0,1]
	v_fma_f32 v83, v99, s66, v98
	v_add_f32_e32 v123, v123, v83
	v_pk_mul_f32 v[20:21], v[124:125], s[34:35] op_sel_hi:[0,1]
	v_pk_mul_f32 v[22:23], v[124:125], s[36:37] op_sel_hi:[0,1]
	v_pk_mul_f32 v[24:25], v[124:125], s[38:39] op_sel_hi:[0,1]
	v_pk_mul_f32 v[26:27], v[124:125], s[40:41] op_sel_hi:[0,1]
	v_pk_mul_f32 v[28:29], v[124:125], s[42:43] op_sel_hi:[0,1]
	v_pk_mul_f32 v[30:31], v[124:125], s[44:45] op_sel_hi:[0,1]
	v_pk_mul_f32 v[32:33], v[124:125], s[46:47] op_sel_hi:[0,1]
	v_mul_f32_e32 v124, v83, v125
	s_waitcnt lgkmcnt(0)
	s_load_dwordx16 s[32:47], s[70:71], 0x100
	v_fma_f32 v98, v36, s64, v122
	v_mul_f32_e64 v99, -|v98|, s65
	v_cvt_f32_f16_e32 v125, v67
	v_exp_f32_e32 v99, v99
	v_max_f32_e32 v98, 0, v98
	v_add_f32_e32 v99, 1.0, v99
	v_log_f32_e32 v99, v99
	v_pk_mul_f32 v[90:91], v[82:83], v[2:3] op_sel:[1,0]
	v_fma_f32 v84, v99, s66, v98
	v_add_f32_e32 v123, v123, v84
	v_exp_f32_e32 v90, v90
	v_exp_f32_e32 v91, v91
	v_pk_mul_f32 v[92:93], v[82:83], v[4:5] op_sel:[1,0]
	v_pk_mul_f32 v[90:91], v[18:19], v[90:91]
	v_exp_f32_e32 v92, v92
	v_pk_fma_f32 v[18:19], v[124:125], s[48:49], v[90:91] op_sel_hi:[0,1,1]
	v_exp_f32_e32 v93, v93
	v_pk_mul_f32 v[94:95], v[82:83], v[6:7] op_sel:[1,0]
	v_pk_mul_f32 v[92:93], v[20:21], v[92:93]
	v_exp_f32_e32 v94, v94
	v_pk_fma_f32 v[20:21], v[124:125], s[50:51], v[92:93] op_sel_hi:[0,1,1]
	v_exp_f32_e32 v95, v95
	v_pk_mul_f32 v[96:97], v[82:83], v[8:9] op_sel:[1,0]
	v_pk_mul_f32 v[94:95], v[22:23], v[94:95]
	v_exp_f32_e32 v96, v96
	v_pk_fma_f32 v[22:23], v[124:125], s[52:53], v[94:95] op_sel_hi:[0,1,1]
	v_exp_f32_e32 v97, v97
	v_pk_mul_f32 v[90:91], v[82:83], v[10:11] op_sel:[1,0]
	v_pk_mul_f32 v[96:97], v[24:25], v[96:97]
	v_exp_f32_e32 v90, v90
	v_pk_fma_f32 v[24:25], v[124:125], s[54:55], v[96:97] op_sel_hi:[0,1,1]
	v_exp_f32_e32 v91, v91
	v_pk_mul_f32 v[92:93], v[82:83], v[12:13] op_sel:[1,0]
	v_pk_mul_f32 v[90:91], v[26:27], v[90:91]
	v_exp_f32_e32 v92, v92
	v_pk_fma_f32 v[26:27], v[124:125], s[56:57], v[90:91] op_sel_hi:[0,1,1]
	v_exp_f32_e32 v93, v93
	v_pk_mul_f32 v[94:95], v[82:83], v[14:15] op_sel:[1,0]
	v_pk_mul_f32 v[92:93], v[28:29], v[92:93]
	v_exp_f32_e32 v94, v94
	v_pk_fma_f32 v[28:29], v[124:125], s[58:59], v[92:93] op_sel_hi:[0,1,1]
	v_exp_f32_e32 v95, v95
	v_pk_mul_f32 v[96:97], v[82:83], v[16:17] op_sel:[1,0]
	v_pk_mul_f32 v[94:95], v[30:31], v[94:95]
	v_exp_f32_e32 v96, v96
	v_pk_fma_f32 v[30:31], v[124:125], s[60:61], v[94:95] op_sel_hi:[0,1,1]
	v_exp_f32_e32 v97, v97
	s_nop 0
	v_pk_mul_f32 v[96:97], v[32:33], v[96:97]
	s_nop 0
	v_pk_fma_f32 v[32:33], v[124:125], s[62:63], v[96:97] op_sel_hi:[0,1,1]
	v_mul_f32_e32 v124, v84, v125
	s_waitcnt lgkmcnt(0)
	s_load_dwordx16 s[48:63], s[70:71], 0x180
	v_fma_f32 v98, v37, s64, v122
	v_mul_f32_e64 v99, -|v98|, s65
	v_cvt_f32_f16_sdwa v125, v67 dst_sel:DWORD dst_unused:UNUSED_PAD src0_sel:WORD_1
	v_exp_f32_e32 v99, v99
	v_max_f32_e32 v98, 0, v98
	v_add_f32_e32 v99, 1.0, v99
	v_log_f32_e32 v99, v99
	v_pk_mul_f32 v[90:91], v[84:85], v[2:3] op_sel_hi:[0,1]
	v_fma_f32 v85, v99, s66, v98
	v_add_f32_e32 v123, v123, v85
	v_exp_f32_e32 v90, v90
	v_exp_f32_e32 v91, v91
	v_pk_mul_f32 v[92:93], v[84:85], v[4:5] op_sel_hi:[0,1]
	v_pk_mul_f32 v[90:91], v[18:19], v[90:91]
	v_exp_f32_e32 v92, v92
	v_pk_fma_f32 v[18:19], v[124:125], s[32:33], v[90:91] op_sel_hi:[0,1,1]
	v_exp_f32_e32 v93, v93
	v_pk_mul_f32 v[94:95], v[84:85], v[6:7] op_sel_hi:[0,1]
	v_pk_mul_f32 v[92:93], v[20:21], v[92:93]
	v_exp_f32_e32 v94, v94
	v_pk_fma_f32 v[20:21], v[124:125], s[34:35], v[92:93] op_sel_hi:[0,1,1]
	v_exp_f32_e32 v95, v95
	v_pk_mul_f32 v[96:97], v[84:85], v[8:9] op_sel_hi:[0,1]
	v_pk_mul_f32 v[94:95], v[22:23], v[94:95]
	v_exp_f32_e32 v96, v96
	v_pk_fma_f32 v[22:23], v[124:125], s[36:37], v[94:95] op_sel_hi:[0,1,1]
	v_exp_f32_e32 v97, v97
	v_pk_mul_f32 v[90:91], v[84:85], v[10:11] op_sel_hi:[0,1]
	v_pk_mul_f32 v[96:97], v[24:25], v[96:97]
	v_exp_f32_e32 v90, v90
	v_pk_fma_f32 v[24:25], v[124:125], s[38:39], v[96:97] op_sel_hi:[0,1,1]
	v_exp_f32_e32 v91, v91
	v_pk_mul_f32 v[92:93], v[84:85], v[12:13] op_sel_hi:[0,1]
	v_pk_mul_f32 v[90:91], v[26:27], v[90:91]
	v_exp_f32_e32 v92, v92
	v_pk_fma_f32 v[26:27], v[124:125], s[40:41], v[90:91] op_sel_hi:[0,1,1]
	v_exp_f32_e32 v93, v93
	v_pk_mul_f32 v[94:95], v[84:85], v[14:15] op_sel_hi:[0,1]
	v_pk_mul_f32 v[92:93], v[28:29], v[92:93]
	v_exp_f32_e32 v94, v94
	v_pk_fma_f32 v[28:29], v[124:125], s[42:43], v[92:93] op_sel_hi:[0,1,1]
	v_exp_f32_e32 v95, v95
	v_pk_mul_f32 v[96:97], v[84:85], v[16:17] op_sel_hi:[0,1]
	v_pk_mul_f32 v[94:95], v[30:31], v[94:95]
	v_exp_f32_e32 v96, v96
	v_pk_fma_f32 v[30:31], v[124:125], s[44:45], v[94:95] op_sel_hi:[0,1,1]
	v_exp_f32_e32 v97, v97
	s_nop 0
	v_pk_mul_f32 v[96:97], v[32:33], v[96:97]
	s_nop 0
	v_pk_fma_f32 v[32:33], v[124:125], s[46:47], v[96:97] op_sel_hi:[0,1,1]
	v_mul_f32_e32 v124, v85, v125
	s_waitcnt lgkmcnt(0)
	s_load_dwordx16 s[32:47], s[70:71], 0x200
	v_fma_f32 v98, v50, s64, v122
	v_mul_f32_e64 v99, -|v98|, s65
	v_cvt_f32_f16_e32 v125, v68
	v_exp_f32_e32 v99, v99
	v_max_f32_e32 v98, 0, v98
	v_add_f32_e32 v99, 1.0, v99
	v_log_f32_e32 v99, v99
	v_pk_mul_f32 v[90:91], v[84:85], v[2:3] op_sel:[1,0]
	v_fma_f32 v86, v99, s66, v98
	v_add_f32_e32 v123, v123, v86
	v_exp_f32_e32 v90, v90
	v_exp_f32_e32 v91, v91
	v_pk_mul_f32 v[92:93], v[84:85], v[4:5] op_sel:[1,0]
	v_pk_mul_f32 v[90:91], v[18:19], v[90:91]
	v_exp_f32_e32 v92, v92
	v_pk_fma_f32 v[18:19], v[124:125], s[48:49], v[90:91] op_sel_hi:[0,1,1]
	v_exp_f32_e32 v93, v93
	v_pk_mul_f32 v[94:95], v[84:85], v[6:7] op_sel:[1,0]
	v_pk_mul_f32 v[92:93], v[20:21], v[92:93]
	v_exp_f32_e32 v94, v94
	v_pk_fma_f32 v[20:21], v[124:125], s[50:51], v[92:93] op_sel_hi:[0,1,1]
	v_exp_f32_e32 v95, v95
	v_pk_mul_f32 v[96:97], v[84:85], v[8:9] op_sel:[1,0]
	v_pk_mul_f32 v[94:95], v[22:23], v[94:95]
	v_exp_f32_e32 v96, v96
	v_pk_fma_f32 v[22:23], v[124:125], s[52:53], v[94:95] op_sel_hi:[0,1,1]
	v_exp_f32_e32 v97, v97
	v_pk_mul_f32 v[90:91], v[84:85], v[10:11] op_sel:[1,0]
	v_pk_mul_f32 v[96:97], v[24:25], v[96:97]
	v_exp_f32_e32 v90, v90
	v_pk_fma_f32 v[24:25], v[124:125], s[54:55], v[96:97] op_sel_hi:[0,1,1]
	v_exp_f32_e32 v91, v91
	v_pk_mul_f32 v[92:93], v[84:85], v[12:13] op_sel:[1,0]
	v_pk_mul_f32 v[90:91], v[26:27], v[90:91]
	v_exp_f32_e32 v92, v92
	v_pk_fma_f32 v[26:27], v[124:125], s[56:57], v[90:91] op_sel_hi:[0,1,1]
	v_exp_f32_e32 v93, v93
	v_pk_mul_f32 v[94:95], v[84:85], v[14:15] op_sel:[1,0]
	v_pk_mul_f32 v[92:93], v[28:29], v[92:93]
	v_exp_f32_e32 v94, v94
	v_pk_fma_f32 v[28:29], v[124:125], s[58:59], v[92:93] op_sel_hi:[0,1,1]
	v_exp_f32_e32 v95, v95
	v_pk_mul_f32 v[96:97], v[84:85], v[16:17] op_sel:[1,0]
	v_pk_mul_f32 v[94:95], v[30:31], v[94:95]
	v_exp_f32_e32 v96, v96
	v_pk_fma_f32 v[30:31], v[124:125], s[60:61], v[94:95] op_sel_hi:[0,1,1]
	v_exp_f32_e32 v97, v97
	s_nop 0
	v_pk_mul_f32 v[96:97], v[32:33], v[96:97]
	s_nop 0
	v_pk_fma_f32 v[32:33], v[124:125], s[62:63], v[96:97] op_sel_hi:[0,1,1]
	v_mul_f32_e32 v124, v86, v125
	global_store_dwordx4 v126, v[82:85], s[72:73]
	s_add_u32 s72, s72, 0x8000
	s_addc_u32 s73, s73, 0
	s_waitcnt lgkmcnt(0)
	s_load_dwordx16 s[48:63], s[70:71], 0x280
	v_fma_f32 v98, v51, s64, v122
	v_mul_f32_e64 v99, -|v98|, s65
	v_cvt_f32_f16_sdwa v125, v68 dst_sel:DWORD dst_unused:UNUSED_PAD src0_sel:WORD_1
	v_exp_f32_e32 v99, v99
	v_max_f32_e32 v98, 0, v98
	v_add_f32_e32 v99, 1.0, v99
	v_log_f32_e32 v99, v99
	v_pk_mul_f32 v[90:91], v[86:87], v[2:3] op_sel_hi:[0,1]
	v_fma_f32 v87, v99, s66, v98
	v_add_f32_e32 v123, v123, v87
	v_exp_f32_e32 v90, v90
	v_exp_f32_e32 v91, v91
	v_pk_mul_f32 v[92:93], v[86:87], v[4:5] op_sel_hi:[0,1]
	v_pk_mul_f32 v[90:91], v[18:19], v[90:91]
	v_exp_f32_e32 v92, v92
	v_pk_fma_f32 v[18:19], v[124:125], s[32:33], v[90:91] op_sel_hi:[0,1,1]
	v_exp_f32_e32 v93, v93
	v_pk_mul_f32 v[94:95], v[86:87], v[6:7] op_sel_hi:[0,1]
	v_pk_mul_f32 v[92:93], v[20:21], v[92:93]
	v_exp_f32_e32 v94, v94
	v_pk_fma_f32 v[20:21], v[124:125], s[34:35], v[92:93] op_sel_hi:[0,1,1]
	v_exp_f32_e32 v95, v95
	v_pk_mul_f32 v[96:97], v[86:87], v[8:9] op_sel_hi:[0,1]
	v_pk_mul_f32 v[94:95], v[22:23], v[94:95]
	v_exp_f32_e32 v96, v96
	v_pk_fma_f32 v[22:23], v[124:125], s[36:37], v[94:95] op_sel_hi:[0,1,1]
	v_exp_f32_e32 v97, v97
	v_pk_mul_f32 v[90:91], v[86:87], v[10:11] op_sel_hi:[0,1]
	v_pk_mul_f32 v[96:97], v[24:25], v[96:97]
	v_exp_f32_e32 v90, v90
	v_pk_fma_f32 v[24:25], v[124:125], s[38:39], v[96:97] op_sel_hi:[0,1,1]
	v_exp_f32_e32 v91, v91
	v_pk_mul_f32 v[92:93], v[86:87], v[12:13] op_sel_hi:[0,1]
	v_pk_mul_f32 v[90:91], v[26:27], v[90:91]
	v_exp_f32_e32 v92, v92
	v_pk_fma_f32 v[26:27], v[124:125], s[40:41], v[90:91] op_sel_hi:[0,1,1]
	v_exp_f32_e32 v93, v93
	v_pk_mul_f32 v[94:95], v[86:87], v[14:15] op_sel_hi:[0,1]
	v_pk_mul_f32 v[92:93], v[28:29], v[92:93]
	v_exp_f32_e32 v94, v94
	v_pk_fma_f32 v[28:29], v[124:125], s[42:43], v[92:93] op_sel_hi:[0,1,1]
	v_exp_f32_e32 v95, v95
	v_pk_mul_f32 v[96:97], v[86:87], v[16:17] op_sel_hi:[0,1]
	v_pk_mul_f32 v[94:95], v[30:31], v[94:95]
	v_exp_f32_e32 v96, v96
	v_pk_fma_f32 v[30:31], v[124:125], s[44:45], v[94:95] op_sel_hi:[0,1,1]
	v_exp_f32_e32 v97, v97
	s_nop 0
	v_pk_mul_f32 v[96:97], v[32:33], v[96:97]
	s_nop 0
	v_pk_fma_f32 v[32:33], v[124:125], s[46:47], v[96:97] op_sel_hi:[0,1,1]
	v_mul_f32_e32 v124, v87, v125
	s_waitcnt lgkmcnt(0)
	s_load_dwordx16 s[32:47], s[70:71], 0x300
	v_fma_f32 v98, v52, s64, v122
	v_mul_f32_e64 v99, -|v98|, s65
	v_cvt_f32_f16_e32 v125, v69
	v_exp_f32_e32 v99, v99
	v_max_f32_e32 v98, 0, v98
	v_add_f32_e32 v99, 1.0, v99
	v_log_f32_e32 v99, v99
	v_pk_mul_f32 v[90:91], v[86:87], v[2:3] op_sel:[1,0]
	v_fma_f32 v88, v99, s66, v98
	v_add_f32_e32 v123, v123, v88
	v_exp_f32_e32 v90, v90
	v_exp_f32_e32 v91, v91
	v_pk_mul_f32 v[92:93], v[86:87], v[4:5] op_sel:[1,0]
	v_pk_mul_f32 v[90:91], v[18:19], v[90:91]
	v_exp_f32_e32 v92, v92
	v_pk_fma_f32 v[18:19], v[124:125], s[48:49], v[90:91] op_sel_hi:[0,1,1]
	v_exp_f32_e32 v93, v93
	v_pk_mul_f32 v[94:95], v[86:87], v[6:7] op_sel:[1,0]
	v_pk_mul_f32 v[92:93], v[20:21], v[92:93]
	v_exp_f32_e32 v94, v94
	v_pk_fma_f32 v[20:21], v[124:125], s[50:51], v[92:93] op_sel_hi:[0,1,1]
	v_exp_f32_e32 v95, v95
	v_pk_mul_f32 v[96:97], v[86:87], v[8:9] op_sel:[1,0]
	v_pk_mul_f32 v[94:95], v[22:23], v[94:95]
	v_exp_f32_e32 v96, v96
	v_pk_fma_f32 v[22:23], v[124:125], s[52:53], v[94:95] op_sel_hi:[0,1,1]
	v_exp_f32_e32 v97, v97
	v_pk_mul_f32 v[90:91], v[86:87], v[10:11] op_sel:[1,0]
	v_pk_mul_f32 v[96:97], v[24:25], v[96:97]
	v_exp_f32_e32 v90, v90
	v_pk_fma_f32 v[24:25], v[124:125], s[54:55], v[96:97] op_sel_hi:[0,1,1]
	v_exp_f32_e32 v91, v91
	v_pk_mul_f32 v[92:93], v[86:87], v[12:13] op_sel:[1,0]
	v_pk_mul_f32 v[90:91], v[26:27], v[90:91]
	v_exp_f32_e32 v92, v92
	v_pk_fma_f32 v[26:27], v[124:125], s[56:57], v[90:91] op_sel_hi:[0,1,1]
	v_exp_f32_e32 v93, v93
	v_pk_mul_f32 v[94:95], v[86:87], v[14:15] op_sel:[1,0]
	v_pk_mul_f32 v[92:93], v[28:29], v[92:93]
	v_exp_f32_e32 v94, v94
	v_pk_fma_f32 v[28:29], v[124:125], s[58:59], v[92:93] op_sel_hi:[0,1,1]
	v_exp_f32_e32 v95, v95
	v_pk_mul_f32 v[96:97], v[86:87], v[16:17] op_sel:[1,0]
	v_pk_mul_f32 v[94:95], v[30:31], v[94:95]
	v_exp_f32_e32 v96, v96
	v_pk_fma_f32 v[30:31], v[124:125], s[60:61], v[94:95] op_sel_hi:[0,1,1]
	v_exp_f32_e32 v97, v97
	s_nop 0
	v_pk_mul_f32 v[96:97], v[32:33], v[96:97]
	s_nop 0
	v_pk_fma_f32 v[32:33], v[124:125], s[62:63], v[96:97] op_sel_hi:[0,1,1]
	v_mul_f32_e32 v124, v88, v125
	s_waitcnt lgkmcnt(0)
	s_load_dwordx16 s[48:63], s[70:71], 0x380
	v_fma_f32 v98, v53, s64, v122
	v_mul_f32_e64 v99, -|v98|, s65
	v_cvt_f32_f16_sdwa v125, v69 dst_sel:DWORD dst_unused:UNUSED_PAD src0_sel:WORD_1
	v_exp_f32_e32 v99, v99
	v_max_f32_e32 v98, 0, v98
	v_add_f32_e32 v99, 1.0, v99
	v_log_f32_e32 v99, v99
	v_pk_mul_f32 v[90:91], v[88:89], v[2:3] op_sel_hi:[0,1]
	v_fma_f32 v89, v99, s66, v98
	v_add_f32_e32 v123, v123, v89
	v_exp_f32_e32 v90, v90
	v_exp_f32_e32 v91, v91
	v_pk_mul_f32 v[92:93], v[88:89], v[4:5] op_sel_hi:[0,1]
	v_pk_mul_f32 v[90:91], v[18:19], v[90:91]
	v_exp_f32_e32 v92, v92
	v_pk_fma_f32 v[18:19], v[124:125], s[32:33], v[90:91] op_sel_hi:[0,1,1]
	v_exp_f32_e32 v93, v93
	v_pk_mul_f32 v[94:95], v[88:89], v[6:7] op_sel_hi:[0,1]
	v_pk_mul_f32 v[92:93], v[20:21], v[92:93]
	v_exp_f32_e32 v94, v94
	v_pk_fma_f32 v[20:21], v[124:125], s[34:35], v[92:93] op_sel_hi:[0,1,1]
	v_exp_f32_e32 v95, v95
	v_pk_mul_f32 v[96:97], v[88:89], v[8:9] op_sel_hi:[0,1]
	v_pk_mul_f32 v[94:95], v[22:23], v[94:95]
	v_exp_f32_e32 v96, v96
	v_pk_fma_f32 v[22:23], v[124:125], s[36:37], v[94:95] op_sel_hi:[0,1,1]
	v_exp_f32_e32 v97, v97
	v_pk_mul_f32 v[90:91], v[88:89], v[10:11] op_sel_hi:[0,1]
	v_pk_mul_f32 v[96:97], v[24:25], v[96:97]
	v_exp_f32_e32 v90, v90
	v_pk_fma_f32 v[24:25], v[124:125], s[38:39], v[96:97] op_sel_hi:[0,1,1]
	v_exp_f32_e32 v91, v91
	v_pk_mul_f32 v[92:93], v[88:89], v[12:13] op_sel_hi:[0,1]
	v_pk_mul_f32 v[90:91], v[26:27], v[90:91]
	v_exp_f32_e32 v92, v92
	v_pk_fma_f32 v[26:27], v[124:125], s[40:41], v[90:91] op_sel_hi:[0,1,1]
	v_exp_f32_e32 v93, v93
	v_pk_mul_f32 v[94:95], v[88:89], v[14:15] op_sel_hi:[0,1]
	v_pk_mul_f32 v[92:93], v[28:29], v[92:93]
	v_exp_f32_e32 v94, v94
	v_pk_fma_f32 v[28:29], v[124:125], s[42:43], v[92:93] op_sel_hi:[0,1,1]
	v_exp_f32_e32 v95, v95
	v_pk_mul_f32 v[96:97], v[88:89], v[16:17] op_sel_hi:[0,1]
	v_pk_mul_f32 v[94:95], v[30:31], v[94:95]
	v_exp_f32_e32 v96, v96
	v_pk_fma_f32 v[30:31], v[124:125], s[44:45], v[94:95] op_sel_hi:[0,1,1]
	v_exp_f32_e32 v97, v97
	s_nop 0
	v_pk_mul_f32 v[96:97], v[32:33], v[96:97]
	s_nop 0
	v_pk_fma_f32 v[32:33], v[124:125], s[46:47], v[96:97] op_sel_hi:[0,1,1]
	v_mul_f32_e32 v124, v89, v125
	s_waitcnt vmcnt(5)
	s_waitcnt lgkmcnt(0)
	s_load_dwordx16 s[32:47], s[70:71], 0x400
	v_fma_f32 v98, v38, s64, v122
	v_mul_f32_e64 v99, -|v98|, s65
	v_cvt_f32_f16_e32 v125, v70
	v_exp_f32_e32 v99, v99
	v_max_f32_e32 v98, 0, v98
	v_add_f32_e32 v99, 1.0, v99
	v_log_f32_e32 v99, v99
	v_pk_mul_f32 v[90:91], v[88:89], v[2:3] op_sel:[1,0]
	v_fma_f32 v82, v99, s66, v98
	v_add_f32_e32 v123, v123, v82
	v_exp_f32_e32 v90, v90
	v_exp_f32_e32 v91, v91
	v_pk_mul_f32 v[92:93], v[88:89], v[4:5] op_sel:[1,0]
	v_pk_mul_f32 v[90:91], v[18:19], v[90:91]
	v_exp_f32_e32 v92, v92
	v_pk_fma_f32 v[18:19], v[124:125], s[48:49], v[90:91] op_sel_hi:[0,1,1]
	v_exp_f32_e32 v93, v93
	v_pk_mul_f32 v[94:95], v[88:89], v[6:7] op_sel:[1,0]
	v_pk_mul_f32 v[92:93], v[20:21], v[92:93]
	v_exp_f32_e32 v94, v94
	v_pk_fma_f32 v[20:21], v[124:125], s[50:51], v[92:93] op_sel_hi:[0,1,1]
	v_exp_f32_e32 v95, v95
	v_pk_mul_f32 v[96:97], v[88:89], v[8:9] op_sel:[1,0]
	v_pk_mul_f32 v[94:95], v[22:23], v[94:95]
	v_exp_f32_e32 v96, v96
	v_pk_fma_f32 v[22:23], v[124:125], s[52:53], v[94:95] op_sel_hi:[0,1,1]
	v_exp_f32_e32 v97, v97
	v_pk_mul_f32 v[90:91], v[88:89], v[10:11] op_sel:[1,0]
	v_pk_mul_f32 v[96:97], v[24:25], v[96:97]
	v_exp_f32_e32 v90, v90
	v_pk_fma_f32 v[24:25], v[124:125], s[54:55], v[96:97] op_sel_hi:[0,1,1]
	v_exp_f32_e32 v91, v91
	v_pk_mul_f32 v[92:93], v[88:89], v[12:13] op_sel:[1,0]
	v_pk_mul_f32 v[90:91], v[26:27], v[90:91]
	v_exp_f32_e32 v92, v92
	v_pk_fma_f32 v[26:27], v[124:125], s[56:57], v[90:91] op_sel_hi:[0,1,1]
	v_exp_f32_e32 v93, v93
	v_pk_mul_f32 v[94:95], v[88:89], v[14:15] op_sel:[1,0]
	v_pk_mul_f32 v[92:93], v[28:29], v[92:93]
	v_exp_f32_e32 v94, v94
	v_pk_fma_f32 v[28:29], v[124:125], s[58:59], v[92:93] op_sel_hi:[0,1,1]
	v_exp_f32_e32 v95, v95
	v_pk_mul_f32 v[96:97], v[88:89], v[16:17] op_sel:[1,0]
	v_pk_mul_f32 v[94:95], v[30:31], v[94:95]
	v_exp_f32_e32 v96, v96
	v_pk_fma_f32 v[30:31], v[124:125], s[60:61], v[94:95] op_sel_hi:[0,1,1]
	v_exp_f32_e32 v97, v97
	s_nop 0
	v_pk_mul_f32 v[96:97], v[32:33], v[96:97]
	s_nop 0
	v_pk_fma_f32 v[32:33], v[124:125], s[62:63], v[96:97] op_sel_hi:[0,1,1]
	v_mul_f32_e32 v124, v82, v125
	global_store_dwordx4 v126, v[86:89], s[72:73]
	s_add_u32 s72, s72, 0x8000
	s_addc_u32 s73, s73, 0
	s_waitcnt lgkmcnt(0)
	s_load_dwordx16 s[48:63], s[70:71], 0x480
	v_fma_f32 v98, v39, s64, v122
	v_mul_f32_e64 v99, -|v98|, s65
	v_cvt_f32_f16_sdwa v125, v70 dst_sel:DWORD dst_unused:UNUSED_PAD src0_sel:WORD_1
	v_exp_f32_e32 v99, v99
	v_max_f32_e32 v98, 0, v98
	v_add_f32_e32 v99, 1.0, v99
	v_log_f32_e32 v99, v99
	v_pk_mul_f32 v[90:91], v[82:83], v[2:3] op_sel_hi:[0,1]
	v_fma_f32 v83, v99, s66, v98
	v_add_f32_e32 v123, v123, v83
	v_exp_f32_e32 v90, v90
	v_exp_f32_e32 v91, v91
	v_pk_mul_f32 v[92:93], v[82:83], v[4:5] op_sel_hi:[0,1]
	v_pk_mul_f32 v[90:91], v[18:19], v[90:91]
	v_exp_f32_e32 v92, v92
	v_pk_fma_f32 v[18:19], v[124:125], s[32:33], v[90:91] op_sel_hi:[0,1,1]
	v_exp_f32_e32 v93, v93
	v_pk_mul_f32 v[94:95], v[82:83], v[6:7] op_sel_hi:[0,1]
	v_pk_mul_f32 v[92:93], v[20:21], v[92:93]
	v_exp_f32_e32 v94, v94
	v_pk_fma_f32 v[20:21], v[124:125], s[34:35], v[92:93] op_sel_hi:[0,1,1]
	v_exp_f32_e32 v95, v95
	v_pk_mul_f32 v[96:97], v[82:83], v[8:9] op_sel_hi:[0,1]
	v_pk_mul_f32 v[94:95], v[22:23], v[94:95]
	v_exp_f32_e32 v96, v96
	v_pk_fma_f32 v[22:23], v[124:125], s[36:37], v[94:95] op_sel_hi:[0,1,1]
	v_exp_f32_e32 v97, v97
	v_pk_mul_f32 v[90:91], v[82:83], v[10:11] op_sel_hi:[0,1]
	v_pk_mul_f32 v[96:97], v[24:25], v[96:97]
	v_exp_f32_e32 v90, v90
	v_pk_fma_f32 v[24:25], v[124:125], s[38:39], v[96:97] op_sel_hi:[0,1,1]
	v_exp_f32_e32 v91, v91
	v_pk_mul_f32 v[92:93], v[82:83], v[12:13] op_sel_hi:[0,1]
	v_pk_mul_f32 v[90:91], v[26:27], v[90:91]
	v_exp_f32_e32 v92, v92
	v_pk_fma_f32 v[26:27], v[124:125], s[40:41], v[90:91] op_sel_hi:[0,1,1]
	v_exp_f32_e32 v93, v93
	v_pk_mul_f32 v[94:95], v[82:83], v[14:15] op_sel_hi:[0,1]
	v_pk_mul_f32 v[92:93], v[28:29], v[92:93]
	v_exp_f32_e32 v94, v94
	v_pk_fma_f32 v[28:29], v[124:125], s[42:43], v[92:93] op_sel_hi:[0,1,1]
	v_exp_f32_e32 v95, v95
	v_pk_mul_f32 v[96:97], v[82:83], v[16:17] op_sel_hi:[0,1]
	v_pk_mul_f32 v[94:95], v[30:31], v[94:95]
	v_exp_f32_e32 v96, v96
	v_pk_fma_f32 v[30:31], v[124:125], s[44:45], v[94:95] op_sel_hi:[0,1,1]
	v_exp_f32_e32 v97, v97
	s_nop 0
	v_pk_mul_f32 v[96:97], v[32:33], v[96:97]
	s_nop 0
	v_pk_fma_f32 v[32:33], v[124:125], s[46:47], v[96:97] op_sel_hi:[0,1,1]
	v_mul_f32_e32 v124, v83, v125
	s_waitcnt lgkmcnt(0)
	s_load_dwordx16 s[32:47], s[70:71], 0x500
	v_fma_f32 v98, v40, s64, v122
	v_mul_f32_e64 v99, -|v98|, s65
	v_cvt_f32_f16_e32 v125, v71
	v_exp_f32_e32 v99, v99
	v_max_f32_e32 v98, 0, v98
	v_add_f32_e32 v99, 1.0, v99
	v_log_f32_e32 v99, v99
	v_pk_mul_f32 v[90:91], v[82:83], v[2:3] op_sel:[1,0]
	v_fma_f32 v84, v99, s66, v98
	v_add_f32_e32 v123, v123, v84
	v_exp_f32_e32 v90, v90
	v_exp_f32_e32 v91, v91
	v_pk_mul_f32 v[92:93], v[82:83], v[4:5] op_sel:[1,0]
	v_pk_mul_f32 v[90:91], v[18:19], v[90:91]
	v_exp_f32_e32 v92, v92
	v_pk_fma_f32 v[18:19], v[124:125], s[48:49], v[90:91] op_sel_hi:[0,1,1]
	v_exp_f32_e32 v93, v93
	v_pk_mul_f32 v[94:95], v[82:83], v[6:7] op_sel:[1,0]
	v_pk_mul_f32 v[92:93], v[20:21], v[92:93]
	v_exp_f32_e32 v94, v94
	v_pk_fma_f32 v[20:21], v[124:125], s[50:51], v[92:93] op_sel_hi:[0,1,1]
	v_exp_f32_e32 v95, v95
	v_pk_mul_f32 v[96:97], v[82:83], v[8:9] op_sel:[1,0]
	v_pk_mul_f32 v[94:95], v[22:23], v[94:95]
	v_exp_f32_e32 v96, v96
	v_pk_fma_f32 v[22:23], v[124:125], s[52:53], v[94:95] op_sel_hi:[0,1,1]
	v_exp_f32_e32 v97, v97
	v_pk_mul_f32 v[90:91], v[82:83], v[10:11] op_sel:[1,0]
	v_pk_mul_f32 v[96:97], v[24:25], v[96:97]
	v_exp_f32_e32 v90, v90
	v_pk_fma_f32 v[24:25], v[124:125], s[54:55], v[96:97] op_sel_hi:[0,1,1]
	v_exp_f32_e32 v91, v91
	v_pk_mul_f32 v[92:93], v[82:83], v[12:13] op_sel:[1,0]
	v_pk_mul_f32 v[90:91], v[26:27], v[90:91]
	v_exp_f32_e32 v92, v92
	v_pk_fma_f32 v[26:27], v[124:125], s[56:57], v[90:91] op_sel_hi:[0,1,1]
	v_exp_f32_e32 v93, v93
	v_pk_mul_f32 v[94:95], v[82:83], v[14:15] op_sel:[1,0]
	v_pk_mul_f32 v[92:93], v[28:29], v[92:93]
	v_exp_f32_e32 v94, v94
	v_pk_fma_f32 v[28:29], v[124:125], s[58:59], v[92:93] op_sel_hi:[0,1,1]
	v_exp_f32_e32 v95, v95
	v_pk_mul_f32 v[96:97], v[82:83], v[16:17] op_sel:[1,0]
	v_pk_mul_f32 v[94:95], v[30:31], v[94:95]
	v_exp_f32_e32 v96, v96
	v_pk_fma_f32 v[30:31], v[124:125], s[60:61], v[94:95] op_sel_hi:[0,1,1]
	v_exp_f32_e32 v97, v97
	s_nop 0
	v_pk_mul_f32 v[96:97], v[32:33], v[96:97]
	s_nop 0
	v_pk_fma_f32 v[32:33], v[124:125], s[62:63], v[96:97] op_sel_hi:[0,1,1]
	v_mul_f32_e32 v124, v84, v125
	s_waitcnt lgkmcnt(0)
	s_load_dwordx16 s[48:63], s[70:71], 0x580
	v_fma_f32 v98, v41, s64, v122
	v_mul_f32_e64 v99, -|v98|, s65
	v_cvt_f32_f16_sdwa v125, v71 dst_sel:DWORD dst_unused:UNUSED_PAD src0_sel:WORD_1
	v_exp_f32_e32 v99, v99
	v_max_f32_e32 v98, 0, v98
	v_add_f32_e32 v99, 1.0, v99
	v_log_f32_e32 v99, v99
	v_pk_mul_f32 v[90:91], v[84:85], v[2:3] op_sel_hi:[0,1]
	v_fma_f32 v85, v99, s66, v98
	v_add_f32_e32 v123, v123, v85
	v_exp_f32_e32 v90, v90
	v_exp_f32_e32 v91, v91
	v_pk_mul_f32 v[92:93], v[84:85], v[4:5] op_sel_hi:[0,1]
	v_pk_mul_f32 v[90:91], v[18:19], v[90:91]
	v_exp_f32_e32 v92, v92
	v_pk_fma_f32 v[18:19], v[124:125], s[32:33], v[90:91] op_sel_hi:[0,1,1]
	v_exp_f32_e32 v93, v93
	v_pk_mul_f32 v[94:95], v[84:85], v[6:7] op_sel_hi:[0,1]
	v_pk_mul_f32 v[92:93], v[20:21], v[92:93]
	v_exp_f32_e32 v94, v94
	v_pk_fma_f32 v[20:21], v[124:125], s[34:35], v[92:93] op_sel_hi:[0,1,1]
	v_exp_f32_e32 v95, v95
	v_pk_mul_f32 v[96:97], v[84:85], v[8:9] op_sel_hi:[0,1]
	v_pk_mul_f32 v[94:95], v[22:23], v[94:95]
	v_exp_f32_e32 v96, v96
	v_pk_fma_f32 v[22:23], v[124:125], s[36:37], v[94:95] op_sel_hi:[0,1,1]
	v_exp_f32_e32 v97, v97
	v_pk_mul_f32 v[90:91], v[84:85], v[10:11] op_sel_hi:[0,1]
	v_pk_mul_f32 v[96:97], v[24:25], v[96:97]
	v_exp_f32_e32 v90, v90
	v_pk_fma_f32 v[24:25], v[124:125], s[38:39], v[96:97] op_sel_hi:[0,1,1]
	v_exp_f32_e32 v91, v91
	v_pk_mul_f32 v[92:93], v[84:85], v[12:13] op_sel_hi:[0,1]
	v_pk_mul_f32 v[90:91], v[26:27], v[90:91]
	v_exp_f32_e32 v92, v92
	v_pk_fma_f32 v[26:27], v[124:125], s[40:41], v[90:91] op_sel_hi:[0,1,1]
	v_exp_f32_e32 v93, v93
	v_pk_mul_f32 v[94:95], v[84:85], v[14:15] op_sel_hi:[0,1]
	v_pk_mul_f32 v[92:93], v[28:29], v[92:93]
	v_exp_f32_e32 v94, v94
	v_pk_fma_f32 v[28:29], v[124:125], s[42:43], v[92:93] op_sel_hi:[0,1,1]
	v_exp_f32_e32 v95, v95
	v_pk_mul_f32 v[96:97], v[84:85], v[16:17] op_sel_hi:[0,1]
	v_pk_mul_f32 v[94:95], v[30:31], v[94:95]
	v_exp_f32_e32 v96, v96
	v_pk_fma_f32 v[30:31], v[124:125], s[44:45], v[94:95] op_sel_hi:[0,1,1]
	v_exp_f32_e32 v97, v97
	s_nop 0
	v_pk_mul_f32 v[96:97], v[32:33], v[96:97]
	s_nop 0
	v_pk_fma_f32 v[32:33], v[124:125], s[46:47], v[96:97] op_sel_hi:[0,1,1]
	v_mul_f32_e32 v124, v85, v125
	s_waitcnt lgkmcnt(0)
	s_load_dwordx16 s[32:47], s[70:71], 0x600
	v_fma_f32 v98, v54, s64, v122
	v_mul_f32_e64 v99, -|v98|, s65
	v_cvt_f32_f16_e32 v125, v72
	v_exp_f32_e32 v99, v99
	v_max_f32_e32 v98, 0, v98
	v_add_f32_e32 v99, 1.0, v99
	v_log_f32_e32 v99, v99
	v_pk_mul_f32 v[90:91], v[84:85], v[2:3] op_sel:[1,0]
	v_fma_f32 v86, v99, s66, v98
	v_add_f32_e32 v123, v123, v86
	v_exp_f32_e32 v90, v90
	v_exp_f32_e32 v91, v91
	v_pk_mul_f32 v[92:93], v[84:85], v[4:5] op_sel:[1,0]
	v_pk_mul_f32 v[90:91], v[18:19], v[90:91]
	v_exp_f32_e32 v92, v92
	v_pk_fma_f32 v[18:19], v[124:125], s[48:49], v[90:91] op_sel_hi:[0,1,1]
	v_exp_f32_e32 v93, v93
	v_pk_mul_f32 v[94:95], v[84:85], v[6:7] op_sel:[1,0]
	v_pk_mul_f32 v[92:93], v[20:21], v[92:93]
	v_exp_f32_e32 v94, v94
	v_pk_fma_f32 v[20:21], v[124:125], s[50:51], v[92:93] op_sel_hi:[0,1,1]
	v_exp_f32_e32 v95, v95
	v_pk_mul_f32 v[96:97], v[84:85], v[8:9] op_sel:[1,0]
	v_pk_mul_f32 v[94:95], v[22:23], v[94:95]
	v_exp_f32_e32 v96, v96
	v_pk_fma_f32 v[22:23], v[124:125], s[52:53], v[94:95] op_sel_hi:[0,1,1]
	v_exp_f32_e32 v97, v97
	v_pk_mul_f32 v[90:91], v[84:85], v[10:11] op_sel:[1,0]
	v_pk_mul_f32 v[96:97], v[24:25], v[96:97]
	v_exp_f32_e32 v90, v90
	v_pk_fma_f32 v[24:25], v[124:125], s[54:55], v[96:97] op_sel_hi:[0,1,1]
	v_exp_f32_e32 v91, v91
	v_pk_mul_f32 v[92:93], v[84:85], v[12:13] op_sel:[1,0]
	v_pk_mul_f32 v[90:91], v[26:27], v[90:91]
	v_exp_f32_e32 v92, v92
	v_pk_fma_f32 v[26:27], v[124:125], s[56:57], v[90:91] op_sel_hi:[0,1,1]
	v_exp_f32_e32 v93, v93
	v_pk_mul_f32 v[94:95], v[84:85], v[14:15] op_sel:[1,0]
	v_pk_mul_f32 v[92:93], v[28:29], v[92:93]
	v_exp_f32_e32 v94, v94
	v_pk_fma_f32 v[28:29], v[124:125], s[58:59], v[92:93] op_sel_hi:[0,1,1]
	v_exp_f32_e32 v95, v95
	v_pk_mul_f32 v[96:97], v[84:85], v[16:17] op_sel:[1,0]
	v_pk_mul_f32 v[94:95], v[30:31], v[94:95]
	v_exp_f32_e32 v96, v96
	v_pk_fma_f32 v[30:31], v[124:125], s[60:61], v[94:95] op_sel_hi:[0,1,1]
	v_exp_f32_e32 v97, v97
	s_nop 0
	v_pk_mul_f32 v[96:97], v[32:33], v[96:97]
	s_nop 0
	v_pk_fma_f32 v[32:33], v[124:125], s[62:63], v[96:97] op_sel_hi:[0,1,1]
	v_mul_f32_e32 v124, v86, v125
	global_store_dwordx4 v126, v[82:85], s[72:73]
	s_add_u32 s72, s72, 0x8000
	s_addc_u32 s73, s73, 0
	s_waitcnt lgkmcnt(0)
	s_load_dwordx16 s[48:63], s[70:71], 0x680
	v_fma_f32 v98, v55, s64, v122
	v_mul_f32_e64 v99, -|v98|, s65
	v_cvt_f32_f16_sdwa v125, v72 dst_sel:DWORD dst_unused:UNUSED_PAD src0_sel:WORD_1
	v_exp_f32_e32 v99, v99
	v_max_f32_e32 v98, 0, v98
	v_add_f32_e32 v99, 1.0, v99
	v_log_f32_e32 v99, v99
	v_pk_mul_f32 v[90:91], v[86:87], v[2:3] op_sel_hi:[0,1]
	v_fma_f32 v87, v99, s66, v98
	v_add_f32_e32 v123, v123, v87
	v_exp_f32_e32 v90, v90
	v_exp_f32_e32 v91, v91
	v_pk_mul_f32 v[92:93], v[86:87], v[4:5] op_sel_hi:[0,1]
	v_pk_mul_f32 v[90:91], v[18:19], v[90:91]
	v_exp_f32_e32 v92, v92
	v_pk_fma_f32 v[18:19], v[124:125], s[32:33], v[90:91] op_sel_hi:[0,1,1]
	v_exp_f32_e32 v93, v93
	v_pk_mul_f32 v[94:95], v[86:87], v[6:7] op_sel_hi:[0,1]
	v_pk_mul_f32 v[92:93], v[20:21], v[92:93]
	v_exp_f32_e32 v94, v94
	v_pk_fma_f32 v[20:21], v[124:125], s[34:35], v[92:93] op_sel_hi:[0,1,1]
	v_exp_f32_e32 v95, v95
	v_pk_mul_f32 v[96:97], v[86:87], v[8:9] op_sel_hi:[0,1]
	v_pk_mul_f32 v[94:95], v[22:23], v[94:95]
	v_exp_f32_e32 v96, v96
	v_pk_fma_f32 v[22:23], v[124:125], s[36:37], v[94:95] op_sel_hi:[0,1,1]
	v_exp_f32_e32 v97, v97
	v_pk_mul_f32 v[90:91], v[86:87], v[10:11] op_sel_hi:[0,1]
	v_pk_mul_f32 v[96:97], v[24:25], v[96:97]
	v_exp_f32_e32 v90, v90
	v_pk_fma_f32 v[24:25], v[124:125], s[38:39], v[96:97] op_sel_hi:[0,1,1]
	v_exp_f32_e32 v91, v91
	v_pk_mul_f32 v[92:93], v[86:87], v[12:13] op_sel_hi:[0,1]
	v_pk_mul_f32 v[90:91], v[26:27], v[90:91]
	v_exp_f32_e32 v92, v92
	v_pk_fma_f32 v[26:27], v[124:125], s[40:41], v[90:91] op_sel_hi:[0,1,1]
	v_exp_f32_e32 v93, v93
	v_pk_mul_f32 v[94:95], v[86:87], v[14:15] op_sel_hi:[0,1]
	v_pk_mul_f32 v[92:93], v[28:29], v[92:93]
	v_exp_f32_e32 v94, v94
	v_pk_fma_f32 v[28:29], v[124:125], s[42:43], v[92:93] op_sel_hi:[0,1,1]
	v_exp_f32_e32 v95, v95
	v_pk_mul_f32 v[96:97], v[86:87], v[16:17] op_sel_hi:[0,1]
	v_pk_mul_f32 v[94:95], v[30:31], v[94:95]
	v_exp_f32_e32 v96, v96
	v_pk_fma_f32 v[30:31], v[124:125], s[44:45], v[94:95] op_sel_hi:[0,1,1]
	v_exp_f32_e32 v97, v97
	s_nop 0
	v_pk_mul_f32 v[96:97], v[32:33], v[96:97]
	s_nop 0
	v_pk_fma_f32 v[32:33], v[124:125], s[46:47], v[96:97] op_sel_hi:[0,1,1]
	v_mul_f32_e32 v124, v87, v125
	s_waitcnt lgkmcnt(0)
	s_load_dwordx16 s[32:47], s[70:71], 0x700
	v_fma_f32 v98, v56, s64, v122
	v_mul_f32_e64 v99, -|v98|, s65
	v_cvt_f32_f16_e32 v125, v73
	v_exp_f32_e32 v99, v99
	v_max_f32_e32 v98, 0, v98
	v_add_f32_e32 v99, 1.0, v99
	v_log_f32_e32 v99, v99
	v_pk_mul_f32 v[90:91], v[86:87], v[2:3] op_sel:[1,0]
	v_fma_f32 v88, v99, s66, v98
	v_add_f32_e32 v123, v123, v88
	v_exp_f32_e32 v90, v90
	v_exp_f32_e32 v91, v91
	v_pk_mul_f32 v[92:93], v[86:87], v[4:5] op_sel:[1,0]
	v_pk_mul_f32 v[90:91], v[18:19], v[90:91]
	v_exp_f32_e32 v92, v92
	v_pk_fma_f32 v[18:19], v[124:125], s[48:49], v[90:91] op_sel_hi:[0,1,1]
	v_exp_f32_e32 v93, v93
	v_pk_mul_f32 v[94:95], v[86:87], v[6:7] op_sel:[1,0]
	v_pk_mul_f32 v[92:93], v[20:21], v[92:93]
	v_exp_f32_e32 v94, v94
	v_pk_fma_f32 v[20:21], v[124:125], s[50:51], v[92:93] op_sel_hi:[0,1,1]
	v_exp_f32_e32 v95, v95
	v_pk_mul_f32 v[96:97], v[86:87], v[8:9] op_sel:[1,0]
	v_pk_mul_f32 v[94:95], v[22:23], v[94:95]
	v_exp_f32_e32 v96, v96
	v_pk_fma_f32 v[22:23], v[124:125], s[52:53], v[94:95] op_sel_hi:[0,1,1]
	v_exp_f32_e32 v97, v97
	v_pk_mul_f32 v[90:91], v[86:87], v[10:11] op_sel:[1,0]
	v_pk_mul_f32 v[96:97], v[24:25], v[96:97]
	v_exp_f32_e32 v90, v90
	v_pk_fma_f32 v[24:25], v[124:125], s[54:55], v[96:97] op_sel_hi:[0,1,1]
	v_exp_f32_e32 v91, v91
	v_pk_mul_f32 v[92:93], v[86:87], v[12:13] op_sel:[1,0]
	v_pk_mul_f32 v[90:91], v[26:27], v[90:91]
	v_exp_f32_e32 v92, v92
	v_pk_fma_f32 v[26:27], v[124:125], s[56:57], v[90:91] op_sel_hi:[0,1,1]
	v_exp_f32_e32 v93, v93
	v_pk_mul_f32 v[94:95], v[86:87], v[14:15] op_sel:[1,0]
	v_pk_mul_f32 v[92:93], v[28:29], v[92:93]
	v_exp_f32_e32 v94, v94
	v_pk_fma_f32 v[28:29], v[124:125], s[58:59], v[92:93] op_sel_hi:[0,1,1]
	v_exp_f32_e32 v95, v95
	v_pk_mul_f32 v[96:97], v[86:87], v[16:17] op_sel:[1,0]
	v_pk_mul_f32 v[94:95], v[30:31], v[94:95]
	v_exp_f32_e32 v96, v96
	v_pk_fma_f32 v[30:31], v[124:125], s[60:61], v[94:95] op_sel_hi:[0,1,1]
	v_exp_f32_e32 v97, v97
	s_nop 0
	v_pk_mul_f32 v[96:97], v[32:33], v[96:97]
	s_nop 0
	v_pk_fma_f32 v[32:33], v[124:125], s[62:63], v[96:97] op_sel_hi:[0,1,1]
	v_mul_f32_e32 v124, v88, v125
	s_waitcnt lgkmcnt(0)
	s_load_dwordx16 s[48:63], s[70:71], 0x780
	v_fma_f32 v98, v57, s64, v122
	v_mul_f32_e64 v99, -|v98|, s65
	v_cvt_f32_f16_sdwa v125, v73 dst_sel:DWORD dst_unused:UNUSED_PAD src0_sel:WORD_1
	v_exp_f32_e32 v99, v99
	v_max_f32_e32 v98, 0, v98
	v_add_f32_e32 v99, 1.0, v99
	v_log_f32_e32 v99, v99
	v_pk_mul_f32 v[90:91], v[88:89], v[2:3] op_sel_hi:[0,1]
	v_fma_f32 v89, v99, s66, v98
	v_add_f32_e32 v123, v123, v89
	v_exp_f32_e32 v90, v90
	v_exp_f32_e32 v91, v91
	v_pk_mul_f32 v[92:93], v[88:89], v[4:5] op_sel_hi:[0,1]
	v_pk_mul_f32 v[90:91], v[18:19], v[90:91]
	v_exp_f32_e32 v92, v92
	v_pk_fma_f32 v[18:19], v[124:125], s[32:33], v[90:91] op_sel_hi:[0,1,1]
	v_exp_f32_e32 v93, v93
	v_pk_mul_f32 v[94:95], v[88:89], v[6:7] op_sel_hi:[0,1]
	v_pk_mul_f32 v[92:93], v[20:21], v[92:93]
	v_exp_f32_e32 v94, v94
	v_pk_fma_f32 v[20:21], v[124:125], s[34:35], v[92:93] op_sel_hi:[0,1,1]
	v_exp_f32_e32 v95, v95
	v_pk_mul_f32 v[96:97], v[88:89], v[8:9] op_sel_hi:[0,1]
	v_pk_mul_f32 v[94:95], v[22:23], v[94:95]
	v_exp_f32_e32 v96, v96
	v_pk_fma_f32 v[22:23], v[124:125], s[36:37], v[94:95] op_sel_hi:[0,1,1]
	v_exp_f32_e32 v97, v97
	v_pk_mul_f32 v[90:91], v[88:89], v[10:11] op_sel_hi:[0,1]
	v_pk_mul_f32 v[96:97], v[24:25], v[96:97]
	v_exp_f32_e32 v90, v90
	v_pk_fma_f32 v[24:25], v[124:125], s[38:39], v[96:97] op_sel_hi:[0,1,1]
	v_exp_f32_e32 v91, v91
	v_pk_mul_f32 v[92:93], v[88:89], v[12:13] op_sel_hi:[0,1]
	v_pk_mul_f32 v[90:91], v[26:27], v[90:91]
	v_exp_f32_e32 v92, v92
	v_pk_fma_f32 v[26:27], v[124:125], s[40:41], v[90:91] op_sel_hi:[0,1,1]
	v_exp_f32_e32 v93, v93
	v_pk_mul_f32 v[94:95], v[88:89], v[14:15] op_sel_hi:[0,1]
	v_pk_mul_f32 v[92:93], v[28:29], v[92:93]
	v_exp_f32_e32 v94, v94
	v_pk_fma_f32 v[28:29], v[124:125], s[42:43], v[92:93] op_sel_hi:[0,1,1]
	v_exp_f32_e32 v95, v95
	v_pk_mul_f32 v[96:97], v[88:89], v[16:17] op_sel_hi:[0,1]
	v_pk_mul_f32 v[94:95], v[30:31], v[94:95]
	v_exp_f32_e32 v96, v96
	v_pk_fma_f32 v[30:31], v[124:125], s[44:45], v[94:95] op_sel_hi:[0,1,1]
	v_exp_f32_e32 v97, v97
	s_nop 0
	v_pk_mul_f32 v[96:97], v[32:33], v[96:97]
	s_nop 0
	v_pk_fma_f32 v[32:33], v[124:125], s[46:47], v[96:97] op_sel_hi:[0,1,1]
	v_mul_f32_e32 v124, v89, v125
	s_waitcnt vmcnt(6)
	s_waitcnt lgkmcnt(0)
	s_load_dwordx16 s[32:47], s[70:71], 0x800
	v_fma_f32 v98, v42, s64, v122
	v_mul_f32_e64 v99, -|v98|, s65
	v_cvt_f32_f16_e32 v125, v74
	v_exp_f32_e32 v99, v99
	v_max_f32_e32 v98, 0, v98
	v_add_f32_e32 v99, 1.0, v99
	v_log_f32_e32 v99, v99
	v_pk_mul_f32 v[90:91], v[88:89], v[2:3] op_sel:[1,0]
	v_fma_f32 v82, v99, s66, v98
	v_add_f32_e32 v123, v123, v82
	v_exp_f32_e32 v90, v90
	v_exp_f32_e32 v91, v91
	v_pk_mul_f32 v[92:93], v[88:89], v[4:5] op_sel:[1,0]
	v_pk_mul_f32 v[90:91], v[18:19], v[90:91]
	v_exp_f32_e32 v92, v92
	v_pk_fma_f32 v[18:19], v[124:125], s[48:49], v[90:91] op_sel_hi:[0,1,1]
	v_exp_f32_e32 v93, v93
	v_pk_mul_f32 v[94:95], v[88:89], v[6:7] op_sel:[1,0]
	v_pk_mul_f32 v[92:93], v[20:21], v[92:93]
	v_exp_f32_e32 v94, v94
	v_pk_fma_f32 v[20:21], v[124:125], s[50:51], v[92:93] op_sel_hi:[0,1,1]
	v_exp_f32_e32 v95, v95
	v_pk_mul_f32 v[96:97], v[88:89], v[8:9] op_sel:[1,0]
	v_pk_mul_f32 v[94:95], v[22:23], v[94:95]
	v_exp_f32_e32 v96, v96
	v_pk_fma_f32 v[22:23], v[124:125], s[52:53], v[94:95] op_sel_hi:[0,1,1]
	v_exp_f32_e32 v97, v97
	v_pk_mul_f32 v[90:91], v[88:89], v[10:11] op_sel:[1,0]
	v_pk_mul_f32 v[96:97], v[24:25], v[96:97]
	v_exp_f32_e32 v90, v90
	v_pk_fma_f32 v[24:25], v[124:125], s[54:55], v[96:97] op_sel_hi:[0,1,1]
	v_exp_f32_e32 v91, v91
	v_pk_mul_f32 v[92:93], v[88:89], v[12:13] op_sel:[1,0]
	v_pk_mul_f32 v[90:91], v[26:27], v[90:91]
	v_exp_f32_e32 v92, v92
	v_pk_fma_f32 v[26:27], v[124:125], s[56:57], v[90:91] op_sel_hi:[0,1,1]
	v_exp_f32_e32 v93, v93
	v_pk_mul_f32 v[94:95], v[88:89], v[14:15] op_sel:[1,0]
	v_pk_mul_f32 v[92:93], v[28:29], v[92:93]
	v_exp_f32_e32 v94, v94
	v_pk_fma_f32 v[28:29], v[124:125], s[58:59], v[92:93] op_sel_hi:[0,1,1]
	v_exp_f32_e32 v95, v95
	v_pk_mul_f32 v[96:97], v[88:89], v[16:17] op_sel:[1,0]
	v_pk_mul_f32 v[94:95], v[30:31], v[94:95]
	v_exp_f32_e32 v96, v96
	v_pk_fma_f32 v[30:31], v[124:125], s[60:61], v[94:95] op_sel_hi:[0,1,1]
	v_exp_f32_e32 v97, v97
	s_nop 0
	v_pk_mul_f32 v[96:97], v[32:33], v[96:97]
	s_nop 0
	v_pk_fma_f32 v[32:33], v[124:125], s[62:63], v[96:97] op_sel_hi:[0,1,1]
	v_mul_f32_e32 v124, v82, v125
	global_store_dwordx4 v126, v[86:89], s[72:73]
	s_add_u32 s72, s72, 0x8000
	s_addc_u32 s73, s73, 0
	s_waitcnt lgkmcnt(0)
	s_load_dwordx16 s[48:63], s[70:71], 0x880
	v_fma_f32 v98, v43, s64, v122
	v_mul_f32_e64 v99, -|v98|, s65
	v_cvt_f32_f16_sdwa v125, v74 dst_sel:DWORD dst_unused:UNUSED_PAD src0_sel:WORD_1
	v_exp_f32_e32 v99, v99
	v_max_f32_e32 v98, 0, v98
	v_add_f32_e32 v99, 1.0, v99
	v_log_f32_e32 v99, v99
	v_pk_mul_f32 v[90:91], v[82:83], v[2:3] op_sel_hi:[0,1]
	v_fma_f32 v83, v99, s66, v98
	v_add_f32_e32 v123, v123, v83
	v_exp_f32_e32 v90, v90
	v_exp_f32_e32 v91, v91
	v_pk_mul_f32 v[92:93], v[82:83], v[4:5] op_sel_hi:[0,1]
	v_pk_mul_f32 v[90:91], v[18:19], v[90:91]
	v_exp_f32_e32 v92, v92
	v_pk_fma_f32 v[18:19], v[124:125], s[32:33], v[90:91] op_sel_hi:[0,1,1]
	v_exp_f32_e32 v93, v93
	v_pk_mul_f32 v[94:95], v[82:83], v[6:7] op_sel_hi:[0,1]
	v_pk_mul_f32 v[92:93], v[20:21], v[92:93]
	v_exp_f32_e32 v94, v94
	v_pk_fma_f32 v[20:21], v[124:125], s[34:35], v[92:93] op_sel_hi:[0,1,1]
	v_exp_f32_e32 v95, v95
	v_pk_mul_f32 v[96:97], v[82:83], v[8:9] op_sel_hi:[0,1]
	v_pk_mul_f32 v[94:95], v[22:23], v[94:95]
	v_exp_f32_e32 v96, v96
	v_pk_fma_f32 v[22:23], v[124:125], s[36:37], v[94:95] op_sel_hi:[0,1,1]
	v_exp_f32_e32 v97, v97
	v_pk_mul_f32 v[90:91], v[82:83], v[10:11] op_sel_hi:[0,1]
	v_pk_mul_f32 v[96:97], v[24:25], v[96:97]
	v_exp_f32_e32 v90, v90
	v_pk_fma_f32 v[24:25], v[124:125], s[38:39], v[96:97] op_sel_hi:[0,1,1]
	v_exp_f32_e32 v91, v91
	v_pk_mul_f32 v[92:93], v[82:83], v[12:13] op_sel_hi:[0,1]
	v_pk_mul_f32 v[90:91], v[26:27], v[90:91]
	v_exp_f32_e32 v92, v92
	v_pk_fma_f32 v[26:27], v[124:125], s[40:41], v[90:91] op_sel_hi:[0,1,1]
	v_exp_f32_e32 v93, v93
	v_pk_mul_f32 v[94:95], v[82:83], v[14:15] op_sel_hi:[0,1]
	v_pk_mul_f32 v[92:93], v[28:29], v[92:93]
	v_exp_f32_e32 v94, v94
	v_pk_fma_f32 v[28:29], v[124:125], s[42:43], v[92:93] op_sel_hi:[0,1,1]
	v_exp_f32_e32 v95, v95
	v_pk_mul_f32 v[96:97], v[82:83], v[16:17] op_sel_hi:[0,1]
	v_pk_mul_f32 v[94:95], v[30:31], v[94:95]
	v_exp_f32_e32 v96, v96
	v_pk_fma_f32 v[30:31], v[124:125], s[44:45], v[94:95] op_sel_hi:[0,1,1]
	v_exp_f32_e32 v97, v97
	s_nop 0
	v_pk_mul_f32 v[96:97], v[32:33], v[96:97]
	s_nop 0
	v_pk_fma_f32 v[32:33], v[124:125], s[46:47], v[96:97] op_sel_hi:[0,1,1]
	v_mul_f32_e32 v124, v83, v125
	s_waitcnt lgkmcnt(0)
	s_load_dwordx16 s[32:47], s[70:71], 0x900
	v_fma_f32 v98, v44, s64, v122
	v_mul_f32_e64 v99, -|v98|, s65
	v_cvt_f32_f16_e32 v125, v75
	v_exp_f32_e32 v99, v99
	v_max_f32_e32 v98, 0, v98
	v_add_f32_e32 v99, 1.0, v99
	v_log_f32_e32 v99, v99
	v_pk_mul_f32 v[90:91], v[82:83], v[2:3] op_sel:[1,0]
	v_fma_f32 v84, v99, s66, v98
	v_add_f32_e32 v123, v123, v84
	v_exp_f32_e32 v90, v90
	v_exp_f32_e32 v91, v91
	v_pk_mul_f32 v[92:93], v[82:83], v[4:5] op_sel:[1,0]
	v_pk_mul_f32 v[90:91], v[18:19], v[90:91]
	v_exp_f32_e32 v92, v92
	v_pk_fma_f32 v[18:19], v[124:125], s[48:49], v[90:91] op_sel_hi:[0,1,1]
	v_exp_f32_e32 v93, v93
	v_pk_mul_f32 v[94:95], v[82:83], v[6:7] op_sel:[1,0]
	v_pk_mul_f32 v[92:93], v[20:21], v[92:93]
	v_exp_f32_e32 v94, v94
	v_pk_fma_f32 v[20:21], v[124:125], s[50:51], v[92:93] op_sel_hi:[0,1,1]
	v_exp_f32_e32 v95, v95
	v_pk_mul_f32 v[96:97], v[82:83], v[8:9] op_sel:[1,0]
	v_pk_mul_f32 v[94:95], v[22:23], v[94:95]
	v_exp_f32_e32 v96, v96
	v_pk_fma_f32 v[22:23], v[124:125], s[52:53], v[94:95] op_sel_hi:[0,1,1]
	v_exp_f32_e32 v97, v97
	v_pk_mul_f32 v[90:91], v[82:83], v[10:11] op_sel:[1,0]
	v_pk_mul_f32 v[96:97], v[24:25], v[96:97]
	v_exp_f32_e32 v90, v90
	v_pk_fma_f32 v[24:25], v[124:125], s[54:55], v[96:97] op_sel_hi:[0,1,1]
	v_exp_f32_e32 v91, v91
	v_pk_mul_f32 v[92:93], v[82:83], v[12:13] op_sel:[1,0]
	v_pk_mul_f32 v[90:91], v[26:27], v[90:91]
	v_exp_f32_e32 v92, v92
	v_pk_fma_f32 v[26:27], v[124:125], s[56:57], v[90:91] op_sel_hi:[0,1,1]
	v_exp_f32_e32 v93, v93
	v_pk_mul_f32 v[94:95], v[82:83], v[14:15] op_sel:[1,0]
	v_pk_mul_f32 v[92:93], v[28:29], v[92:93]
	v_exp_f32_e32 v94, v94
	v_pk_fma_f32 v[28:29], v[124:125], s[58:59], v[92:93] op_sel_hi:[0,1,1]
	v_exp_f32_e32 v95, v95
	v_pk_mul_f32 v[96:97], v[82:83], v[16:17] op_sel:[1,0]
	v_pk_mul_f32 v[94:95], v[30:31], v[94:95]
	v_exp_f32_e32 v96, v96
	v_pk_fma_f32 v[30:31], v[124:125], s[60:61], v[94:95] op_sel_hi:[0,1,1]
	v_exp_f32_e32 v97, v97
	s_nop 0
	v_pk_mul_f32 v[96:97], v[32:33], v[96:97]
	s_nop 0
	v_pk_fma_f32 v[32:33], v[124:125], s[62:63], v[96:97] op_sel_hi:[0,1,1]
	v_mul_f32_e32 v124, v84, v125
	s_waitcnt lgkmcnt(0)
	s_load_dwordx16 s[48:63], s[70:71], 0x980
	v_fma_f32 v98, v45, s64, v122
	v_mul_f32_e64 v99, -|v98|, s65
	v_cvt_f32_f16_sdwa v125, v75 dst_sel:DWORD dst_unused:UNUSED_PAD src0_sel:WORD_1
	v_exp_f32_e32 v99, v99
	v_max_f32_e32 v98, 0, v98
	v_add_f32_e32 v99, 1.0, v99
	v_log_f32_e32 v99, v99
	v_pk_mul_f32 v[90:91], v[84:85], v[2:3] op_sel_hi:[0,1]
	v_fma_f32 v85, v99, s66, v98
	v_add_f32_e32 v123, v123, v85
	v_exp_f32_e32 v90, v90
	v_exp_f32_e32 v91, v91
	v_pk_mul_f32 v[92:93], v[84:85], v[4:5] op_sel_hi:[0,1]
	v_pk_mul_f32 v[90:91], v[18:19], v[90:91]
	v_exp_f32_e32 v92, v92
	v_pk_fma_f32 v[18:19], v[124:125], s[32:33], v[90:91] op_sel_hi:[0,1,1]
	v_exp_f32_e32 v93, v93
	v_pk_mul_f32 v[94:95], v[84:85], v[6:7] op_sel_hi:[0,1]
	v_pk_mul_f32 v[92:93], v[20:21], v[92:93]
	v_exp_f32_e32 v94, v94
	v_pk_fma_f32 v[20:21], v[124:125], s[34:35], v[92:93] op_sel_hi:[0,1,1]
	v_exp_f32_e32 v95, v95
	v_pk_mul_f32 v[96:97], v[84:85], v[8:9] op_sel_hi:[0,1]
	v_pk_mul_f32 v[94:95], v[22:23], v[94:95]
	v_exp_f32_e32 v96, v96
	v_pk_fma_f32 v[22:23], v[124:125], s[36:37], v[94:95] op_sel_hi:[0,1,1]
	v_exp_f32_e32 v97, v97
	v_pk_mul_f32 v[90:91], v[84:85], v[10:11] op_sel_hi:[0,1]
	v_pk_mul_f32 v[96:97], v[24:25], v[96:97]
	v_exp_f32_e32 v90, v90
	v_pk_fma_f32 v[24:25], v[124:125], s[38:39], v[96:97] op_sel_hi:[0,1,1]
	v_exp_f32_e32 v91, v91
	v_pk_mul_f32 v[92:93], v[84:85], v[12:13] op_sel_hi:[0,1]
	v_pk_mul_f32 v[90:91], v[26:27], v[90:91]
	v_exp_f32_e32 v92, v92
	v_pk_fma_f32 v[26:27], v[124:125], s[40:41], v[90:91] op_sel_hi:[0,1,1]
	v_exp_f32_e32 v93, v93
	v_pk_mul_f32 v[94:95], v[84:85], v[14:15] op_sel_hi:[0,1]
	v_pk_mul_f32 v[92:93], v[28:29], v[92:93]
	v_exp_f32_e32 v94, v94
	v_pk_fma_f32 v[28:29], v[124:125], s[42:43], v[92:93] op_sel_hi:[0,1,1]
	v_exp_f32_e32 v95, v95
	v_pk_mul_f32 v[96:97], v[84:85], v[16:17] op_sel_hi:[0,1]
	v_pk_mul_f32 v[94:95], v[30:31], v[94:95]
	v_exp_f32_e32 v96, v96
	v_pk_fma_f32 v[30:31], v[124:125], s[44:45], v[94:95] op_sel_hi:[0,1,1]
	v_exp_f32_e32 v97, v97
	s_nop 0
	v_pk_mul_f32 v[96:97], v[32:33], v[96:97]
	s_nop 0
	v_pk_fma_f32 v[32:33], v[124:125], s[46:47], v[96:97] op_sel_hi:[0,1,1]
	v_mul_f32_e32 v124, v85, v125
	s_waitcnt lgkmcnt(0)
	s_load_dwordx16 s[32:47], s[70:71], 0xa00
	v_fma_f32 v98, v58, s64, v122
	v_mul_f32_e64 v99, -|v98|, s65
	v_cvt_f32_f16_e32 v125, v76
	v_exp_f32_e32 v99, v99
	v_max_f32_e32 v98, 0, v98
	v_add_f32_e32 v99, 1.0, v99
	v_log_f32_e32 v99, v99
	v_pk_mul_f32 v[90:91], v[84:85], v[2:3] op_sel:[1,0]
	v_fma_f32 v86, v99, s66, v98
	v_add_f32_e32 v123, v123, v86
	v_exp_f32_e32 v90, v90
	v_exp_f32_e32 v91, v91
	v_pk_mul_f32 v[92:93], v[84:85], v[4:5] op_sel:[1,0]
	v_pk_mul_f32 v[90:91], v[18:19], v[90:91]
	v_exp_f32_e32 v92, v92
	v_pk_fma_f32 v[18:19], v[124:125], s[48:49], v[90:91] op_sel_hi:[0,1,1]
	v_exp_f32_e32 v93, v93
	v_pk_mul_f32 v[94:95], v[84:85], v[6:7] op_sel:[1,0]
	v_pk_mul_f32 v[92:93], v[20:21], v[92:93]
	v_exp_f32_e32 v94, v94
	v_pk_fma_f32 v[20:21], v[124:125], s[50:51], v[92:93] op_sel_hi:[0,1,1]
	v_exp_f32_e32 v95, v95
	v_pk_mul_f32 v[96:97], v[84:85], v[8:9] op_sel:[1,0]
	v_pk_mul_f32 v[94:95], v[22:23], v[94:95]
	v_exp_f32_e32 v96, v96
	v_pk_fma_f32 v[22:23], v[124:125], s[52:53], v[94:95] op_sel_hi:[0,1,1]
	v_exp_f32_e32 v97, v97
	v_pk_mul_f32 v[90:91], v[84:85], v[10:11] op_sel:[1,0]
	v_pk_mul_f32 v[96:97], v[24:25], v[96:97]
	v_exp_f32_e32 v90, v90
	v_pk_fma_f32 v[24:25], v[124:125], s[54:55], v[96:97] op_sel_hi:[0,1,1]
	v_exp_f32_e32 v91, v91
	v_pk_mul_f32 v[92:93], v[84:85], v[12:13] op_sel:[1,0]
	v_pk_mul_f32 v[90:91], v[26:27], v[90:91]
	v_exp_f32_e32 v92, v92
	v_pk_fma_f32 v[26:27], v[124:125], s[56:57], v[90:91] op_sel_hi:[0,1,1]
	v_exp_f32_e32 v93, v93
	v_pk_mul_f32 v[94:95], v[84:85], v[14:15] op_sel:[1,0]
	v_pk_mul_f32 v[92:93], v[28:29], v[92:93]
	v_exp_f32_e32 v94, v94
	v_pk_fma_f32 v[28:29], v[124:125], s[58:59], v[92:93] op_sel_hi:[0,1,1]
	v_exp_f32_e32 v95, v95
	v_pk_mul_f32 v[96:97], v[84:85], v[16:17] op_sel:[1,0]
	v_pk_mul_f32 v[94:95], v[30:31], v[94:95]
	v_exp_f32_e32 v96, v96
	v_pk_fma_f32 v[30:31], v[124:125], s[60:61], v[94:95] op_sel_hi:[0,1,1]
	v_exp_f32_e32 v97, v97
	s_nop 0
	v_pk_mul_f32 v[96:97], v[32:33], v[96:97]
	s_nop 0
	v_pk_fma_f32 v[32:33], v[124:125], s[62:63], v[96:97] op_sel_hi:[0,1,1]
	v_mul_f32_e32 v124, v86, v125
	global_store_dwordx4 v126, v[82:85], s[72:73]
	s_add_u32 s72, s72, 0x8000
	s_addc_u32 s73, s73, 0
	s_waitcnt lgkmcnt(0)
	s_load_dwordx16 s[48:63], s[70:71], 0xa80
	v_fma_f32 v98, v59, s64, v122
	v_mul_f32_e64 v99, -|v98|, s65
	v_cvt_f32_f16_sdwa v125, v76 dst_sel:DWORD dst_unused:UNUSED_PAD src0_sel:WORD_1
	v_exp_f32_e32 v99, v99
	v_max_f32_e32 v98, 0, v98
	v_add_f32_e32 v99, 1.0, v99
	v_log_f32_e32 v99, v99
	v_pk_mul_f32 v[90:91], v[86:87], v[2:3] op_sel_hi:[0,1]
	v_fma_f32 v87, v99, s66, v98
	v_add_f32_e32 v123, v123, v87
	v_exp_f32_e32 v90, v90
	v_exp_f32_e32 v91, v91
	v_pk_mul_f32 v[92:93], v[86:87], v[4:5] op_sel_hi:[0,1]
	v_pk_mul_f32 v[90:91], v[18:19], v[90:91]
	v_exp_f32_e32 v92, v92
	v_pk_fma_f32 v[18:19], v[124:125], s[32:33], v[90:91] op_sel_hi:[0,1,1]
	v_exp_f32_e32 v93, v93
	v_pk_mul_f32 v[94:95], v[86:87], v[6:7] op_sel_hi:[0,1]
	v_pk_mul_f32 v[92:93], v[20:21], v[92:93]
	v_exp_f32_e32 v94, v94
	v_pk_fma_f32 v[20:21], v[124:125], s[34:35], v[92:93] op_sel_hi:[0,1,1]
	v_exp_f32_e32 v95, v95
	v_pk_mul_f32 v[96:97], v[86:87], v[8:9] op_sel_hi:[0,1]
	v_pk_mul_f32 v[94:95], v[22:23], v[94:95]
	v_exp_f32_e32 v96, v96
	v_pk_fma_f32 v[22:23], v[124:125], s[36:37], v[94:95] op_sel_hi:[0,1,1]
	v_exp_f32_e32 v97, v97
	v_pk_mul_f32 v[90:91], v[86:87], v[10:11] op_sel_hi:[0,1]
	v_pk_mul_f32 v[96:97], v[24:25], v[96:97]
	v_exp_f32_e32 v90, v90
	v_pk_fma_f32 v[24:25], v[124:125], s[38:39], v[96:97] op_sel_hi:[0,1,1]
	v_exp_f32_e32 v91, v91
	v_pk_mul_f32 v[92:93], v[86:87], v[12:13] op_sel_hi:[0,1]
	v_pk_mul_f32 v[90:91], v[26:27], v[90:91]
	v_exp_f32_e32 v92, v92
	v_pk_fma_f32 v[26:27], v[124:125], s[40:41], v[90:91] op_sel_hi:[0,1,1]
	v_exp_f32_e32 v93, v93
	v_pk_mul_f32 v[94:95], v[86:87], v[14:15] op_sel_hi:[0,1]
	v_pk_mul_f32 v[92:93], v[28:29], v[92:93]
	v_exp_f32_e32 v94, v94
	v_pk_fma_f32 v[28:29], v[124:125], s[42:43], v[92:93] op_sel_hi:[0,1,1]
	v_exp_f32_e32 v95, v95
	v_pk_mul_f32 v[96:97], v[86:87], v[16:17] op_sel_hi:[0,1]
	v_pk_mul_f32 v[94:95], v[30:31], v[94:95]
	v_exp_f32_e32 v96, v96
	v_pk_fma_f32 v[30:31], v[124:125], s[44:45], v[94:95] op_sel_hi:[0,1,1]
	v_exp_f32_e32 v97, v97
	s_nop 0
	v_pk_mul_f32 v[96:97], v[32:33], v[96:97]
	s_nop 0
	v_pk_fma_f32 v[32:33], v[124:125], s[46:47], v[96:97] op_sel_hi:[0,1,1]
	v_mul_f32_e32 v124, v87, v125
	s_waitcnt lgkmcnt(0)
	s_load_dwordx16 s[32:47], s[70:71], 0xb00
	v_fma_f32 v98, v60, s64, v122
	v_mul_f32_e64 v99, -|v98|, s65
	v_cvt_f32_f16_e32 v125, v77
	v_exp_f32_e32 v99, v99
	v_max_f32_e32 v98, 0, v98
	v_add_f32_e32 v99, 1.0, v99
	v_log_f32_e32 v99, v99
	v_pk_mul_f32 v[90:91], v[86:87], v[2:3] op_sel:[1,0]
	v_fma_f32 v88, v99, s66, v98
	v_add_f32_e32 v123, v123, v88
	v_exp_f32_e32 v90, v90
	v_exp_f32_e32 v91, v91
	v_pk_mul_f32 v[92:93], v[86:87], v[4:5] op_sel:[1,0]
	v_pk_mul_f32 v[90:91], v[18:19], v[90:91]
	v_exp_f32_e32 v92, v92
	v_pk_fma_f32 v[18:19], v[124:125], s[48:49], v[90:91] op_sel_hi:[0,1,1]
	v_exp_f32_e32 v93, v93
	v_pk_mul_f32 v[94:95], v[86:87], v[6:7] op_sel:[1,0]
	v_pk_mul_f32 v[92:93], v[20:21], v[92:93]
	v_exp_f32_e32 v94, v94
	v_pk_fma_f32 v[20:21], v[124:125], s[50:51], v[92:93] op_sel_hi:[0,1,1]
	v_exp_f32_e32 v95, v95
	v_pk_mul_f32 v[96:97], v[86:87], v[8:9] op_sel:[1,0]
	v_pk_mul_f32 v[94:95], v[22:23], v[94:95]
	v_exp_f32_e32 v96, v96
	v_pk_fma_f32 v[22:23], v[124:125], s[52:53], v[94:95] op_sel_hi:[0,1,1]
	v_exp_f32_e32 v97, v97
	v_pk_mul_f32 v[90:91], v[86:87], v[10:11] op_sel:[1,0]
	v_pk_mul_f32 v[96:97], v[24:25], v[96:97]
	v_exp_f32_e32 v90, v90
	v_pk_fma_f32 v[24:25], v[124:125], s[54:55], v[96:97] op_sel_hi:[0,1,1]
	v_exp_f32_e32 v91, v91
	v_pk_mul_f32 v[92:93], v[86:87], v[12:13] op_sel:[1,0]
	v_pk_mul_f32 v[90:91], v[26:27], v[90:91]
	v_exp_f32_e32 v92, v92
	v_pk_fma_f32 v[26:27], v[124:125], s[56:57], v[90:91] op_sel_hi:[0,1,1]
	v_exp_f32_e32 v93, v93
	v_pk_mul_f32 v[94:95], v[86:87], v[14:15] op_sel:[1,0]
	v_pk_mul_f32 v[92:93], v[28:29], v[92:93]
	v_exp_f32_e32 v94, v94
	v_pk_fma_f32 v[28:29], v[124:125], s[58:59], v[92:93] op_sel_hi:[0,1,1]
	v_exp_f32_e32 v95, v95
	v_pk_mul_f32 v[96:97], v[86:87], v[16:17] op_sel:[1,0]
	v_pk_mul_f32 v[94:95], v[30:31], v[94:95]
	v_exp_f32_e32 v96, v96
	v_pk_fma_f32 v[30:31], v[124:125], s[60:61], v[94:95] op_sel_hi:[0,1,1]
	v_exp_f32_e32 v97, v97
	s_nop 0
	v_pk_mul_f32 v[96:97], v[32:33], v[96:97]
	s_nop 0
	v_pk_fma_f32 v[32:33], v[124:125], s[62:63], v[96:97] op_sel_hi:[0,1,1]
	v_mul_f32_e32 v124, v88, v125
	s_waitcnt lgkmcnt(0)
	s_load_dwordx16 s[48:63], s[70:71], 0xb80
	v_fma_f32 v98, v61, s64, v122
	v_mul_f32_e64 v99, -|v98|, s65
	v_cvt_f32_f16_sdwa v125, v77 dst_sel:DWORD dst_unused:UNUSED_PAD src0_sel:WORD_1
	v_exp_f32_e32 v99, v99
	v_max_f32_e32 v98, 0, v98
	v_add_f32_e32 v99, 1.0, v99
	v_log_f32_e32 v99, v99
	v_pk_mul_f32 v[90:91], v[88:89], v[2:3] op_sel_hi:[0,1]
	v_fma_f32 v89, v99, s66, v98
	v_add_f32_e32 v123, v123, v89
	v_exp_f32_e32 v90, v90
	v_exp_f32_e32 v91, v91
	v_pk_mul_f32 v[92:93], v[88:89], v[4:5] op_sel_hi:[0,1]
	v_pk_mul_f32 v[90:91], v[18:19], v[90:91]
	v_exp_f32_e32 v92, v92
	v_pk_fma_f32 v[18:19], v[124:125], s[32:33], v[90:91] op_sel_hi:[0,1,1]
	v_exp_f32_e32 v93, v93
	v_pk_mul_f32 v[94:95], v[88:89], v[6:7] op_sel_hi:[0,1]
	v_pk_mul_f32 v[92:93], v[20:21], v[92:93]
	v_exp_f32_e32 v94, v94
	v_pk_fma_f32 v[20:21], v[124:125], s[34:35], v[92:93] op_sel_hi:[0,1,1]
	v_exp_f32_e32 v95, v95
	v_pk_mul_f32 v[96:97], v[88:89], v[8:9] op_sel_hi:[0,1]
	v_pk_mul_f32 v[94:95], v[22:23], v[94:95]
	v_exp_f32_e32 v96, v96
	v_pk_fma_f32 v[22:23], v[124:125], s[36:37], v[94:95] op_sel_hi:[0,1,1]
	v_exp_f32_e32 v97, v97
	v_pk_mul_f32 v[90:91], v[88:89], v[10:11] op_sel_hi:[0,1]
	v_pk_mul_f32 v[96:97], v[24:25], v[96:97]
	v_exp_f32_e32 v90, v90
	v_pk_fma_f32 v[24:25], v[124:125], s[38:39], v[96:97] op_sel_hi:[0,1,1]
	v_exp_f32_e32 v91, v91
	v_pk_mul_f32 v[92:93], v[88:89], v[12:13] op_sel_hi:[0,1]
	v_pk_mul_f32 v[90:91], v[26:27], v[90:91]
	v_exp_f32_e32 v92, v92
	v_pk_fma_f32 v[26:27], v[124:125], s[40:41], v[90:91] op_sel_hi:[0,1,1]
	v_exp_f32_e32 v93, v93
	v_pk_mul_f32 v[94:95], v[88:89], v[14:15] op_sel_hi:[0,1]
	v_pk_mul_f32 v[92:93], v[28:29], v[92:93]
	v_exp_f32_e32 v94, v94
	v_pk_fma_f32 v[28:29], v[124:125], s[42:43], v[92:93] op_sel_hi:[0,1,1]
	v_exp_f32_e32 v95, v95
	v_pk_mul_f32 v[96:97], v[88:89], v[16:17] op_sel_hi:[0,1]
	v_pk_mul_f32 v[94:95], v[30:31], v[94:95]
	v_exp_f32_e32 v96, v96
	v_pk_fma_f32 v[30:31], v[124:125], s[44:45], v[94:95] op_sel_hi:[0,1,1]
	v_exp_f32_e32 v97, v97
	s_nop 0
	v_pk_mul_f32 v[96:97], v[32:33], v[96:97]
	s_nop 0
	v_pk_fma_f32 v[32:33], v[124:125], s[46:47], v[96:97] op_sel_hi:[0,1,1]
	v_mul_f32_e32 v124, v89, v125
	s_waitcnt vmcnt(7)
	s_waitcnt lgkmcnt(0)
	s_load_dwordx16 s[32:47], s[70:71], 0xc00
	v_fma_f32 v98, v46, s64, v122
	v_mul_f32_e64 v99, -|v98|, s65
	v_cvt_f32_f16_e32 v125, v78
	v_exp_f32_e32 v99, v99
	v_max_f32_e32 v98, 0, v98
	v_add_f32_e32 v99, 1.0, v99
	v_log_f32_e32 v99, v99
	v_pk_mul_f32 v[90:91], v[88:89], v[2:3] op_sel:[1,0]
	v_fma_f32 v82, v99, s66, v98
	v_add_f32_e32 v123, v123, v82
	v_exp_f32_e32 v90, v90
	v_exp_f32_e32 v91, v91
	v_pk_mul_f32 v[92:93], v[88:89], v[4:5] op_sel:[1,0]
	v_pk_mul_f32 v[90:91], v[18:19], v[90:91]
	v_exp_f32_e32 v92, v92
	v_pk_fma_f32 v[18:19], v[124:125], s[48:49], v[90:91] op_sel_hi:[0,1,1]
	v_exp_f32_e32 v93, v93
	v_pk_mul_f32 v[94:95], v[88:89], v[6:7] op_sel:[1,0]
	v_pk_mul_f32 v[92:93], v[20:21], v[92:93]
	v_exp_f32_e32 v94, v94
	v_pk_fma_f32 v[20:21], v[124:125], s[50:51], v[92:93] op_sel_hi:[0,1,1]
	v_exp_f32_e32 v95, v95
	v_pk_mul_f32 v[96:97], v[88:89], v[8:9] op_sel:[1,0]
	v_pk_mul_f32 v[94:95], v[22:23], v[94:95]
	v_exp_f32_e32 v96, v96
	v_pk_fma_f32 v[22:23], v[124:125], s[52:53], v[94:95] op_sel_hi:[0,1,1]
	v_exp_f32_e32 v97, v97
	v_pk_mul_f32 v[90:91], v[88:89], v[10:11] op_sel:[1,0]
	v_pk_mul_f32 v[96:97], v[24:25], v[96:97]
	v_exp_f32_e32 v90, v90
	v_pk_fma_f32 v[24:25], v[124:125], s[54:55], v[96:97] op_sel_hi:[0,1,1]
	v_exp_f32_e32 v91, v91
	v_pk_mul_f32 v[92:93], v[88:89], v[12:13] op_sel:[1,0]
	v_pk_mul_f32 v[90:91], v[26:27], v[90:91]
	v_exp_f32_e32 v92, v92
	v_pk_fma_f32 v[26:27], v[124:125], s[56:57], v[90:91] op_sel_hi:[0,1,1]
	v_exp_f32_e32 v93, v93
	v_pk_mul_f32 v[94:95], v[88:89], v[14:15] op_sel:[1,0]
	v_pk_mul_f32 v[92:93], v[28:29], v[92:93]
	v_exp_f32_e32 v94, v94
	v_pk_fma_f32 v[28:29], v[124:125], s[58:59], v[92:93] op_sel_hi:[0,1,1]
	v_exp_f32_e32 v95, v95
	v_pk_mul_f32 v[96:97], v[88:89], v[16:17] op_sel:[1,0]
	v_pk_mul_f32 v[94:95], v[30:31], v[94:95]
	v_exp_f32_e32 v96, v96
	v_pk_fma_f32 v[30:31], v[124:125], s[60:61], v[94:95] op_sel_hi:[0,1,1]
	v_exp_f32_e32 v97, v97
	s_nop 0
	v_pk_mul_f32 v[96:97], v[32:33], v[96:97]
	s_nop 0
	v_pk_fma_f32 v[32:33], v[124:125], s[62:63], v[96:97] op_sel_hi:[0,1,1]
	v_mul_f32_e32 v124, v82, v125
	global_store_dwordx4 v126, v[86:89], s[72:73]
	s_add_u32 s72, s72, 0x8000
	s_addc_u32 s73, s73, 0
	s_waitcnt lgkmcnt(0)
	s_load_dwordx16 s[48:63], s[70:71], 0xc80
	v_fma_f32 v98, v47, s64, v122
	v_mul_f32_e64 v99, -|v98|, s65
	v_cvt_f32_f16_sdwa v125, v78 dst_sel:DWORD dst_unused:UNUSED_PAD src0_sel:WORD_1
	v_exp_f32_e32 v99, v99
	v_max_f32_e32 v98, 0, v98
	v_add_f32_e32 v99, 1.0, v99
	v_log_f32_e32 v99, v99
	v_pk_mul_f32 v[90:91], v[82:83], v[2:3] op_sel_hi:[0,1]
	v_fma_f32 v83, v99, s66, v98
	v_add_f32_e32 v123, v123, v83
	v_exp_f32_e32 v90, v90
	v_exp_f32_e32 v91, v91
	v_pk_mul_f32 v[92:93], v[82:83], v[4:5] op_sel_hi:[0,1]
	v_pk_mul_f32 v[90:91], v[18:19], v[90:91]
	v_exp_f32_e32 v92, v92
	v_pk_fma_f32 v[18:19], v[124:125], s[32:33], v[90:91] op_sel_hi:[0,1,1]
	v_exp_f32_e32 v93, v93
	v_pk_mul_f32 v[94:95], v[82:83], v[6:7] op_sel_hi:[0,1]
	v_pk_mul_f32 v[92:93], v[20:21], v[92:93]
	v_exp_f32_e32 v94, v94
	v_pk_fma_f32 v[20:21], v[124:125], s[34:35], v[92:93] op_sel_hi:[0,1,1]
	v_exp_f32_e32 v95, v95
	v_pk_mul_f32 v[96:97], v[82:83], v[8:9] op_sel_hi:[0,1]
	v_pk_mul_f32 v[94:95], v[22:23], v[94:95]
	v_exp_f32_e32 v96, v96
	v_pk_fma_f32 v[22:23], v[124:125], s[36:37], v[94:95] op_sel_hi:[0,1,1]
	v_exp_f32_e32 v97, v97
	v_pk_mul_f32 v[90:91], v[82:83], v[10:11] op_sel_hi:[0,1]
	v_pk_mul_f32 v[96:97], v[24:25], v[96:97]
	v_exp_f32_e32 v90, v90
	v_pk_fma_f32 v[24:25], v[124:125], s[38:39], v[96:97] op_sel_hi:[0,1,1]
	v_exp_f32_e32 v91, v91
	v_pk_mul_f32 v[92:93], v[82:83], v[12:13] op_sel_hi:[0,1]
	v_pk_mul_f32 v[90:91], v[26:27], v[90:91]
	v_exp_f32_e32 v92, v92
	v_pk_fma_f32 v[26:27], v[124:125], s[40:41], v[90:91] op_sel_hi:[0,1,1]
	v_exp_f32_e32 v93, v93
	v_pk_mul_f32 v[94:95], v[82:83], v[14:15] op_sel_hi:[0,1]
	v_pk_mul_f32 v[92:93], v[28:29], v[92:93]
	v_exp_f32_e32 v94, v94
	v_pk_fma_f32 v[28:29], v[124:125], s[42:43], v[92:93] op_sel_hi:[0,1,1]
	v_exp_f32_e32 v95, v95
	v_pk_mul_f32 v[96:97], v[82:83], v[16:17] op_sel_hi:[0,1]
	v_pk_mul_f32 v[94:95], v[30:31], v[94:95]
	v_exp_f32_e32 v96, v96
	v_pk_fma_f32 v[30:31], v[124:125], s[44:45], v[94:95] op_sel_hi:[0,1,1]
	v_exp_f32_e32 v97, v97
	s_nop 0
	v_pk_mul_f32 v[96:97], v[32:33], v[96:97]
	s_nop 0
	v_pk_fma_f32 v[32:33], v[124:125], s[46:47], v[96:97] op_sel_hi:[0,1,1]
	v_mul_f32_e32 v124, v83, v125
	s_waitcnt lgkmcnt(0)
	s_load_dwordx16 s[32:47], s[70:71], 0xd00
	v_fma_f32 v98, v48, s64, v122
	v_mul_f32_e64 v99, -|v98|, s65
	v_cvt_f32_f16_e32 v125, v79
	v_exp_f32_e32 v99, v99
	v_max_f32_e32 v98, 0, v98
	v_add_f32_e32 v99, 1.0, v99
	v_log_f32_e32 v99, v99
	v_pk_mul_f32 v[90:91], v[82:83], v[2:3] op_sel:[1,0]
	v_fma_f32 v84, v99, s66, v98
	v_add_f32_e32 v123, v123, v84
	v_exp_f32_e32 v90, v90
	v_exp_f32_e32 v91, v91
	v_pk_mul_f32 v[92:93], v[82:83], v[4:5] op_sel:[1,0]
	v_pk_mul_f32 v[90:91], v[18:19], v[90:91]
	v_exp_f32_e32 v92, v92
	v_pk_fma_f32 v[18:19], v[124:125], s[48:49], v[90:91] op_sel_hi:[0,1,1]
	v_exp_f32_e32 v93, v93
	v_pk_mul_f32 v[94:95], v[82:83], v[6:7] op_sel:[1,0]
	v_pk_mul_f32 v[92:93], v[20:21], v[92:93]
	v_exp_f32_e32 v94, v94
	v_pk_fma_f32 v[20:21], v[124:125], s[50:51], v[92:93] op_sel_hi:[0,1,1]
	v_exp_f32_e32 v95, v95
	v_pk_mul_f32 v[96:97], v[82:83], v[8:9] op_sel:[1,0]
	v_pk_mul_f32 v[94:95], v[22:23], v[94:95]
	v_exp_f32_e32 v96, v96
	v_pk_fma_f32 v[22:23], v[124:125], s[52:53], v[94:95] op_sel_hi:[0,1,1]
	v_exp_f32_e32 v97, v97
	v_pk_mul_f32 v[90:91], v[82:83], v[10:11] op_sel:[1,0]
	v_pk_mul_f32 v[96:97], v[24:25], v[96:97]
	v_exp_f32_e32 v90, v90
	v_pk_fma_f32 v[24:25], v[124:125], s[54:55], v[96:97] op_sel_hi:[0,1,1]
	v_exp_f32_e32 v91, v91
	v_pk_mul_f32 v[92:93], v[82:83], v[12:13] op_sel:[1,0]
	v_pk_mul_f32 v[90:91], v[26:27], v[90:91]
	v_exp_f32_e32 v92, v92
	v_pk_fma_f32 v[26:27], v[124:125], s[56:57], v[90:91] op_sel_hi:[0,1,1]
	v_exp_f32_e32 v93, v93
	v_pk_mul_f32 v[94:95], v[82:83], v[14:15] op_sel:[1,0]
	v_pk_mul_f32 v[92:93], v[28:29], v[92:93]
	v_exp_f32_e32 v94, v94
	v_pk_fma_f32 v[28:29], v[124:125], s[58:59], v[92:93] op_sel_hi:[0,1,1]
	v_exp_f32_e32 v95, v95
	v_pk_mul_f32 v[96:97], v[82:83], v[16:17] op_sel:[1,0]
	v_pk_mul_f32 v[94:95], v[30:31], v[94:95]
	v_exp_f32_e32 v96, v96
	v_pk_fma_f32 v[30:31], v[124:125], s[60:61], v[94:95] op_sel_hi:[0,1,1]
	v_exp_f32_e32 v97, v97
	s_nop 0
	v_pk_mul_f32 v[96:97], v[32:33], v[96:97]
	s_nop 0
	v_pk_fma_f32 v[32:33], v[124:125], s[62:63], v[96:97] op_sel_hi:[0,1,1]
	v_mul_f32_e32 v124, v84, v125
	s_waitcnt lgkmcnt(0)
	s_load_dwordx16 s[48:63], s[70:71], 0xd80
	v_fma_f32 v98, v49, s64, v122
	v_mul_f32_e64 v99, -|v98|, s65
	v_cvt_f32_f16_sdwa v125, v79 dst_sel:DWORD dst_unused:UNUSED_PAD src0_sel:WORD_1
	v_exp_f32_e32 v99, v99
	v_max_f32_e32 v98, 0, v98
	v_add_f32_e32 v99, 1.0, v99
	v_log_f32_e32 v99, v99
	v_pk_mul_f32 v[90:91], v[84:85], v[2:3] op_sel_hi:[0,1]
	v_fma_f32 v85, v99, s66, v98
	v_add_f32_e32 v123, v123, v85
	v_exp_f32_e32 v90, v90
	v_exp_f32_e32 v91, v91
	v_pk_mul_f32 v[92:93], v[84:85], v[4:5] op_sel_hi:[0,1]
	v_pk_mul_f32 v[90:91], v[18:19], v[90:91]
	v_exp_f32_e32 v92, v92
	v_pk_fma_f32 v[18:19], v[124:125], s[32:33], v[90:91] op_sel_hi:[0,1,1]
	v_exp_f32_e32 v93, v93
	v_pk_mul_f32 v[94:95], v[84:85], v[6:7] op_sel_hi:[0,1]
	v_pk_mul_f32 v[92:93], v[20:21], v[92:93]
	v_exp_f32_e32 v94, v94
	v_pk_fma_f32 v[20:21], v[124:125], s[34:35], v[92:93] op_sel_hi:[0,1,1]
	v_exp_f32_e32 v95, v95
	v_pk_mul_f32 v[96:97], v[84:85], v[8:9] op_sel_hi:[0,1]
	v_pk_mul_f32 v[94:95], v[22:23], v[94:95]
	v_exp_f32_e32 v96, v96
	v_pk_fma_f32 v[22:23], v[124:125], s[36:37], v[94:95] op_sel_hi:[0,1,1]
	v_exp_f32_e32 v97, v97
	v_pk_mul_f32 v[90:91], v[84:85], v[10:11] op_sel_hi:[0,1]
	v_pk_mul_f32 v[96:97], v[24:25], v[96:97]
	v_exp_f32_e32 v90, v90
	v_pk_fma_f32 v[24:25], v[124:125], s[38:39], v[96:97] op_sel_hi:[0,1,1]
	v_exp_f32_e32 v91, v91
	v_pk_mul_f32 v[92:93], v[84:85], v[12:13] op_sel_hi:[0,1]
	v_pk_mul_f32 v[90:91], v[26:27], v[90:91]
	v_exp_f32_e32 v92, v92
	v_pk_fma_f32 v[26:27], v[124:125], s[40:41], v[90:91] op_sel_hi:[0,1,1]
	v_exp_f32_e32 v93, v93
	v_pk_mul_f32 v[94:95], v[84:85], v[14:15] op_sel_hi:[0,1]
	v_pk_mul_f32 v[92:93], v[28:29], v[92:93]
	v_exp_f32_e32 v94, v94
	v_pk_fma_f32 v[28:29], v[124:125], s[42:43], v[92:93] op_sel_hi:[0,1,1]
	v_exp_f32_e32 v95, v95
	v_pk_mul_f32 v[96:97], v[84:85], v[16:17] op_sel_hi:[0,1]
	v_pk_mul_f32 v[94:95], v[30:31], v[94:95]
	v_exp_f32_e32 v96, v96
	v_pk_fma_f32 v[30:31], v[124:125], s[44:45], v[94:95] op_sel_hi:[0,1,1]
	v_exp_f32_e32 v97, v97
	s_nop 0
	v_pk_mul_f32 v[96:97], v[32:33], v[96:97]
	s_nop 0
	v_pk_fma_f32 v[32:33], v[124:125], s[46:47], v[96:97] op_sel_hi:[0,1,1]
	v_mul_f32_e32 v124, v85, v125
	s_waitcnt lgkmcnt(0)
	s_load_dwordx16 s[32:47], s[70:71], 0xe00
	v_fma_f32 v98, v62, s64, v122
	v_mul_f32_e64 v99, -|v98|, s65
	v_cvt_f32_f16_e32 v125, v80
	v_exp_f32_e32 v99, v99
	v_max_f32_e32 v98, 0, v98
	v_add_f32_e32 v99, 1.0, v99
	v_log_f32_e32 v99, v99
	v_pk_mul_f32 v[90:91], v[84:85], v[2:3] op_sel:[1,0]
	v_fma_f32 v86, v99, s66, v98
	v_add_f32_e32 v123, v123, v86
	v_exp_f32_e32 v90, v90
	v_exp_f32_e32 v91, v91
	v_pk_mul_f32 v[92:93], v[84:85], v[4:5] op_sel:[1,0]
	v_pk_mul_f32 v[90:91], v[18:19], v[90:91]
	v_exp_f32_e32 v92, v92
	v_pk_fma_f32 v[18:19], v[124:125], s[48:49], v[90:91] op_sel_hi:[0,1,1]
	v_exp_f32_e32 v93, v93
	v_pk_mul_f32 v[94:95], v[84:85], v[6:7] op_sel:[1,0]
	v_pk_mul_f32 v[92:93], v[20:21], v[92:93]
	v_exp_f32_e32 v94, v94
	v_pk_fma_f32 v[20:21], v[124:125], s[50:51], v[92:93] op_sel_hi:[0,1,1]
	v_exp_f32_e32 v95, v95
	v_pk_mul_f32 v[96:97], v[84:85], v[8:9] op_sel:[1,0]
	v_pk_mul_f32 v[94:95], v[22:23], v[94:95]
	v_exp_f32_e32 v96, v96
	v_pk_fma_f32 v[22:23], v[124:125], s[52:53], v[94:95] op_sel_hi:[0,1,1]
	v_exp_f32_e32 v97, v97
	v_pk_mul_f32 v[90:91], v[84:85], v[10:11] op_sel:[1,0]
	v_pk_mul_f32 v[96:97], v[24:25], v[96:97]
	v_exp_f32_e32 v90, v90
	v_pk_fma_f32 v[24:25], v[124:125], s[54:55], v[96:97] op_sel_hi:[0,1,1]
	v_exp_f32_e32 v91, v91
	v_pk_mul_f32 v[92:93], v[84:85], v[12:13] op_sel:[1,0]
	v_pk_mul_f32 v[90:91], v[26:27], v[90:91]
	v_exp_f32_e32 v92, v92
	v_pk_fma_f32 v[26:27], v[124:125], s[56:57], v[90:91] op_sel_hi:[0,1,1]
	v_exp_f32_e32 v93, v93
	v_pk_mul_f32 v[94:95], v[84:85], v[14:15] op_sel:[1,0]
	v_pk_mul_f32 v[92:93], v[28:29], v[92:93]
	v_exp_f32_e32 v94, v94
	v_pk_fma_f32 v[28:29], v[124:125], s[58:59], v[92:93] op_sel_hi:[0,1,1]
	v_exp_f32_e32 v95, v95
	v_pk_mul_f32 v[96:97], v[84:85], v[16:17] op_sel:[1,0]
	v_pk_mul_f32 v[94:95], v[30:31], v[94:95]
	v_exp_f32_e32 v96, v96
	v_pk_fma_f32 v[30:31], v[124:125], s[60:61], v[94:95] op_sel_hi:[0,1,1]
	v_exp_f32_e32 v97, v97
	s_nop 0
	v_pk_mul_f32 v[96:97], v[32:33], v[96:97]
	s_nop 0
	v_pk_fma_f32 v[32:33], v[124:125], s[62:63], v[96:97] op_sel_hi:[0,1,1]
	v_mul_f32_e32 v124, v86, v125
	global_store_dwordx4 v126, v[82:85], s[72:73]
	s_add_u32 s72, s72, 0x8000
	s_addc_u32 s73, s73, 0
	s_waitcnt lgkmcnt(0)
	s_load_dwordx16 s[48:63], s[70:71], 0xe80
	v_fma_f32 v98, v63, s64, v122
	v_mul_f32_e64 v99, -|v98|, s65
	v_cvt_f32_f16_sdwa v125, v80 dst_sel:DWORD dst_unused:UNUSED_PAD src0_sel:WORD_1
	v_exp_f32_e32 v99, v99
	v_max_f32_e32 v98, 0, v98
	v_add_f32_e32 v99, 1.0, v99
	v_log_f32_e32 v99, v99
	v_pk_mul_f32 v[90:91], v[86:87], v[2:3] op_sel_hi:[0,1]
	v_fma_f32 v87, v99, s66, v98
	v_add_f32_e32 v123, v123, v87
	v_exp_f32_e32 v90, v90
	v_exp_f32_e32 v91, v91
	v_pk_mul_f32 v[92:93], v[86:87], v[4:5] op_sel_hi:[0,1]
	v_pk_mul_f32 v[90:91], v[18:19], v[90:91]
	v_exp_f32_e32 v92, v92
	v_pk_fma_f32 v[18:19], v[124:125], s[32:33], v[90:91] op_sel_hi:[0,1,1]
	v_exp_f32_e32 v93, v93
	v_pk_mul_f32 v[94:95], v[86:87], v[6:7] op_sel_hi:[0,1]
	v_pk_mul_f32 v[92:93], v[20:21], v[92:93]
	v_exp_f32_e32 v94, v94
	v_pk_fma_f32 v[20:21], v[124:125], s[34:35], v[92:93] op_sel_hi:[0,1,1]
	v_exp_f32_e32 v95, v95
	v_pk_mul_f32 v[96:97], v[86:87], v[8:9] op_sel_hi:[0,1]
	v_pk_mul_f32 v[94:95], v[22:23], v[94:95]
	v_exp_f32_e32 v96, v96
	v_pk_fma_f32 v[22:23], v[124:125], s[36:37], v[94:95] op_sel_hi:[0,1,1]
	v_exp_f32_e32 v97, v97
	v_pk_mul_f32 v[90:91], v[86:87], v[10:11] op_sel_hi:[0,1]
	v_pk_mul_f32 v[96:97], v[24:25], v[96:97]
	v_exp_f32_e32 v90, v90
	v_pk_fma_f32 v[24:25], v[124:125], s[38:39], v[96:97] op_sel_hi:[0,1,1]
	v_exp_f32_e32 v91, v91
	v_pk_mul_f32 v[92:93], v[86:87], v[12:13] op_sel_hi:[0,1]
	v_pk_mul_f32 v[90:91], v[26:27], v[90:91]
	v_exp_f32_e32 v92, v92
	v_pk_fma_f32 v[26:27], v[124:125], s[40:41], v[90:91] op_sel_hi:[0,1,1]
	v_exp_f32_e32 v93, v93
	v_pk_mul_f32 v[94:95], v[86:87], v[14:15] op_sel_hi:[0,1]
	v_pk_mul_f32 v[92:93], v[28:29], v[92:93]
	v_exp_f32_e32 v94, v94
	v_pk_fma_f32 v[28:29], v[124:125], s[42:43], v[92:93] op_sel_hi:[0,1,1]
	v_exp_f32_e32 v95, v95
	v_pk_mul_f32 v[96:97], v[86:87], v[16:17] op_sel_hi:[0,1]
	v_pk_mul_f32 v[94:95], v[30:31], v[94:95]
	v_exp_f32_e32 v96, v96
	v_pk_fma_f32 v[30:31], v[124:125], s[44:45], v[94:95] op_sel_hi:[0,1,1]
	v_exp_f32_e32 v97, v97
	s_nop 0
	v_pk_mul_f32 v[96:97], v[32:33], v[96:97]
	s_nop 0
	v_pk_fma_f32 v[32:33], v[124:125], s[46:47], v[96:97] op_sel_hi:[0,1,1]
	v_mul_f32_e32 v124, v87, v125
	s_waitcnt lgkmcnt(0)
	s_load_dwordx16 s[32:47], s[70:71], 0xf00
	v_fma_f32 v98, v64, s64, v122
	v_mul_f32_e64 v99, -|v98|, s65
	v_cvt_f32_f16_e32 v125, v81
	v_exp_f32_e32 v99, v99
	v_max_f32_e32 v98, 0, v98
	v_add_f32_e32 v99, 1.0, v99
	v_log_f32_e32 v99, v99
	v_pk_mul_f32 v[90:91], v[86:87], v[2:3] op_sel:[1,0]
	v_fma_f32 v88, v99, s66, v98
	v_add_f32_e32 v123, v123, v88
	v_exp_f32_e32 v90, v90
	v_exp_f32_e32 v91, v91
	v_pk_mul_f32 v[92:93], v[86:87], v[4:5] op_sel:[1,0]
	v_pk_mul_f32 v[90:91], v[18:19], v[90:91]
	v_exp_f32_e32 v92, v92
	v_pk_fma_f32 v[18:19], v[124:125], s[48:49], v[90:91] op_sel_hi:[0,1,1]
	v_exp_f32_e32 v93, v93
	v_pk_mul_f32 v[94:95], v[86:87], v[6:7] op_sel:[1,0]
	v_pk_mul_f32 v[92:93], v[20:21], v[92:93]
	v_exp_f32_e32 v94, v94
	v_pk_fma_f32 v[20:21], v[124:125], s[50:51], v[92:93] op_sel_hi:[0,1,1]
	v_exp_f32_e32 v95, v95
	v_pk_mul_f32 v[96:97], v[86:87], v[8:9] op_sel:[1,0]
	v_pk_mul_f32 v[94:95], v[22:23], v[94:95]
	v_exp_f32_e32 v96, v96
	v_pk_fma_f32 v[22:23], v[124:125], s[52:53], v[94:95] op_sel_hi:[0,1,1]
	v_exp_f32_e32 v97, v97
	v_pk_mul_f32 v[90:91], v[86:87], v[10:11] op_sel:[1,0]
	v_pk_mul_f32 v[96:97], v[24:25], v[96:97]
	v_exp_f32_e32 v90, v90
	v_pk_fma_f32 v[24:25], v[124:125], s[54:55], v[96:97] op_sel_hi:[0,1,1]
	v_exp_f32_e32 v91, v91
	v_pk_mul_f32 v[92:93], v[86:87], v[12:13] op_sel:[1,0]
	v_pk_mul_f32 v[90:91], v[26:27], v[90:91]
	v_exp_f32_e32 v92, v92
	v_pk_fma_f32 v[26:27], v[124:125], s[56:57], v[90:91] op_sel_hi:[0,1,1]
	v_exp_f32_e32 v93, v93
	v_pk_mul_f32 v[94:95], v[86:87], v[14:15] op_sel:[1,0]
	v_pk_mul_f32 v[92:93], v[28:29], v[92:93]
	v_exp_f32_e32 v94, v94
	v_pk_fma_f32 v[28:29], v[124:125], s[58:59], v[92:93] op_sel_hi:[0,1,1]
	v_exp_f32_e32 v95, v95
	v_pk_mul_f32 v[96:97], v[86:87], v[16:17] op_sel:[1,0]
	v_pk_mul_f32 v[94:95], v[30:31], v[94:95]
	v_exp_f32_e32 v96, v96
	v_pk_fma_f32 v[30:31], v[124:125], s[60:61], v[94:95] op_sel_hi:[0,1,1]
	v_exp_f32_e32 v97, v97
	s_nop 0
	v_pk_mul_f32 v[96:97], v[32:33], v[96:97]
	s_nop 0
	v_pk_fma_f32 v[32:33], v[124:125], s[62:63], v[96:97] op_sel_hi:[0,1,1]
	v_mul_f32_e32 v124, v88, v125
	s_waitcnt lgkmcnt(0)
	s_load_dwordx16 s[48:63], s[70:71], 0xf80
	v_fma_f32 v98, v65, s64, v122
	v_mul_f32_e64 v99, -|v98|, s65
	v_cvt_f32_f16_sdwa v125, v81 dst_sel:DWORD dst_unused:UNUSED_PAD src0_sel:WORD_1
	v_exp_f32_e32 v99, v99
	v_max_f32_e32 v98, 0, v98
	v_add_f32_e32 v99, 1.0, v99
	v_log_f32_e32 v99, v99
	v_pk_mul_f32 v[90:91], v[88:89], v[2:3] op_sel_hi:[0,1]
	v_fma_f32 v89, v99, s66, v98
	v_add_f32_e32 v123, v123, v89
	v_exp_f32_e32 v90, v90
	v_exp_f32_e32 v91, v91
	v_pk_mul_f32 v[92:93], v[88:89], v[4:5] op_sel_hi:[0,1]
	v_pk_mul_f32 v[90:91], v[18:19], v[90:91]
	v_exp_f32_e32 v92, v92
	v_pk_fma_f32 v[18:19], v[124:125], s[32:33], v[90:91] op_sel_hi:[0,1,1]
	v_exp_f32_e32 v93, v93
	v_pk_mul_f32 v[94:95], v[88:89], v[6:7] op_sel_hi:[0,1]
	v_pk_mul_f32 v[92:93], v[20:21], v[92:93]
	v_exp_f32_e32 v94, v94
	v_pk_fma_f32 v[20:21], v[124:125], s[34:35], v[92:93] op_sel_hi:[0,1,1]
	v_exp_f32_e32 v95, v95
	v_pk_mul_f32 v[96:97], v[88:89], v[8:9] op_sel_hi:[0,1]
	v_pk_mul_f32 v[94:95], v[22:23], v[94:95]
	v_exp_f32_e32 v96, v96
	v_pk_fma_f32 v[22:23], v[124:125], s[36:37], v[94:95] op_sel_hi:[0,1,1]
	v_exp_f32_e32 v97, v97
	v_pk_mul_f32 v[90:91], v[88:89], v[10:11] op_sel_hi:[0,1]
	v_pk_mul_f32 v[96:97], v[24:25], v[96:97]
	v_exp_f32_e32 v90, v90
	v_pk_fma_f32 v[24:25], v[124:125], s[38:39], v[96:97] op_sel_hi:[0,1,1]
	v_exp_f32_e32 v91, v91
	v_pk_mul_f32 v[92:93], v[88:89], v[12:13] op_sel_hi:[0,1]
	v_pk_mul_f32 v[90:91], v[26:27], v[90:91]
	v_exp_f32_e32 v92, v92
	v_pk_fma_f32 v[26:27], v[124:125], s[40:41], v[90:91] op_sel_hi:[0,1,1]
	v_exp_f32_e32 v93, v93
	v_pk_mul_f32 v[94:95], v[88:89], v[14:15] op_sel_hi:[0,1]
	v_pk_mul_f32 v[92:93], v[28:29], v[92:93]
	v_exp_f32_e32 v94, v94
	v_pk_fma_f32 v[28:29], v[124:125], s[42:43], v[92:93] op_sel_hi:[0,1,1]
	v_exp_f32_e32 v95, v95
	v_pk_mul_f32 v[96:97], v[88:89], v[16:17] op_sel_hi:[0,1]
	v_pk_mul_f32 v[94:95], v[30:31], v[94:95]
	v_exp_f32_e32 v96, v96
	v_pk_fma_f32 v[30:31], v[124:125], s[44:45], v[94:95] op_sel_hi:[0,1,1]
	v_exp_f32_e32 v97, v97
	s_nop 0
	v_pk_mul_f32 v[96:97], v[32:33], v[96:97]
	s_nop 0
	v_pk_fma_f32 v[32:33], v[124:125], s[46:47], v[96:97] op_sel_hi:[0,1,1]
	v_mul_f32_e32 v124, v89, v125
	s_waitcnt lgkmcnt(0)
	v_pk_mul_f32 v[90:91], v[88:89], v[2:3] op_sel:[1,0]
	v_pk_mul_f32 v[92:93], v[88:89], v[4:5] op_sel:[1,0]
	v_exp_f32_e32 v90, v90
	v_exp_f32_e32 v91, v91
	v_exp_f32_e32 v92, v92
	v_pk_mul_f32 v[90:91], v[18:19], v[90:91]
	v_exp_f32_e32 v93, v93
	v_pk_fma_f32 v[18:19], v[124:125], s[48:49], v[90:91] op_sel_hi:[0,1,1]
	v_pk_mul_f32 v[92:93], v[20:21], v[92:93]
	v_pk_mul_f32 v[94:95], v[88:89], v[6:7] op_sel:[1,0]
	v_pk_fma_f32 v[20:21], v[124:125], s[50:51], v[92:93] op_sel_hi:[0,1,1]
	v_exp_f32_e32 v94, v94
	v_exp_f32_e32 v95, v95
	v_pk_mul_f32 v[96:97], v[88:89], v[8:9] op_sel:[1,0]
	v_pk_mul_f32 v[94:95], v[22:23], v[94:95]
	v_exp_f32_e32 v96, v96
	v_pk_fma_f32 v[22:23], v[124:125], s[52:53], v[94:95] op_sel_hi:[0,1,1]
	v_exp_f32_e32 v97, v97
	v_pk_mul_f32 v[90:91], v[88:89], v[10:11] op_sel:[1,0]
	v_pk_mul_f32 v[96:97], v[24:25], v[96:97]
	v_exp_f32_e32 v90, v90
	v_pk_fma_f32 v[24:25], v[124:125], s[54:55], v[96:97] op_sel_hi:[0,1,1]
	v_exp_f32_e32 v91, v91
	v_pk_mul_f32 v[92:93], v[88:89], v[12:13] op_sel:[1,0]
	v_pk_mul_f32 v[90:91], v[26:27], v[90:91]
	v_exp_f32_e32 v92, v92
	v_pk_fma_f32 v[26:27], v[124:125], s[56:57], v[90:91] op_sel_hi:[0,1,1]
	v_exp_f32_e32 v93, v93
	v_pk_mul_f32 v[94:95], v[88:89], v[14:15] op_sel:[1,0]
	v_pk_mul_f32 v[92:93], v[28:29], v[92:93]
	v_exp_f32_e32 v94, v94
	v_pk_fma_f32 v[28:29], v[124:125], s[58:59], v[92:93] op_sel_hi:[0,1,1]
	v_exp_f32_e32 v95, v95
	v_pk_mul_f32 v[96:97], v[88:89], v[16:17] op_sel:[1,0]
	v_pk_mul_f32 v[94:95], v[30:31], v[94:95]
	v_exp_f32_e32 v96, v96
	v_pk_fma_f32 v[30:31], v[124:125], s[60:61], v[94:95] op_sel_hi:[0,1,1]
	v_exp_f32_e32 v97, v97
	s_nop 0
	v_pk_mul_f32 v[96:97], v[32:33], v[96:97]
	s_nop 0
	v_pk_fma_f32 v[32:33], v[124:125], s[62:63], v[96:97] op_sel_hi:[0,1,1]
	global_store_dwordx4 v126, v[86:89], s[72:73]
	s_waitcnt vmcnt(8)
	v_pk_mul_f32 v[114:115], v[114:115], s[86:87] op_sel_hi:[1,0]
	v_pk_mul_f32 v[116:117], v[116:117], s[86:87] op_sel_hi:[1,0]
	v_pk_mul_f32 v[118:119], v[118:119], s[86:87] op_sel_hi:[1,0]
	v_pk_mul_f32 v[120:121], v[120:121], s[86:87] op_sel_hi:[1,0]
	v_cvt_pk_f16_f32 v90, v118, v119
	v_cvt_pk_f16_f32 v91, v120, v121
	v_cvt_pk_f16_f32 v92, v114, v115
	v_cvt_pk_f16_f32 v93, v116, v117
	v_lshlrev_b32_e32 v127, 4, v0
	global_store_dwordx4 v127, v[90:93], s[80:81]
	v_lshlrev_b32_e32 v127, 2, v1
	v_pk_mul_f32 v[18:19], v[18:19], s[84:85] op_sel_hi:[1,0]
	v_pk_mul_f32 v[20:21], v[20:21], s[84:85] op_sel_hi:[1,0]
	v_pk_mul_f32 v[22:23], v[22:23], s[84:85] op_sel_hi:[1,0]
	v_pk_mul_f32 v[24:25], v[24:25], s[84:85] op_sel_hi:[1,0]
	v_pk_mul_f32 v[26:27], v[26:27], s[84:85] op_sel_hi:[1,0]
	v_pk_mul_f32 v[28:29], v[28:29], s[84:85] op_sel_hi:[1,0]
	v_pk_mul_f32 v[30:31], v[30:31], s[84:85] op_sel_hi:[1,0]
	v_pk_mul_f32 v[32:33], v[32:33], s[84:85] op_sel_hi:[1,0]
	v_cvt_pk_f16_f32 v98, v18, v19
	v_cvt_pk_f16_f32 v99, v20, v21
	v_cvt_pk_f16_f32 v100, v22, v23
	v_cvt_pk_f16_f32 v101, v24, v25
	v_cvt_pk_f16_f32 v102, v26, v27
	v_cvt_pk_f16_f32 v103, v28, v29
	v_cvt_pk_f16_f32 v104, v30, v31
	v_cvt_pk_f16_f32 v105, v32, v33
	global_store_dword v127, v98, s[76:77]
	s_add_u32 s76, s76, 0x2000
	s_addc_u32 s77, s77, 0
	global_store_dword v127, v99, s[76:77]
	s_add_u32 s76, s76, 0x2000
	s_addc_u32 s77, s77, 0
	global_store_dword v127, v100, s[76:77]
	s_add_u32 s76, s76, 0x2000
	s_addc_u32 s77, s77, 0
	global_store_dword v127, v101, s[76:77]
	s_add_u32 s76, s76, 0x2000
	s_addc_u32 s77, s77, 0
	global_store_dword v127, v102, s[76:77]
	s_add_u32 s76, s76, 0x2000
	s_addc_u32 s77, s77, 0
	global_store_dword v127, v103, s[76:77]
	s_add_u32 s76, s76, 0x2000
	s_addc_u32 s77, s77, 0
	global_store_dword v127, v104, s[76:77]
	s_add_u32 s76, s76, 0x2000
	s_addc_u32 s77, s77, 0
	global_store_dword v127, v105, s[76:77]
	global_store_dword v127, v123, s[78:79]
	s_endpgm
	.p2alignl 8, 3212836864

_Z10scan_pass2PKDF16_PKfS2_S0_S2_S0_PDF16_S2_:
	s_load_dwordx16 s[8:23], s[0:1], 0x0
	s_mov_b32 s28, 0x3e800000
	s_mov_b32 s29, 0x3c800000
	s_mov_b32 s30, 0x40800000
	s_lshl_b32 s5, s4, 11
	s_lshl_b32 s6, s3, 5
	s_add_i32 s5, s5, s6
	s_lshl_b32 s6, s4, 6
	s_add_i32 s6, s6, s3
	s_getreg_b32 s7, hwreg(HW_REG_HW_ID, 0, 4)
	s_and_b32 s7, s7, 3
	s_cmp_eq_u32 s7, 0
	s_cbranch_scc1 .Lstag_p2_done

.Lstag_p2_done:
	v_lshl_or_b32 v1, s2, 8, v0
	v_lshlrev_b32_e32 v99, 1, v1
	v_lshlrev_b32_e32 v100, 6, v1
	v_lshlrev_b32_e32 v101, 2, v1
	v_lshlrev_b32_e32 v102, 4, v1
	v_lshlrev_b32_e32 v103, 3, v1
	s_waitcnt lgkmcnt(0)
	s_lshl_b32 s7, s5, 7
	s_add_u32 s24, s10, s7
	s_addc_u32 s25, s11, 0
	s_load_dwordx16 s[32:47], s[24:25], 0x0
	s_load_dwordx16 s[48:63], s[24:25], 0x40
	global_load_dwordx4 v[2:5], v100, s[12:13]
	global_load_dwordx4 v[6:9], v100, s[12:13] offset:16
	global_load_dwordx4 v[10:13], v100, s[12:13] offset:32
	global_load_dwordx4 v[14:17], v100, s[12:13] offset:48
	s_lshl_b32 s7, s6, 16
	s_add_u32 s96, s14, s7
	s_addc_u32 s97, s15, 0
	global_load_dword v104, v101, s[96:97]
	s_add_u32 s96, s96, 0x2000
	s_addc_u32 s97, s97, 0
	global_load_dword v105, v101, s[96:97]
	s_add_u32 s96, s96, 0x2000
	s_addc_u32 s97, s97, 0
	global_load_dword v106, v101, s[96:97]
	s_add_u32 s96, s96, 0x2000
	s_addc_u32 s97, s97, 0
	global_load_dword v107, v101, s[96:97]
	s_add_u32 s96, s96, 0x2000
	s_addc_u32 s97, s97, 0
	global_load_dword v108, v101, s[96:97]
	s_add_u32 s96, s96, 0x2000
	s_addc_u32 s97, s97, 0
	global_load_dword v109, v101, s[96:97]
	s_add_u32 s96, s96, 0x2000
	s_addc_u32 s97, s97, 0
	global_load_dword v110, v101, s[96:97]
	s_add_u32 s96, s96, 0x2000
	s_addc_u32 s97, s97, 0
	global_load_dword v111, v101, s[96:97]
	s_lshr_b32 s7, s5, 2
	s_lshl_b32 s7, s7, 15
	s_add_u32 s0, s22, s7
	s_addc_u32 s1, s23, 0
	s_add_u32 s2, s18, s7
	s_addc_u32 s3, s19, 0
	s_add_u32 s2, s2, 0x4000
	s_addc_u32 s3, s3, 0
	s_lshr_b32 s7, s5, 3
	s_lshl_b32 s7, s7, 15
	s_add_u32 s8, s8, s7
	s_addc_u32 s9, s9, 0
	s_lshl_b32 s7, s5, 12
	s_add_u32 s26, s20, s7
	s_addc_u32 s27, s21, 0
	global_load_dwordx4 v[34:37], v102, s[0:1]
	s_add_u32 s0, s0, 0x8000
	s_addc_u32 s1, s1, 0
	global_load_dwordx4 v[42:45], v102, s[8:9]
	s_add_u32 s8, s8, 0x8000
	s_addc_u32 s9, s9, 0
	global_load_dwordx2 v[46:47], v103, s[2:3]
	s_add_u32 s2, s2, 0x8000
	s_addc_u32 s3, s3, 0
	global_load_dwordx4 v[38:41], v102, s[0:1]
	s_add_u32 s0, s0, 0x8000
	s_addc_u32 s1, s1, 0
	global_load_dwordx2 v[48:49], v103, s[2:3]
	s_add_u32 s2, s2, 0x8000
	s_addc_u32 s3, s3, 0
	global_load_dword v98, v101, s[16:17]
	s_waitcnt vmcnt(6)
	v_cvt_f32_f16_e32 v18, v104
	v_cvt_f32_f16_sdwa v19, v104 dst_sel:DWORD dst_unused:UNUSED_PAD src0_sel:WORD_1
	v_cvt_f32_f16_e32 v20, v105
	v_cvt_f32_f16_sdwa v21, v105 dst_sel:DWORD dst_unused:UNUSED_PAD src0_sel:WORD_1
	v_cvt_f32_f16_e32 v22, v106
	v_cvt_f32_f16_sdwa v23, v106 dst_sel:DWORD dst_unused:UNUSED_PAD src0_sel:WORD_1
	v_cvt_f32_f16_e32 v24, v107
	v_cvt_f32_f16_sdwa v25, v107 dst_sel:DWORD dst_unused:UNUSED_PAD src0_sel:WORD_1
	v_cvt_f32_f16_e32 v26, v108
	v_cvt_f32_f16_sdwa v27, v108 dst_sel:DWORD dst_unused:UNUSED_PAD src0_sel:WORD_1
	v_cvt_f32_f16_e32 v28, v109
	v_cvt_f32_f16_sdwa v29, v109 dst_sel:DWORD dst_unused:UNUSED_PAD src0_sel:WORD_1
	v_cvt_f32_f16_e32 v30, v110
	v_cvt_f32_f16_sdwa v31, v110 dst_sel:DWORD dst_unused:UNUSED_PAD src0_sel:WORD_1
	v_cvt_f32_f16_e32 v32, v111
	v_cvt_f32_f16_sdwa v33, v111 dst_sel:DWORD dst_unused:UNUSED_PAD src0_sel:WORD_1
	v_pk_mul_f32 v[18:19], v[18:19], s[28:29] op_sel_hi:[1,0]
	v_pk_mul_f32 v[20:21], v[20:21], s[28:29] op_sel_hi:[1,0]
	v_pk_mul_f32 v[22:23], v[22:23], s[28:29] op_sel_hi:[1,0]
	v_pk_mul_f32 v[24:25], v[24:25], s[28:29] op_sel_hi:[1,0]
	v_pk_mul_f32 v[26:27], v[26:27], s[28:29] op_sel_hi:[1,0]
	v_pk_mul_f32 v[28:29], v[28:29], s[28:29] op_sel_hi:[1,0]
	v_pk_mul_f32 v[30:31], v[30:31], s[28:29] op_sel_hi:[1,0]
	v_pk_mul_f32 v[32:33], v[32:33], s[28:29] op_sel_hi:[1,0]
	s_waitcnt vmcnt(0)
	global_load_dwordx4 v[50:53], v102, s[0:1]
	s_add_u32 s0, s0, 0x8000
	s_addc_u32 s1, s1, 0
	global_load_dwordx4 v[58:61], v102, s[8:9]
	s_add_u32 s8, s8, 0x8000
	s_addc_u32 s9, s9, 0
	global_load_dwordx2 v[62:63], v103, s[2:3]
	s_add_u32 s2, s2, 0x8000
	s_addc_u32 s3, s3, 0
	global_load_dwordx4 v[54:57], v102, s[0:1]
	s_add_u32 s0, s0, 0x8000
	s_addc_u32 s1, s1, 0
	global_load_dwordx2 v[64:65], v103, s[2:3]
	s_add_u32 s2, s2, 0x8000
	s_addc_u32 s3, s3, 0
	s_waitcnt lgkmcnt(0)
	s_load_dwordx16 s[64:79], s[24:25], 0x80
	s_load_dwordx16 s[80:95], s[24:25], 0xc0
	v_cvt_f32_f16_e32 v113, v42
	v_mul_f32_e32 v112, v34, v113
	v_pk_mul_f32 v[104:105], v[34:35], v[2:3] op_sel_hi:[0,1]
	v_pk_mul_f32 v[106:107], v[34:35], v[4:5] op_sel_hi:[0,1]
	v_exp_f32_e32 v104, v104
	v_exp_f32_e32 v105, v105
	v_exp_f32_e32 v106, v106
	v_pk_mul_f32 v[104:105], v[18:19], v[104:105]
	v_exp_f32_e32 v107, v107
	v_pk_fma_f32 v[18:19], v[112:113], s[32:33], v[104:105] op_sel_hi:[0,1,1]
	v_pk_mul_f32 v[106:107], v[20:21], v[106:107]
	v_pk_fma_f32 v[114:115], s[48:49], v[18:19], 0 op_sel_hi:[1,1,0]
	v_pk_fma_f32 v[20:21], v[112:113], s[34:35], v[106:107] op_sel_hi:[0,1,1]
	v_pk_mul_f32 v[108:109], v[34:35], v[6:7] op_sel_hi:[0,1]
	v_pk_fma_f32 v[114:115], s[50:51], v[20:21], v[114:115]
	v_exp_f32_e32 v108, v108
	v_exp_f32_e32 v109, v109
	v_pk_mul_f32 v[110:111], v[34:35], v[8:9] op_sel_hi:[0,1]
	v_pk_mul_f32 v[108:109], v[22:23], v[108:109]
	v_exp_f32_e32 v110, v110
	v_pk_fma_f32 v[22:23], v[112:113], s[36:37], v[108:109] op_sel_hi:[0,1,1]
	v_exp_f32_e32 v111, v111
	v_pk_fma_f32 v[114:115], s[52:53], v[22:23], v[114:115]
	v_pk_mul_f32 v[110:111], v[24:25], v[110:111]
	v_pk_mul_f32 v[104:105], v[34:35], v[10:11] op_sel_hi:[0,1]
	v_pk_fma_f32 v[24:25], v[112:113], s[38:39], v[110:111] op_sel_hi:[0,1,1]
	v_exp_f32_e32 v104, v104
	v_pk_fma_f32 v[114:115], s[54:55], v[24:25], v[114:115]
	v_exp_f32_e32 v105, v105
	v_pk_mul_f32 v[106:107], v[34:35], v[12:13] op_sel_hi:[0,1]
	v_pk_mul_f32 v[104:105], v[26:27], v[104:105]
	v_exp_f32_e32 v106, v106
	v_pk_fma_f32 v[26:27], v[112:113], s[40:41], v[104:105] op_sel_hi:[0,1,1]
	v_exp_f32_e32 v107, v107
	v_pk_fma_f32 v[114:115], s[56:57], v[26:27], v[114:115]
	v_pk_mul_f32 v[106:107], v[28:29], v[106:107]
	v_pk_mul_f32 v[108:109], v[34:35], v[14:15] op_sel_hi:[0,1]
	v_pk_fma_f32 v[28:29], v[112:113], s[42:43], v[106:107] op_sel_hi:[0,1,1]
	v_exp_f32_e32 v108, v108
	v_pk_fma_f32 v[114:115], s[58:59], v[28:29], v[114:115]
	v_exp_f32_e32 v109, v109
	v_pk_mul_f32 v[110:111], v[34:35], v[16:17] op_sel_hi:[0,1]
	v_pk_mul_f32 v[108:109], v[30:31], v[108:109]
	v_exp_f32_e32 v110, v110
	v_pk_fma_f32 v[30:31], v[112:113], s[44:45], v[108:109] op_sel_hi:[0,1,1]
	v_exp_f32_e32 v111, v111
	v_pk_fma_f32 v[114:115], s[60:61], v[30:31], v[114:115]
	v_pk_mul_f32 v[110:111], v[32:33], v[110:111]
	v_cvt_f32_f16_e32 v117, v46
	v_pk_fma_f32 v[32:33], v[112:113], s[46:47], v[110:111] op_sel_hi:[0,1,1]
	s_nop 0
	v_pk_fma_f32 v[114:115], s[62:63], v[32:33], v[114:115]
	s_nop 0
	v_add_f32_e32 v116, v114, v115
	v_fmac_f32_e32 v116, v98, v113
	v_mul_f32_e32 v116, v116, v117
	v_fma_mixlo_f16 v116, v116, s30, 0
	global_store_short v99, v116, s[26:27]
	s_add_u32 s26, s26, 0x1000
	s_addc_u32 s27, s27, 0
	s_waitcnt lgkmcnt(0)
	s_load_dwordx16 s[32:47], s[24:25], 0x100
	s_load_dwordx16 s[48:63], s[24:25], 0x140
	v_cvt_f32_f16_sdwa v113, v42 dst_sel:DWORD dst_unused:UNUSED_PAD src0_sel:WORD_1
	v_pk_mul_f32 v[104:105], v[34:35], v[2:3] op_sel:[1,0]
	v_mul_f32_e32 v112, v35, v113
	v_exp_f32_e32 v104, v104
	v_exp_f32_e32 v105, v105
	v_pk_mul_f32 v[106:107], v[34:35], v[4:5] op_sel:[1,0]
	v_pk_mul_f32 v[104:105], v[18:19], v[104:105]
	v_exp_f32_e32 v106, v106
	v_pk_fma_f32 v[18:19], v[112:113], s[64:65], v[104:105] op_sel_hi:[0,1,1]
	v_exp_f32_e32 v107, v107
	v_pk_fma_f32 v[114:115], s[80:81], v[18:19], 0 op_sel_hi:[1,1,0]
	v_pk_mul_f32 v[106:107], v[20:21], v[106:107]
	v_pk_mul_f32 v[108:109], v[34:35], v[6:7] op_sel:[1,0]
	v_pk_fma_f32 v[20:21], v[112:113], s[66:67], v[106:107] op_sel_hi:[0,1,1]
	v_exp_f32_e32 v108, v108
	v_pk_fma_f32 v[114:115], s[82:83], v[20:21], v[114:115]
	v_exp_f32_e32 v109, v109
	v_pk_mul_f32 v[110:111], v[34:35], v[8:9] op_sel:[1,0]
	v_pk_mul_f32 v[108:109], v[22:23], v[108:109]
	v_exp_f32_e32 v110, v110
	v_pk_fma_f32 v[22:23], v[112:113], s[68:69], v[108:109] op_sel_hi:[0,1,1]
	v_exp_f32_e32 v111, v111
	v_pk_fma_f32 v[114:115], s[84:85], v[22:23], v[114:115]
	v_pk_mul_f32 v[110:111], v[24:25], v[110:111]
	v_pk_mul_f32 v[104:105], v[34:35], v[10:11] op_sel:[1,0]
	v_pk_fma_f32 v[24:25], v[112:113], s[70:71], v[110:111] op_sel_hi:[0,1,1]
	v_exp_f32_e32 v104, v104
	v_pk_fma_f32 v[114:115], s[86:87], v[24:25], v[114:115]
	v_exp_f32_e32 v105, v105
	v_pk_mul_f32 v[106:107], v[34:35], v[12:13] op_sel:[1,0]
	v_pk_mul_f32 v[104:105], v[26:27], v[104:105]
	v_exp_f32_e32 v106, v106
	v_pk_fma_f32 v[26:27], v[112:113], s[72:73], v[104:105] op_sel_hi:[0,1,1]
	v_exp_f32_e32 v107, v107
	v_pk_fma_f32 v[114:115], s[88:89], v[26:27], v[114:115]
	v_pk_mul_f32 v[106:107], v[28:29], v[106:107]
	v_pk_mul_f32 v[108:109], v[34:35], v[14:15] op_sel:[1,0]
	v_pk_fma_f32 v[28:29], v[112:113], s[74:75], v[106:107] op_sel_hi:[0,1,1]
	v_exp_f32_e32 v108, v108
	v_pk_fma_f32 v[114:115], s[90:91], v[28:29], v[114:115]
	v_exp_f32_e32 v109, v109
	v_pk_mul_f32 v[110:111], v[34:35], v[16:17] op_sel:[1,0]
	v_pk_mul_f32 v[108:109], v[30:31], v[108:109]
	v_exp_f32_e32 v110, v110
	v_pk_fma_f32 v[30:31], v[112:113], s[76:77], v[108:109] op_sel_hi:[0,1,1]
	v_exp_f32_e32 v111, v111
	v_pk_fma_f32 v[114:115], s[92:93], v[30:31], v[114:115]
	v_pk_mul_f32 v[110:111], v[32:33], v[110:111]
	v_cvt_f32_f16_sdwa v117, v46 dst_sel:DWORD dst_unused:UNUSED_PAD src0_sel:WORD_1
	v_pk_fma_f32 v[32:33], v[112:113], s[78:79], v[110:111] op_sel_hi:[0,1,1]
	s_nop 0
	v_pk_fma_f32 v[114:115], s[94:95], v[32:33], v[114:115]
	s_nop 0
	v_add_f32_e32 v116, v114, v115
	v_fmac_f32_e32 v116, v98, v113
	v_mul_f32_e32 v116, v116, v117
	v_fma_mixlo_f16 v116, v116, s30, 0
	global_store_short v99, v116, s[26:27]
	s_add_u32 s26, s26, 0x1000
	s_addc_u32 s27, s27, 0
	s_waitcnt lgkmcnt(0)
	s_load_dwordx16 s[64:79], s[24:25], 0x180
	s_load_dwordx16 s[80:95], s[24:25], 0x1c0
	v_cvt_f32_f16_e32 v113, v43
	v_mul_f32_e32 v112, v36, v113
	v_pk_mul_f32 v[104:105], v[36:37], v[2:3] op_sel_hi:[0,1]
	v_pk_mul_f32 v[106:107], v[36:37], v[4:5] op_sel_hi:[0,1]
	v_exp_f32_e32 v104, v104
	v_exp_f32_e32 v105, v105
	v_exp_f32_e32 v106, v106
	v_pk_mul_f32 v[104:105], v[18:19], v[104:105]
	v_exp_f32_e32 v107, v107
	v_pk_fma_f32 v[18:19], v[112:113], s[32:33], v[104:105] op_sel_hi:[0,1,1]
	v_pk_mul_f32 v[106:107], v[20:21], v[106:107]
	v_pk_fma_f32 v[114:115], s[48:49], v[18:19], 0 op_sel_hi:[1,1,0]
	v_pk_fma_f32 v[20:21], v[112:113], s[34:35], v[106:107] op_sel_hi:[0,1,1]
	v_pk_mul_f32 v[108:109], v[36:37], v[6:7] op_sel_hi:[0,1]
	v_pk_fma_f32 v[114:115], s[50:51], v[20:21], v[114:115]
	v_exp_f32_e32 v108, v108
	v_exp_f32_e32 v109, v109
	v_pk_mul_f32 v[110:111], v[36:37], v[8:9] op_sel_hi:[0,1]
	v_pk_mul_f32 v[108:109], v[22:23], v[108:109]
	v_exp_f32_e32 v110, v110
	v_pk_fma_f32 v[22:23], v[112:113], s[36:37], v[108:109] op_sel_hi:[0,1,1]
	v_exp_f32_e32 v111, v111
	v_pk_fma_f32 v[114:115], s[52:53], v[22:23], v[114:115]
	v_pk_mul_f32 v[110:111], v[24:25], v[110:111]
	v_pk_mul_f32 v[104:105], v[36:37], v[10:11] op_sel_hi:[0,1]
	v_pk_fma_f32 v[24:25], v[112:113], s[38:39], v[110:111] op_sel_hi:[0,1,1]
	v_exp_f32_e32 v104, v104
	v_pk_fma_f32 v[114:115], s[54:55], v[24:25], v[114:115]
	v_exp_f32_e32 v105, v105
	v_pk_mul_f32 v[106:107], v[36:37], v[12:13] op_sel_hi:[0,1]
	v_pk_mul_f32 v[104:105], v[26:27], v[104:105]
	v_exp_f32_e32 v106, v106
	v_pk_fma_f32 v[26:27], v[112:113], s[40:41], v[104:105] op_sel_hi:[0,1,1]
	v_exp_f32_e32 v107, v107
	v_pk_fma_f32 v[114:115], s[56:57], v[26:27], v[114:115]
	v_pk_mul_f32 v[106:107], v[28:29], v[106:107]
	v_pk_mul_f32 v[108:109], v[36:37], v[14:15] op_sel_hi:[0,1]
	v_pk_fma_f32 v[28:29], v[112:113], s[42:43], v[106:107] op_sel_hi:[0,1,1]
	v_exp_f32_e32 v108, v108
	v_pk_fma_f32 v[114:115], s[58:59], v[28:29], v[114:115]
	v_exp_f32_e32 v109, v109
	v_pk_mul_f32 v[110:111], v[36:37], v[16:17] op_sel_hi:[0,1]
	v_pk_mul_f32 v[108:109], v[30:31], v[108:109]
	v_exp_f32_e32 v110, v110
	v_pk_fma_f32 v[30:31], v[112:113], s[44:45], v[108:109] op_sel_hi:[0,1,1]
	v_exp_f32_e32 v111, v111
	v_pk_fma_f32 v[114:115], s[60:61], v[30:31], v[114:115]
	v_pk_mul_f32 v[110:111], v[32:33], v[110:111]
	v_cvt_f32_f16_e32 v117, v47
	v_pk_fma_f32 v[32:33], v[112:113], s[46:47], v[110:111] op_sel_hi:[0,1,1]
	s_nop 0
	v_pk_fma_f32 v[114:115], s[62:63], v[32:33], v[114:115]
	s_nop 0
	v_add_f32_e32 v116, v114, v115
	v_fmac_f32_e32 v116, v98, v113
	v_mul_f32_e32 v116, v116, v117
	v_fma_mixlo_f16 v116, v116, s30, 0
	global_store_short v99, v116, s[26:27]
	s_add_u32 s26, s26, 0x1000
	s_addc_u32 s27, s27, 0
	s_waitcnt lgkmcnt(0)
	s_load_dwordx16 s[32:47], s[24:25], 0x200
	s_load_dwordx16 s[48:63], s[24:25], 0x240
	v_cvt_f32_f16_sdwa v113, v43 dst_sel:DWORD dst_unused:UNUSED_PAD src0_sel:WORD_1
	v_pk_mul_f32 v[104:105], v[36:37], v[2:3] op_sel:[1,0]
	v_mul_f32_e32 v112, v37, v113
	v_exp_f32_e32 v104, v104
	v_exp_f32_e32 v105, v105
	v_pk_mul_f32 v[106:107], v[36:37], v[4:5] op_sel:[1,0]
	v_pk_mul_f32 v[104:105], v[18:19], v[104:105]
	v_exp_f32_e32 v106, v106
	v_pk_fma_f32 v[18:19], v[112:113], s[64:65], v[104:105] op_sel_hi:[0,1,1]
	v_exp_f32_e32 v107, v107
	v_pk_fma_f32 v[114:115], s[80:81], v[18:19], 0 op_sel_hi:[1,1,0]
	v_pk_mul_f32 v[106:107], v[20:21], v[106:107]
	v_pk_mul_f32 v[108:109], v[36:37], v[6:7] op_sel:[1,0]
	v_pk_fma_f32 v[20:21], v[112:113], s[66:67], v[106:107] op_sel_hi:[0,1,1]
	v_exp_f32_e32 v108, v108
	v_pk_fma_f32 v[114:115], s[82:83], v[20:21], v[114:115]
	v_exp_f32_e32 v109, v109
	v_pk_mul_f32 v[110:111], v[36:37], v[8:9] op_sel:[1,0]
	v_pk_mul_f32 v[108:109], v[22:23], v[108:109]
	v_exp_f32_e32 v110, v110
	v_pk_fma_f32 v[22:23], v[112:113], s[68:69], v[108:109] op_sel_hi:[0,1,1]
	v_exp_f32_e32 v111, v111
	v_pk_fma_f32 v[114:115], s[84:85], v[22:23], v[114:115]
	v_pk_mul_f32 v[110:111], v[24:25], v[110:111]
	v_pk_mul_f32 v[104:105], v[36:37], v[10:11] op_sel:[1,0]
	v_pk_fma_f32 v[24:25], v[112:113], s[70:71], v[110:111] op_sel_hi:[0,1,1]
	v_exp_f32_e32 v104, v104
	v_pk_fma_f32 v[114:115], s[86:87], v[24:25], v[114:115]
	v_exp_f32_e32 v105, v105
	v_pk_mul_f32 v[106:107], v[36:37], v[12:13] op_sel:[1,0]
	v_pk_mul_f32 v[104:105], v[26:27], v[104:105]
	v_exp_f32_e32 v106, v106
	v_pk_fma_f32 v[26:27], v[112:113], s[72:73], v[104:105] op_sel_hi:[0,1,1]
	v_exp_f32_e32 v107, v107
	v_pk_fma_f32 v[114:115], s[88:89], v[26:27], v[114:115]
	v_pk_mul_f32 v[106:107], v[28:29], v[106:107]
	v_pk_mul_f32 v[108:109], v[36:37], v[14:15] op_sel:[1,0]
	v_pk_fma_f32 v[28:29], v[112:113], s[74:75], v[106:107] op_sel_hi:[0,1,1]
	v_exp_f32_e32 v108, v108
	v_pk_fma_f32 v[114:115], s[90:91], v[28:29], v[114:115]
	v_exp_f32_e32 v109, v109
	v_pk_mul_f32 v[110:111], v[36:37], v[16:17] op_sel:[1,0]
	v_pk_mul_f32 v[108:109], v[30:31], v[108:109]
	v_exp_f32_e32 v110, v110
	v_pk_fma_f32 v[30:31], v[112:113], s[76:77], v[108:109] op_sel_hi:[0,1,1]
	v_exp_f32_e32 v111, v111
	v_pk_fma_f32 v[114:115], s[92:93], v[30:31], v[114:115]
	v_pk_mul_f32 v[110:111], v[32:33], v[110:111]
	v_cvt_f32_f16_sdwa v117, v47 dst_sel:DWORD dst_unused:UNUSED_PAD src0_sel:WORD_1
	v_pk_fma_f32 v[32:33], v[112:113], s[78:79], v[110:111] op_sel_hi:[0,1,1]
	s_nop 0
	v_pk_fma_f32 v[114:115], s[94:95], v[32:33], v[114:115]
	s_nop 0
	v_add_f32_e32 v116, v114, v115
	v_fmac_f32_e32 v116, v98, v113
	v_mul_f32_e32 v116, v116, v117
	v_fma_mixlo_f16 v116, v116, s30, 0
	global_store_short v99, v116, s[26:27]
	s_add_u32 s26, s26, 0x1000
	s_addc_u32 s27, s27, 0
	s_waitcnt lgkmcnt(0)
	s_load_dwordx16 s[64:79], s[24:25], 0x280
	s_load_dwordx16 s[80:95], s[24:25], 0x2c0
	v_cvt_f32_f16_e32 v113, v44
	v_mul_f32_e32 v112, v38, v113
	v_pk_mul_f32 v[104:105], v[38:39], v[2:3] op_sel_hi:[0,1]
	v_pk_mul_f32 v[106:107], v[38:39], v[4:5] op_sel_hi:[0,1]
	v_exp_f32_e32 v104, v104
	v_exp_f32_e32 v105, v105
	v_exp_f32_e32 v106, v106
	v_pk_mul_f32 v[104:105], v[18:19], v[104:105]
	v_exp_f32_e32 v107, v107
	v_pk_fma_f32 v[18:19], v[112:113], s[32:33], v[104:105] op_sel_hi:[0,1,1]
	v_pk_mul_f32 v[106:107], v[20:21], v[106:107]
	v_pk_fma_f32 v[114:115], s[48:49], v[18:19], 0 op_sel_hi:[1,1,0]
	v_pk_fma_f32 v[20:21], v[112:113], s[34:35], v[106:107] op_sel_hi:[0,1,1]
	v_pk_mul_f32 v[108:109], v[38:39], v[6:7] op_sel_hi:[0,1]
	v_pk_fma_f32 v[114:115], s[50:51], v[20:21], v[114:115]
	v_exp_f32_e32 v108, v108
	v_exp_f32_e32 v109, v109
	v_pk_mul_f32 v[110:111], v[38:39], v[8:9] op_sel_hi:[0,1]
	v_pk_mul_f32 v[108:109], v[22:23], v[108:109]
	v_exp_f32_e32 v110, v110
	v_pk_fma_f32 v[22:23], v[112:113], s[36:37], v[108:109] op_sel_hi:[0,1,1]
	v_exp_f32_e32 v111, v111
	v_pk_fma_f32 v[114:115], s[52:53], v[22:23], v[114:115]
	v_pk_mul_f32 v[110:111], v[24:25], v[110:111]
	v_pk_mul_f32 v[104:105], v[38:39], v[10:11] op_sel_hi:[0,1]
	v_pk_fma_f32 v[24:25], v[112:113], s[38:39], v[110:111] op_sel_hi:[0,1,1]
	v_exp_f32_e32 v104, v104
	v_pk_fma_f32 v[114:115], s[54:55], v[24:25], v[114:115]
	v_exp_f32_e32 v105, v105
	v_pk_mul_f32 v[106:107], v[38:39], v[12:13] op_sel_hi:[0,1]
	v_pk_mul_f32 v[104:105], v[26:27], v[104:105]
	v_exp_f32_e32 v106, v106
	v_pk_fma_f32 v[26:27], v[112:113], s[40:41], v[104:105] op_sel_hi:[0,1,1]
	v_exp_f32_e32 v107, v107
	v_pk_fma_f32 v[114:115], s[56:57], v[26:27], v[114:115]
	v_pk_mul_f32 v[106:107], v[28:29], v[106:107]
	v_pk_mul_f32 v[108:109], v[38:39], v[14:15] op_sel_hi:[0,1]
	v_pk_fma_f32 v[28:29], v[112:113], s[42:43], v[106:107] op_sel_hi:[0,1,1]
	v_exp_f32_e32 v108, v108
	v_pk_fma_f32 v[114:115], s[58:59], v[28:29], v[114:115]
	v_exp_f32_e32 v109, v109
	v_pk_mul_f32 v[110:111], v[38:39], v[16:17] op_sel_hi:[0,1]
	v_pk_mul_f32 v[108:109], v[30:31], v[108:109]
	v_exp_f32_e32 v110, v110
	v_pk_fma_f32 v[30:31], v[112:113], s[44:45], v[108:109] op_sel_hi:[0,1,1]
	v_exp_f32_e32 v111, v111
	v_pk_fma_f32 v[114:115], s[60:61], v[30:31], v[114:115]
	v_pk_mul_f32 v[110:111], v[32:33], v[110:111]
	v_cvt_f32_f16_e32 v117, v48
	v_pk_fma_f32 v[32:33], v[112:113], s[46:47], v[110:111] op_sel_hi:[0,1,1]
	s_nop 0
	v_pk_fma_f32 v[114:115], s[62:63], v[32:33], v[114:115]
	s_nop 0
	v_add_f32_e32 v116, v114, v115
	v_fmac_f32_e32 v116, v98, v113
	v_mul_f32_e32 v116, v116, v117
	v_fma_mixlo_f16 v116, v116, s30, 0
	global_store_short v99, v116, s[26:27]
	s_add_u32 s26, s26, 0x1000
	s_addc_u32 s27, s27, 0
	s_waitcnt lgkmcnt(0)
	s_load_dwordx16 s[32:47], s[24:25], 0x300
	s_load_dwordx16 s[48:63], s[24:25], 0x340
	v_cvt_f32_f16_sdwa v113, v44 dst_sel:DWORD dst_unused:UNUSED_PAD src0_sel:WORD_1
	v_pk_mul_f32 v[104:105], v[38:39], v[2:3] op_sel:[1,0]
	v_mul_f32_e32 v112, v39, v113
	v_exp_f32_e32 v104, v104
	v_exp_f32_e32 v105, v105
	v_pk_mul_f32 v[106:107], v[38:39], v[4:5] op_sel:[1,0]
	v_pk_mul_f32 v[104:105], v[18:19], v[104:105]
	v_exp_f32_e32 v106, v106
	v_pk_fma_f32 v[18:19], v[112:113], s[64:65], v[104:105] op_sel_hi:[0,1,1]
	v_exp_f32_e32 v107, v107
	v_pk_fma_f32 v[114:115], s[80:81], v[18:19], 0 op_sel_hi:[1,1,0]
	v_pk_mul_f32 v[106:107], v[20:21], v[106:107]
	v_pk_mul_f32 v[108:109], v[38:39], v[6:7] op_sel:[1,0]
	v_pk_fma_f32 v[20:21], v[112:113], s[66:67], v[106:107] op_sel_hi:[0,1,1]
	v_exp_f32_e32 v108, v108
	v_pk_fma_f32 v[114:115], s[82:83], v[20:21], v[114:115]
	v_exp_f32_e32 v109, v109
	v_pk_mul_f32 v[110:111], v[38:39], v[8:9] op_sel:[1,0]
	v_pk_mul_f32 v[108:109], v[22:23], v[108:109]
	v_exp_f32_e32 v110, v110
	v_pk_fma_f32 v[22:23], v[112:113], s[68:69], v[108:109] op_sel_hi:[0,1,1]
	v_exp_f32_e32 v111, v111
	v_pk_fma_f32 v[114:115], s[84:85], v[22:23], v[114:115]
	v_pk_mul_f32 v[110:111], v[24:25], v[110:111]
	v_pk_mul_f32 v[104:105], v[38:39], v[10:11] op_sel:[1,0]
	v_pk_fma_f32 v[24:25], v[112:113], s[70:71], v[110:111] op_sel_hi:[0,1,1]
	v_exp_f32_e32 v104, v104
	v_pk_fma_f32 v[114:115], s[86:87], v[24:25], v[114:115]
	v_exp_f32_e32 v105, v105
	v_pk_mul_f32 v[106:107], v[38:39], v[12:13] op_sel:[1,0]
	v_pk_mul_f32 v[104:105], v[26:27], v[104:105]
	v_exp_f32_e32 v106, v106
	v_pk_fma_f32 v[26:27], v[112:113], s[72:73], v[104:105] op_sel_hi:[0,1,1]
	v_exp_f32_e32 v107, v107
	v_pk_fma_f32 v[114:115], s[88:89], v[26:27], v[114:115]
	v_pk_mul_f32 v[106:107], v[28:29], v[106:107]
	v_pk_mul_f32 v[108:109], v[38:39], v[14:15] op_sel:[1,0]
	v_pk_fma_f32 v[28:29], v[112:113], s[74:75], v[106:107] op_sel_hi:[0,1,1]
	v_exp_f32_e32 v108, v108
	v_pk_fma_f32 v[114:115], s[90:91], v[28:29], v[114:115]
	v_exp_f32_e32 v109, v109
	v_pk_mul_f32 v[110:111], v[38:39], v[16:17] op_sel:[1,0]
	v_pk_mul_f32 v[108:109], v[30:31], v[108:109]
	v_exp_f32_e32 v110, v110
	v_pk_fma_f32 v[30:31], v[112:113], s[76:77], v[108:109] op_sel_hi:[0,1,1]
	v_exp_f32_e32 v111, v111
	v_pk_fma_f32 v[114:115], s[92:93], v[30:31], v[114:115]
	v_pk_mul_f32 v[110:111], v[32:33], v[110:111]
	v_cvt_f32_f16_sdwa v117, v48 dst_sel:DWORD dst_unused:UNUSED_PAD src0_sel:WORD_1
	v_pk_fma_f32 v[32:33], v[112:113], s[78:79], v[110:111] op_sel_hi:[0,1,1]
	s_nop 0
	v_pk_fma_f32 v[114:115], s[94:95], v[32:33], v[114:115]
	s_nop 0
	v_add_f32_e32 v116, v114, v115
	v_fmac_f32_e32 v116, v98, v113
	v_mul_f32_e32 v116, v116, v117
	v_fma_mixlo_f16 v116, v116, s30, 0
	global_store_short v99, v116, s[26:27]
	s_add_u32 s26, s26, 0x1000
	s_addc_u32 s27, s27, 0
	s_waitcnt lgkmcnt(0)
	s_load_dwordx16 s[64:79], s[24:25], 0x380
	s_load_dwordx16 s[80:95], s[24:25], 0x3c0
	v_cvt_f32_f16_e32 v113, v45
	v_mul_f32_e32 v112, v40, v113
	v_pk_mul_f32 v[104:105], v[40:41], v[2:3] op_sel_hi:[0,1]
	v_pk_mul_f32 v[106:107], v[40:41], v[4:5] op_sel_hi:[0,1]
	v_exp_f32_e32 v104, v104
	v_exp_f32_e32 v105, v105
	v_exp_f32_e32 v106, v106
	v_pk_mul_f32 v[104:105], v[18:19], v[104:105]
	v_exp_f32_e32 v107, v107
	v_pk_fma_f32 v[18:19], v[112:113], s[32:33], v[104:105] op_sel_hi:[0,1,1]
	v_pk_mul_f32 v[106:107], v[20:21], v[106:107]
	v_pk_fma_f32 v[114:115], s[48:49], v[18:19], 0 op_sel_hi:[1,1,0]
	v_pk_fma_f32 v[20:21], v[112:113], s[34:35], v[106:107] op_sel_hi:[0,1,1]
	v_pk_mul_f32 v[108:109], v[40:41], v[6:7] op_sel_hi:[0,1]
	v_pk_fma_f32 v[114:115], s[50:51], v[20:21], v[114:115]
	v_exp_f32_e32 v108, v108
	v_exp_f32_e32 v109, v109
	v_pk_mul_f32 v[110:111], v[40:41], v[8:9] op_sel_hi:[0,1]
	v_pk_mul_f32 v[108:109], v[22:23], v[108:109]
	v_exp_f32_e32 v110, v110
	v_pk_fma_f32 v[22:23], v[112:113], s[36:37], v[108:109] op_sel_hi:[0,1,1]
	v_exp_f32_e32 v111, v111
	v_pk_fma_f32 v[114:115], s[52:53], v[22:23], v[114:115]
	v_pk_mul_f32 v[110:111], v[24:25], v[110:111]
	v_pk_mul_f32 v[104:105], v[40:41], v[10:11] op_sel_hi:[0,1]
	v_pk_fma_f32 v[24:25], v[112:113], s[38:39], v[110:111] op_sel_hi:[0,1,1]
	v_exp_f32_e32 v104, v104
	v_pk_fma_f32 v[114:115], s[54:55], v[24:25], v[114:115]
	v_exp_f32_e32 v105, v105
	v_pk_mul_f32 v[106:107], v[40:41], v[12:13] op_sel_hi:[0,1]
	v_pk_mul_f32 v[104:105], v[26:27], v[104:105]
	v_exp_f32_e32 v106, v106
	v_pk_fma_f32 v[26:27], v[112:113], s[40:41], v[104:105] op_sel_hi:[0,1,1]
	v_exp_f32_e32 v107, v107
	v_pk_fma_f32 v[114:115], s[56:57], v[26:27], v[114:115]
	v_pk_mul_f32 v[106:107], v[28:29], v[106:107]
	v_pk_mul_f32 v[108:109], v[40:41], v[14:15] op_sel_hi:[0,1]
	v_pk_fma_f32 v[28:29], v[112:113], s[42:43], v[106:107] op_sel_hi:[0,1,1]
	v_exp_f32_e32 v108, v108
	v_pk_fma_f32 v[114:115], s[58:59], v[28:29], v[114:115]
	v_exp_f32_e32 v109, v109
	v_pk_mul_f32 v[110:111], v[40:41], v[16:17] op_sel_hi:[0,1]
	v_pk_mul_f32 v[108:109], v[30:31], v[108:109]
	v_exp_f32_e32 v110, v110
	v_pk_fma_f32 v[30:31], v[112:113], s[44:45], v[108:109] op_sel_hi:[0,1,1]
	v_exp_f32_e32 v111, v111
	v_pk_fma_f32 v[114:115], s[60:61], v[30:31], v[114:115]
	v_pk_mul_f32 v[110:111], v[32:33], v[110:111]
	v_cvt_f32_f16_e32 v117, v49
	v_pk_fma_f32 v[32:33], v[112:113], s[46:47], v[110:111] op_sel_hi:[0,1,1]
	s_nop 0
	v_pk_fma_f32 v[114:115], s[62:63], v[32:33], v[114:115]
	s_nop 0
	v_add_f32_e32 v116, v114, v115
	v_fmac_f32_e32 v116, v98, v113
	v_mul_f32_e32 v116, v116, v117
	v_fma_mixlo_f16 v116, v116, s30, 0
	global_store_short v99, v116, s[26:27]
	s_add_u32 s26, s26, 0x1000
	s_addc_u32 s27, s27, 0
	s_waitcnt lgkmcnt(0)
	s_load_dwordx16 s[32:47], s[24:25], 0x400
	s_load_dwordx16 s[48:63], s[24:25], 0x440
	v_cvt_f32_f16_sdwa v113, v45 dst_sel:DWORD dst_unused:UNUSED_PAD src0_sel:WORD_1
	v_pk_mul_f32 v[104:105], v[40:41], v[2:3] op_sel:[1,0]
	v_mul_f32_e32 v112, v41, v113
	v_exp_f32_e32 v104, v104
	v_exp_f32_e32 v105, v105
	v_pk_mul_f32 v[106:107], v[40:41], v[4:5] op_sel:[1,0]
	v_pk_mul_f32 v[104:105], v[18:19], v[104:105]
	v_exp_f32_e32 v106, v106
	v_pk_fma_f32 v[18:19], v[112:113], s[64:65], v[104:105] op_sel_hi:[0,1,1]
	v_exp_f32_e32 v107, v107
	v_pk_fma_f32 v[114:115], s[80:81], v[18:19], 0 op_sel_hi:[1,1,0]
	v_pk_mul_f32 v[106:107], v[20:21], v[106:107]
	v_pk_mul_f32 v[108:109], v[40:41], v[6:7] op_sel:[1,0]
	v_pk_fma_f32 v[20:21], v[112:113], s[66:67], v[106:107] op_sel_hi:[0,1,1]
	v_exp_f32_e32 v108, v108
	v_pk_fma_f32 v[114:115], s[82:83], v[20:21], v[114:115]
	v_exp_f32_e32 v109, v109
	v_pk_mul_f32 v[110:111], v[40:41], v[8:9] op_sel:[1,0]
	v_pk_mul_f32 v[108:109], v[22:23], v[108:109]
	v_exp_f32_e32 v110, v110
	v_pk_fma_f32 v[22:23], v[112:113], s[68:69], v[108:109] op_sel_hi:[0,1,1]
	v_exp_f32_e32 v111, v111
	v_pk_fma_f32 v[114:115], s[84:85], v[22:23], v[114:115]
	v_pk_mul_f32 v[110:111], v[24:25], v[110:111]
	v_pk_mul_f32 v[104:105], v[40:41], v[10:11] op_sel:[1,0]
	v_pk_fma_f32 v[24:25], v[112:113], s[70:71], v[110:111] op_sel_hi:[0,1,1]
	v_exp_f32_e32 v104, v104
	v_pk_fma_f32 v[114:115], s[86:87], v[24:25], v[114:115]
	v_exp_f32_e32 v105, v105
	v_pk_mul_f32 v[106:107], v[40:41], v[12:13] op_sel:[1,0]
	v_pk_mul_f32 v[104:105], v[26:27], v[104:105]
	v_exp_f32_e32 v106, v106
	v_pk_fma_f32 v[26:27], v[112:113], s[72:73], v[104:105] op_sel_hi:[0,1,1]
	v_exp_f32_e32 v107, v107
	v_pk_fma_f32 v[114:115], s[88:89], v[26:27], v[114:115]
	v_pk_mul_f32 v[106:107], v[28:29], v[106:107]
	v_pk_mul_f32 v[108:109], v[40:41], v[14:15] op_sel:[1,0]
	v_pk_fma_f32 v[28:29], v[112:113], s[74:75], v[106:107] op_sel_hi:[0,1,1]
	v_exp_f32_e32 v108, v108
	v_pk_fma_f32 v[114:115], s[90:91], v[28:29], v[114:115]
	v_exp_f32_e32 v109, v109
	v_pk_mul_f32 v[110:111], v[40:41], v[16:17] op_sel:[1,0]
	v_pk_mul_f32 v[108:109], v[30:31], v[108:109]
	v_exp_f32_e32 v110, v110
	v_pk_fma_f32 v[30:31], v[112:113], s[76:77], v[108:109] op_sel_hi:[0,1,1]
	v_exp_f32_e32 v111, v111
	v_pk_fma_f32 v[114:115], s[92:93], v[30:31], v[114:115]
	v_pk_mul_f32 v[110:111], v[32:33], v[110:111]
	v_cvt_f32_f16_sdwa v117, v49 dst_sel:DWORD dst_unused:UNUSED_PAD src0_sel:WORD_1
	v_pk_fma_f32 v[32:33], v[112:113], s[78:79], v[110:111] op_sel_hi:[0,1,1]
	s_nop 0
	v_pk_fma_f32 v[114:115], s[94:95], v[32:33], v[114:115]
	s_nop 0
	v_add_f32_e32 v116, v114, v115
	v_fmac_f32_e32 v116, v98, v113
	v_mul_f32_e32 v116, v116, v117
	v_fma_mixlo_f16 v116, v116, s30, 0
	global_store_short v99, v116, s[26:27]
	s_add_u32 s26, s26, 0x1000
	s_addc_u32 s27, s27, 0
	s_waitcnt vmcnt(8)
	global_load_dwordx4 v[66:69], v102, s[0:1]
	s_add_u32 s0, s0, 0x8000
	s_addc_u32 s1, s1, 0
	global_load_dwordx4 v[74:77], v102, s[8:9]
	s_add_u32 s8, s8, 0x8000
	s_addc_u32 s9, s9, 0
	global_load_dwordx2 v[78:79], v103, s[2:3]
	s_add_u32 s2, s2, 0x8000
	s_addc_u32 s3, s3, 0
	global_load_dwordx4 v[70:73], v102, s[0:1]
	s_add_u32 s0, s0, 0x8000
	s_addc_u32 s1, s1, 0
	global_load_dwordx2 v[80:81], v103, s[2:3]
	s_add_u32 s2, s2, 0x8000
	s_addc_u32 s3, s3, 0
	s_waitcnt lgkmcnt(0)
	s_load_dwordx16 s[64:79], s[24:25], 0x480
	s_load_dwordx16 s[80:95], s[24:25], 0x4c0
	v_cvt_f32_f16_e32 v113, v58
	v_mul_f32_e32 v112, v50, v113
	v_pk_mul_f32 v[104:105], v[50:51], v[2:3] op_sel_hi:[0,1]
	v_pk_mul_f32 v[106:107], v[50:51], v[4:5] op_sel_hi:[0,1]
	v_exp_f32_e32 v104, v104
	v_exp_f32_e32 v105, v105
	v_exp_f32_e32 v106, v106
	v_pk_mul_f32 v[104:105], v[18:19], v[104:105]
	v_exp_f32_e32 v107, v107
	v_pk_fma_f32 v[18:19], v[112:113], s[32:33], v[104:105] op_sel_hi:[0,1,1]
	v_pk_mul_f32 v[106:107], v[20:21], v[106:107]
	v_pk_fma_f32 v[114:115], s[48:49], v[18:19], 0 op_sel_hi:[1,1,0]
	v_pk_fma_f32 v[20:21], v[112:113], s[34:35], v[106:107] op_sel_hi:[0,1,1]
	v_pk_mul_f32 v[108:109], v[50:51], v[6:7] op_sel_hi:[0,1]
	v_pk_fma_f32 v[114:115], s[50:51], v[20:21], v[114:115]
	v_exp_f32_e32 v108, v108
	v_exp_f32_e32 v109, v109
	v_pk_mul_f32 v[110:111], v[50:51], v[8:9] op_sel_hi:[0,1]
	v_pk_mul_f32 v[108:109], v[22:23], v[108:109]
	v_exp_f32_e32 v110, v110
	v_pk_fma_f32 v[22:23], v[112:113], s[36:37], v[108:109] op_sel_hi:[0,1,1]
	v_exp_f32_e32 v111, v111
	v_pk_fma_f32 v[114:115], s[52:53], v[22:23], v[114:115]
	v_pk_mul_f32 v[110:111], v[24:25], v[110:111]
	v_pk_mul_f32 v[104:105], v[50:51], v[10:11] op_sel_hi:[0,1]
	v_pk_fma_f32 v[24:25], v[112:113], s[38:39], v[110:111] op_sel_hi:[0,1,1]
	v_exp_f32_e32 v104, v104
	v_pk_fma_f32 v[114:115], s[54:55], v[24:25], v[114:115]
	v_exp_f32_e32 v105, v105
	v_pk_mul_f32 v[106:107], v[50:51], v[12:13] op_sel_hi:[0,1]
	v_pk_mul_f32 v[104:105], v[26:27], v[104:105]
	v_exp_f32_e32 v106, v106
	v_pk_fma_f32 v[26:27], v[112:113], s[40:41], v[104:105] op_sel_hi:[0,1,1]
	v_exp_f32_e32 v107, v107
	v_pk_fma_f32 v[114:115], s[56:57], v[26:27], v[114:115]
	v_pk_mul_f32 v[106:107], v[28:29], v[106:107]
	v_pk_mul_f32 v[108:109], v[50:51], v[14:15] op_sel_hi:[0,1]
	v_pk_fma_f32 v[28:29], v[112:113], s[42:43], v[106:107] op_sel_hi:[0,1,1]
	v_exp_f32_e32 v108, v108
	v_pk_fma_f32 v[114:115], s[58:59], v[28:29], v[114:115]
	v_exp_f32_e32 v109, v109
	v_pk_mul_f32 v[110:111], v[50:51], v[16:17] op_sel_hi:[0,1]
	v_pk_mul_f32 v[108:109], v[30:31], v[108:109]
	v_exp_f32_e32 v110, v110
	v_pk_fma_f32 v[30:31], v[112:113], s[44:45], v[108:109] op_sel_hi:[0,1,1]
	v_exp_f32_e32 v111, v111
	v_pk_fma_f32 v[114:115], s[60:61], v[30:31], v[114:115]
	v_pk_mul_f32 v[110:111], v[32:33], v[110:111]
	v_cvt_f32_f16_e32 v117, v62
	v_pk_fma_f32 v[32:33], v[112:113], s[46:47], v[110:111] op_sel_hi:[0,1,1]
	s_nop 0
	v_pk_fma_f32 v[114:115], s[62:63], v[32:33], v[114:115]
	s_nop 0
	v_add_f32_e32 v116, v114, v115
	v_fmac_f32_e32 v116, v98, v113
	v_mul_f32_e32 v116, v116, v117
	v_fma_mixlo_f16 v116, v116, s30, 0
	global_store_short v99, v116, s[26:27]
	s_add_u32 s26, s26, 0x1000
	s_addc_u32 s27, s27, 0
	s_waitcnt lgkmcnt(0)
	s_load_dwordx16 s[32:47], s[24:25], 0x500
	s_load_dwordx16 s[48:63], s[24:25], 0x540
	v_cvt_f32_f16_sdwa v113, v58 dst_sel:DWORD dst_unused:UNUSED_PAD src0_sel:WORD_1
	v_pk_mul_f32 v[104:105], v[50:51], v[2:3] op_sel:[1,0]
	v_mul_f32_e32 v112, v51, v113
	v_exp_f32_e32 v104, v104
	v_exp_f32_e32 v105, v105
	v_pk_mul_f32 v[106:107], v[50:51], v[4:5] op_sel:[1,0]
	v_pk_mul_f32 v[104:105], v[18:19], v[104:105]
	v_exp_f32_e32 v106, v106
	v_pk_fma_f32 v[18:19], v[112:113], s[64:65], v[104:105] op_sel_hi:[0,1,1]
	v_exp_f32_e32 v107, v107
	v_pk_fma_f32 v[114:115], s[80:81], v[18:19], 0 op_sel_hi:[1,1,0]
	v_pk_mul_f32 v[106:107], v[20:21], v[106:107]
	v_pk_mul_f32 v[108:109], v[50:51], v[6:7] op_sel:[1,0]
	v_pk_fma_f32 v[20:21], v[112:113], s[66:67], v[106:107] op_sel_hi:[0,1,1]
	v_exp_f32_e32 v108, v108
	v_pk_fma_f32 v[114:115], s[82:83], v[20:21], v[114:115]
	v_exp_f32_e32 v109, v109
	v_pk_mul_f32 v[110:111], v[50:51], v[8:9] op_sel:[1,0]
	v_pk_mul_f32 v[108:109], v[22:23], v[108:109]
	v_exp_f32_e32 v110, v110
	v_pk_fma_f32 v[22:23], v[112:113], s[68:69], v[108:109] op_sel_hi:[0,1,1]
	v_exp_f32_e32 v111, v111
	v_pk_fma_f32 v[114:115], s[84:85], v[22:23], v[114:115]
	v_pk_mul_f32 v[110:111], v[24:25], v[110:111]
	v_pk_mul_f32 v[104:105], v[50:51], v[10:11] op_sel:[1,0]
	v_pk_fma_f32 v[24:25], v[112:113], s[70:71], v[110:111] op_sel_hi:[0,1,1]
	v_exp_f32_e32 v104, v104
	v_pk_fma_f32 v[114:115], s[86:87], v[24:25], v[114:115]
	v_exp_f32_e32 v105, v105
	v_pk_mul_f32 v[106:107], v[50:51], v[12:13] op_sel:[1,0]
	v_pk_mul_f32 v[104:105], v[26:27], v[104:105]
	v_exp_f32_e32 v106, v106
	v_pk_fma_f32 v[26:27], v[112:113], s[72:73], v[104:105] op_sel_hi:[0,1,1]
	v_exp_f32_e32 v107, v107
	v_pk_fma_f32 v[114:115], s[88:89], v[26:27], v[114:115]
	v_pk_mul_f32 v[106:107], v[28:29], v[106:107]
	v_pk_mul_f32 v[108:109], v[50:51], v[14:15] op_sel:[1,0]
	v_pk_fma_f32 v[28:29], v[112:113], s[74:75], v[106:107] op_sel_hi:[0,1,1]
	v_exp_f32_e32 v108, v108
	v_pk_fma_f32 v[114:115], s[90:91], v[28:29], v[114:115]
	v_exp_f32_e32 v109, v109
	v_pk_mul_f32 v[110:111], v[50:51], v[16:17] op_sel:[1,0]
	v_pk_mul_f32 v[108:109], v[30:31], v[108:109]
	v_exp_f32_e32 v110, v110
	v_pk_fma_f32 v[30:31], v[112:113], s[76:77], v[108:109] op_sel_hi:[0,1,1]
	v_exp_f32_e32 v111, v111
	v_pk_fma_f32 v[114:115], s[92:93], v[30:31], v[114:115]
	v_pk_mul_f32 v[110:111], v[32:33], v[110:111]
	v_cvt_f32_f16_sdwa v117, v62 dst_sel:DWORD dst_unused:UNUSED_PAD src0_sel:WORD_1
	v_pk_fma_f32 v[32:33], v[112:113], s[78:79], v[110:111] op_sel_hi:[0,1,1]
	s_nop 0
	v_pk_fma_f32 v[114:115], s[94:95], v[32:33], v[114:115]
	s_nop 0
	v_add_f32_e32 v116, v114, v115
	v_fmac_f32_e32 v116, v98, v113
	v_mul_f32_e32 v116, v116, v117
	v_fma_mixlo_f16 v116, v116, s30, 0
	global_store_short v99, v116, s[26:27]
	s_add_u32 s26, s26, 0x1000
	s_addc_u32 s27, s27, 0
	s_waitcnt lgkmcnt(0)
	s_load_dwordx16 s[64:79], s[24:25], 0x580
	s_load_dwordx16 s[80:95], s[24:25], 0x5c0
	v_cvt_f32_f16_e32 v113, v59
	v_mul_f32_e32 v112, v52, v113
	v_pk_mul_f32 v[104:105], v[52:53], v[2:3] op_sel_hi:[0,1]
	v_pk_mul_f32 v[106:107], v[52:53], v[4:5] op_sel_hi:[0,1]
	v_exp_f32_e32 v104, v104
	v_exp_f32_e32 v105, v105
	v_exp_f32_e32 v106, v106
	v_pk_mul_f32 v[104:105], v[18:19], v[104:105]
	v_exp_f32_e32 v107, v107
	v_pk_fma_f32 v[18:19], v[112:113], s[32:33], v[104:105] op_sel_hi:[0,1,1]
	v_pk_mul_f32 v[106:107], v[20:21], v[106:107]
	v_pk_fma_f32 v[114:115], s[48:49], v[18:19], 0 op_sel_hi:[1,1,0]
	v_pk_fma_f32 v[20:21], v[112:113], s[34:35], v[106:107] op_sel_hi:[0,1,1]
	v_pk_mul_f32 v[108:109], v[52:53], v[6:7] op_sel_hi:[0,1]
	v_pk_fma_f32 v[114:115], s[50:51], v[20:21], v[114:115]
	v_exp_f32_e32 v108, v108
	v_exp_f32_e32 v109, v109
	v_pk_mul_f32 v[110:111], v[52:53], v[8:9] op_sel_hi:[0,1]
	v_pk_mul_f32 v[108:109], v[22:23], v[108:109]
	v_exp_f32_e32 v110, v110
	v_pk_fma_f32 v[22:23], v[112:113], s[36:37], v[108:109] op_sel_hi:[0,1,1]
	v_exp_f32_e32 v111, v111
	v_pk_fma_f32 v[114:115], s[52:53], v[22:23], v[114:115]
	v_pk_mul_f32 v[110:111], v[24:25], v[110:111]
	v_pk_mul_f32 v[104:105], v[52:53], v[10:11] op_sel_hi:[0,1]
	v_pk_fma_f32 v[24:25], v[112:113], s[38:39], v[110:111] op_sel_hi:[0,1,1]
	v_exp_f32_e32 v104, v104
	v_pk_fma_f32 v[114:115], s[54:55], v[24:25], v[114:115]
	v_exp_f32_e32 v105, v105
	v_pk_mul_f32 v[106:107], v[52:53], v[12:13] op_sel_hi:[0,1]
	v_pk_mul_f32 v[104:105], v[26:27], v[104:105]
	v_exp_f32_e32 v106, v106
	v_pk_fma_f32 v[26:27], v[112:113], s[40:41], v[104:105] op_sel_hi:[0,1,1]
	v_exp_f32_e32 v107, v107
	v_pk_fma_f32 v[114:115], s[56:57], v[26:27], v[114:115]
	v_pk_mul_f32 v[106:107], v[28:29], v[106:107]
	v_pk_mul_f32 v[108:109], v[52:53], v[14:15] op_sel_hi:[0,1]
	v_pk_fma_f32 v[28:29], v[112:113], s[42:43], v[106:107] op_sel_hi:[0,1,1]
	v_exp_f32_e32 v108, v108
	v_pk_fma_f32 v[114:115], s[58:59], v[28:29], v[114:115]
	v_exp_f32_e32 v109, v109
	v_pk_mul_f32 v[110:111], v[52:53], v[16:17] op_sel_hi:[0,1]
	v_pk_mul_f32 v[108:109], v[30:31], v[108:109]
	v_exp_f32_e32 v110, v110
	v_pk_fma_f32 v[30:31], v[112:113], s[44:45], v[108:109] op_sel_hi:[0,1,1]
	v_exp_f32_e32 v111, v111
	v_pk_fma_f32 v[114:115], s[60:61], v[30:31], v[114:115]
	v_pk_mul_f32 v[110:111], v[32:33], v[110:111]
	v_cvt_f32_f16_e32 v117, v63
	v_pk_fma_f32 v[32:33], v[112:113], s[46:47], v[110:111] op_sel_hi:[0,1,1]
	s_nop 0
	v_pk_fma_f32 v[114:115], s[62:63], v[32:33], v[114:115]
	s_nop 0
	v_add_f32_e32 v116, v114, v115
	v_fmac_f32_e32 v116, v98, v113
	v_mul_f32_e32 v116, v116, v117
	v_fma_mixlo_f16 v116, v116, s30, 0
	global_store_short v99, v116, s[26:27]
	s_add_u32 s26, s26, 0x1000
	s_addc_u32 s27, s27, 0
	s_waitcnt lgkmcnt(0)
	s_load_dwordx16 s[32:47], s[24:25], 0x600
	s_load_dwordx16 s[48:63], s[24:25], 0x640
	v_cvt_f32_f16_sdwa v113, v59 dst_sel:DWORD dst_unused:UNUSED_PAD src0_sel:WORD_1
	v_pk_mul_f32 v[104:105], v[52:53], v[2:3] op_sel:[1,0]
	v_mul_f32_e32 v112, v53, v113
	v_exp_f32_e32 v104, v104
	v_exp_f32_e32 v105, v105
	v_pk_mul_f32 v[106:107], v[52:53], v[4:5] op_sel:[1,0]
	v_pk_mul_f32 v[104:105], v[18:19], v[104:105]
	v_exp_f32_e32 v106, v106
	v_pk_fma_f32 v[18:19], v[112:113], s[64:65], v[104:105] op_sel_hi:[0,1,1]
	v_exp_f32_e32 v107, v107
	v_pk_fma_f32 v[114:115], s[80:81], v[18:19], 0 op_sel_hi:[1,1,0]
	v_pk_mul_f32 v[106:107], v[20:21], v[106:107]
	v_pk_mul_f32 v[108:109], v[52:53], v[6:7] op_sel:[1,0]
	v_pk_fma_f32 v[20:21], v[112:113], s[66:67], v[106:107] op_sel_hi:[0,1,1]
	v_exp_f32_e32 v108, v108
	v_pk_fma_f32 v[114:115], s[82:83], v[20:21], v[114:115]
	v_exp_f32_e32 v109, v109
	v_pk_mul_f32 v[110:111], v[52:53], v[8:9] op_sel:[1,0]
	v_pk_mul_f32 v[108:109], v[22:23], v[108:109]
	v_exp_f32_e32 v110, v110
	v_pk_fma_f32 v[22:23], v[112:113], s[68:69], v[108:109] op_sel_hi:[0,1,1]
	v_exp_f32_e32 v111, v111
	v_pk_fma_f32 v[114:115], s[84:85], v[22:23], v[114:115]
	v_pk_mul_f32 v[110:111], v[24:25], v[110:111]
	v_pk_mul_f32 v[104:105], v[52:53], v[10:11] op_sel:[1,0]
	v_pk_fma_f32 v[24:25], v[112:113], s[70:71], v[110:111] op_sel_hi:[0,1,1]
	v_exp_f32_e32 v104, v104
	v_pk_fma_f32 v[114:115], s[86:87], v[24:25], v[114:115]
	v_exp_f32_e32 v105, v105
	v_pk_mul_f32 v[106:107], v[52:53], v[12:13] op_sel:[1,0]
	v_pk_mul_f32 v[104:105], v[26:27], v[104:105]
	v_exp_f32_e32 v106, v106
	v_pk_fma_f32 v[26:27], v[112:113], s[72:73], v[104:105] op_sel_hi:[0,1,1]
	v_exp_f32_e32 v107, v107
	v_pk_fma_f32 v[114:115], s[88:89], v[26:27], v[114:115]
	v_pk_mul_f32 v[106:107], v[28:29], v[106:107]
	v_pk_mul_f32 v[108:109], v[52:53], v[14:15] op_sel:[1,0]
	v_pk_fma_f32 v[28:29], v[112:113], s[74:75], v[106:107] op_sel_hi:[0,1,1]
	v_exp_f32_e32 v108, v108
	v_pk_fma_f32 v[114:115], s[90:91], v[28:29], v[114:115]
	v_exp_f32_e32 v109, v109
	v_pk_mul_f32 v[110:111], v[52:53], v[16:17] op_sel:[1,0]
	v_pk_mul_f32 v[108:109], v[30:31], v[108:109]
	v_exp_f32_e32 v110, v110
	v_pk_fma_f32 v[30:31], v[112:113], s[76:77], v[108:109] op_sel_hi:[0,1,1]
	v_exp_f32_e32 v111, v111
	v_pk_fma_f32 v[114:115], s[92:93], v[30:31], v[114:115]
	v_pk_mul_f32 v[110:111], v[32:33], v[110:111]
	v_cvt_f32_f16_sdwa v117, v63 dst_sel:DWORD dst_unused:UNUSED_PAD src0_sel:WORD_1
	v_pk_fma_f32 v[32:33], v[112:113], s[78:79], v[110:111] op_sel_hi:[0,1,1]
	s_nop 0
	v_pk_fma_f32 v[114:115], s[94:95], v[32:33], v[114:115]
	s_nop 0
	v_add_f32_e32 v116, v114, v115
	v_fmac_f32_e32 v116, v98, v113
	v_mul_f32_e32 v116, v116, v117
	v_fma_mixlo_f16 v116, v116, s30, 0
	global_store_short v99, v116, s[26:27]
	s_add_u32 s26, s26, 0x1000
	s_addc_u32 s27, s27, 0
	s_waitcnt lgkmcnt(0)
	s_load_dwordx16 s[64:79], s[24:25], 0x680
	s_load_dwordx16 s[80:95], s[24:25], 0x6c0
	v_cvt_f32_f16_e32 v113, v60
	v_mul_f32_e32 v112, v54, v113
	v_pk_mul_f32 v[104:105], v[54:55], v[2:3] op_sel_hi:[0,1]
	v_pk_mul_f32 v[106:107], v[54:55], v[4:5] op_sel_hi:[0,1]
	v_exp_f32_e32 v104, v104
	v_exp_f32_e32 v105, v105
	v_exp_f32_e32 v106, v106
	v_pk_mul_f32 v[104:105], v[18:19], v[104:105]
	v_exp_f32_e32 v107, v107
	v_pk_fma_f32 v[18:19], v[112:113], s[32:33], v[104:105] op_sel_hi:[0,1,1]
	v_pk_mul_f32 v[106:107], v[20:21], v[106:107]
	v_pk_fma_f32 v[114:115], s[48:49], v[18:19], 0 op_sel_hi:[1,1,0]
	v_pk_fma_f32 v[20:21], v[112:113], s[34:35], v[106:107] op_sel_hi:[0,1,1]
	v_pk_mul_f32 v[108:109], v[54:55], v[6:7] op_sel_hi:[0,1]
	v_pk_fma_f32 v[114:115], s[50:51], v[20:21], v[114:115]
	v_exp_f32_e32 v108, v108
	v_exp_f32_e32 v109, v109
	v_pk_mul_f32 v[110:111], v[54:55], v[8:9] op_sel_hi:[0,1]
	v_pk_mul_f32 v[108:109], v[22:23], v[108:109]
	v_exp_f32_e32 v110, v110
	v_pk_fma_f32 v[22:23], v[112:113], s[36:37], v[108:109] op_sel_hi:[0,1,1]
	v_exp_f32_e32 v111, v111
	v_pk_fma_f32 v[114:115], s[52:53], v[22:23], v[114:115]
	v_pk_mul_f32 v[110:111], v[24:25], v[110:111]
	v_pk_mul_f32 v[104:105], v[54:55], v[10:11] op_sel_hi:[0,1]
	v_pk_fma_f32 v[24:25], v[112:113], s[38:39], v[110:111] op_sel_hi:[0,1,1]
	v_exp_f32_e32 v104, v104
	v_pk_fma_f32 v[114:115], s[54:55], v[24:25], v[114:115]
	v_exp_f32_e32 v105, v105
	v_pk_mul_f32 v[106:107], v[54:55], v[12:13] op_sel_hi:[0,1]
	v_pk_mul_f32 v[104:105], v[26:27], v[104:105]
	v_exp_f32_e32 v106, v106
	v_pk_fma_f32 v[26:27], v[112:113], s[40:41], v[104:105] op_sel_hi:[0,1,1]
	v_exp_f32_e32 v107, v107
	v_pk_fma_f32 v[114:115], s[56:57], v[26:27], v[114:115]
	v_pk_mul_f32 v[106:107], v[28:29], v[106:107]
	v_pk_mul_f32 v[108:109], v[54:55], v[14:15] op_sel_hi:[0,1]
	v_pk_fma_f32 v[28:29], v[112:113], s[42:43], v[106:107] op_sel_hi:[0,1,1]
	v_exp_f32_e32 v108, v108
	v_pk_fma_f32 v[114:115], s[58:59], v[28:29], v[114:115]
	v_exp_f32_e32 v109, v109
	v_pk_mul_f32 v[110:111], v[54:55], v[16:17] op_sel_hi:[0,1]
	v_pk_mul_f32 v[108:109], v[30:31], v[108:109]
	v_exp_f32_e32 v110, v110
	v_pk_fma_f32 v[30:31], v[112:113], s[44:45], v[108:109] op_sel_hi:[0,1,1]
	v_exp_f32_e32 v111, v111
	v_pk_fma_f32 v[114:115], s[60:61], v[30:31], v[114:115]
	v_pk_mul_f32 v[110:111], v[32:33], v[110:111]
	v_cvt_f32_f16_e32 v117, v64
	v_pk_fma_f32 v[32:33], v[112:113], s[46:47], v[110:111] op_sel_hi:[0,1,1]
	s_nop 0
	v_pk_fma_f32 v[114:115], s[62:63], v[32:33], v[114:115]
	s_nop 0
	v_add_f32_e32 v116, v114, v115
	v_fmac_f32_e32 v116, v98, v113
	v_mul_f32_e32 v116, v116, v117
	v_fma_mixlo_f16 v116, v116, s30, 0
	global_store_short v99, v116, s[26:27]
	s_add_u32 s26, s26, 0x1000
	s_addc_u32 s27, s27, 0
	s_waitcnt lgkmcnt(0)
	s_load_dwordx16 s[32:47], s[24:25], 0x700
	s_load_dwordx16 s[48:63], s[24:25], 0x740
	v_cvt_f32_f16_sdwa v113, v60 dst_sel:DWORD dst_unused:UNUSED_PAD src0_sel:WORD_1
	v_pk_mul_f32 v[104:105], v[54:55], v[2:3] op_sel:[1,0]
	v_mul_f32_e32 v112, v55, v113
	v_exp_f32_e32 v104, v104
	v_exp_f32_e32 v105, v105
	v_pk_mul_f32 v[106:107], v[54:55], v[4:5] op_sel:[1,0]
	v_pk_mul_f32 v[104:105], v[18:19], v[104:105]
	v_exp_f32_e32 v106, v106
	v_pk_fma_f32 v[18:19], v[112:113], s[64:65], v[104:105] op_sel_hi:[0,1,1]
	v_exp_f32_e32 v107, v107
	v_pk_fma_f32 v[114:115], s[80:81], v[18:19], 0 op_sel_hi:[1,1,0]
	v_pk_mul_f32 v[106:107], v[20:21], v[106:107]
	v_pk_mul_f32 v[108:109], v[54:55], v[6:7] op_sel:[1,0]
	v_pk_fma_f32 v[20:21], v[112:113], s[66:67], v[106:107] op_sel_hi:[0,1,1]
	v_exp_f32_e32 v108, v108
	v_pk_fma_f32 v[114:115], s[82:83], v[20:21], v[114:115]
	v_exp_f32_e32 v109, v109
	v_pk_mul_f32 v[110:111], v[54:55], v[8:9] op_sel:[1,0]
	v_pk_mul_f32 v[108:109], v[22:23], v[108:109]
	v_exp_f32_e32 v110, v110
	v_pk_fma_f32 v[22:23], v[112:113], s[68:69], v[108:109] op_sel_hi:[0,1,1]
	v_exp_f32_e32 v111, v111
	v_pk_fma_f32 v[114:115], s[84:85], v[22:23], v[114:115]
	v_pk_mul_f32 v[110:111], v[24:25], v[110:111]
	v_pk_mul_f32 v[104:105], v[54:55], v[10:11] op_sel:[1,0]
	v_pk_fma_f32 v[24:25], v[112:113], s[70:71], v[110:111] op_sel_hi:[0,1,1]
	v_exp_f32_e32 v104, v104
	v_pk_fma_f32 v[114:115], s[86:87], v[24:25], v[114:115]
	v_exp_f32_e32 v105, v105
	v_pk_mul_f32 v[106:107], v[54:55], v[12:13] op_sel:[1,0]
	v_pk_mul_f32 v[104:105], v[26:27], v[104:105]
	v_exp_f32_e32 v106, v106
	v_pk_fma_f32 v[26:27], v[112:113], s[72:73], v[104:105] op_sel_hi:[0,1,1]
	v_exp_f32_e32 v107, v107
	v_pk_fma_f32 v[114:115], s[88:89], v[26:27], v[114:115]
	v_pk_mul_f32 v[106:107], v[28:29], v[106:107]
	v_pk_mul_f32 v[108:109], v[54:55], v[14:15] op_sel:[1,0]
	v_pk_fma_f32 v[28:29], v[112:113], s[74:75], v[106:107] op_sel_hi:[0,1,1]
	v_exp_f32_e32 v108, v108
	v_pk_fma_f32 v[114:115], s[90:91], v[28:29], v[114:115]
	v_exp_f32_e32 v109, v109
	v_pk_mul_f32 v[110:111], v[54:55], v[16:17] op_sel:[1,0]
	v_pk_mul_f32 v[108:109], v[30:31], v[108:109]
	v_exp_f32_e32 v110, v110
	v_pk_fma_f32 v[30:31], v[112:113], s[76:77], v[108:109] op_sel_hi:[0,1,1]
	v_exp_f32_e32 v111, v111
	v_pk_fma_f32 v[114:115], s[92:93], v[30:31], v[114:115]
	v_pk_mul_f32 v[110:111], v[32:33], v[110:111]
	v_cvt_f32_f16_sdwa v117, v64 dst_sel:DWORD dst_unused:UNUSED_PAD src0_sel:WORD_1
	v_pk_fma_f32 v[32:33], v[112:113], s[78:79], v[110:111] op_sel_hi:[0,1,1]
	s_nop 0
	v_pk_fma_f32 v[114:115], s[94:95], v[32:33], v[114:115]
	s_nop 0
	v_add_f32_e32 v116, v114, v115
	v_fmac_f32_e32 v116, v98, v113
	v_mul_f32_e32 v116, v116, v117
	v_fma_mixlo_f16 v116, v116, s30, 0
	global_store_short v99, v116, s[26:27]
	s_add_u32 s26, s26, 0x1000
	s_addc_u32 s27, s27, 0
	s_waitcnt lgkmcnt(0)
	s_load_dwordx16 s[64:79], s[24:25], 0x780
	s_load_dwordx16 s[80:95], s[24:25], 0x7c0
	v_cvt_f32_f16_e32 v113, v61
	v_mul_f32_e32 v112, v56, v113
	v_pk_mul_f32 v[104:105], v[56:57], v[2:3] op_sel_hi:[0,1]
	v_pk_mul_f32 v[106:107], v[56:57], v[4:5] op_sel_hi:[0,1]
	v_exp_f32_e32 v104, v104
	v_exp_f32_e32 v105, v105
	v_exp_f32_e32 v106, v106
	v_pk_mul_f32 v[104:105], v[18:19], v[104:105]
	v_exp_f32_e32 v107, v107
	v_pk_fma_f32 v[18:19], v[112:113], s[32:33], v[104:105] op_sel_hi:[0,1,1]
	v_pk_mul_f32 v[106:107], v[20:21], v[106:107]
	v_pk_fma_f32 v[114:115], s[48:49], v[18:19], 0 op_sel_hi:[1,1,0]
	v_pk_fma_f32 v[20:21], v[112:113], s[34:35], v[106:107] op_sel_hi:[0,1,1]
	v_pk_mul_f32 v[108:109], v[56:57], v[6:7] op_sel_hi:[0,1]
	v_pk_fma_f32 v[114:115], s[50:51], v[20:21], v[114:115]
	v_exp_f32_e32 v108, v108
	v_exp_f32_e32 v109, v109
	v_pk_mul_f32 v[110:111], v[56:57], v[8:9] op_sel_hi:[0,1]
	v_pk_mul_f32 v[108:109], v[22:23], v[108:109]
	v_exp_f32_e32 v110, v110
	v_pk_fma_f32 v[22:23], v[112:113], s[36:37], v[108:109] op_sel_hi:[0,1,1]
	v_exp_f32_e32 v111, v111
	v_pk_fma_f32 v[114:115], s[52:53], v[22:23], v[114:115]
	v_pk_mul_f32 v[110:111], v[24:25], v[110:111]
	v_pk_mul_f32 v[104:105], v[56:57], v[10:11] op_sel_hi:[0,1]
	v_pk_fma_f32 v[24:25], v[112:113], s[38:39], v[110:111] op_sel_hi:[0,1,1]
	v_exp_f32_e32 v104, v104
	v_pk_fma_f32 v[114:115], s[54:55], v[24:25], v[114:115]
	v_exp_f32_e32 v105, v105
	v_pk_mul_f32 v[106:107], v[56:57], v[12:13] op_sel_hi:[0,1]
	v_pk_mul_f32 v[104:105], v[26:27], v[104:105]
	v_exp_f32_e32 v106, v106
	v_pk_fma_f32 v[26:27], v[112:113], s[40:41], v[104:105] op_sel_hi:[0,1,1]
	v_exp_f32_e32 v107, v107
	v_pk_fma_f32 v[114:115], s[56:57], v[26:27], v[114:115]
	v_pk_mul_f32 v[106:107], v[28:29], v[106:107]
	v_pk_mul_f32 v[108:109], v[56:57], v[14:15] op_sel_hi:[0,1]
	v_pk_fma_f32 v[28:29], v[112:113], s[42:43], v[106:107] op_sel_hi:[0,1,1]
	v_exp_f32_e32 v108, v108
	v_pk_fma_f32 v[114:115], s[58:59], v[28:29], v[114:115]
	v_exp_f32_e32 v109, v109
	v_pk_mul_f32 v[110:111], v[56:57], v[16:17] op_sel_hi:[0,1]
	v_pk_mul_f32 v[108:109], v[30:31], v[108:109]
	v_exp_f32_e32 v110, v110
	v_pk_fma_f32 v[30:31], v[112:113], s[44:45], v[108:109] op_sel_hi:[0,1,1]
	v_exp_f32_e32 v111, v111
	v_pk_fma_f32 v[114:115], s[60:61], v[30:31], v[114:115]
	v_pk_mul_f32 v[110:111], v[32:33], v[110:111]
	v_cvt_f32_f16_e32 v117, v65
	v_pk_fma_f32 v[32:33], v[112:113], s[46:47], v[110:111] op_sel_hi:[0,1,1]
	s_nop 0
	v_pk_fma_f32 v[114:115], s[62:63], v[32:33], v[114:115]
	s_nop 0
	v_add_f32_e32 v116, v114, v115
	v_fmac_f32_e32 v116, v98, v113
	v_mul_f32_e32 v116, v116, v117
	v_fma_mixlo_f16 v116, v116, s30, 0
	global_store_short v99, v116, s[26:27]
	s_add_u32 s26, s26, 0x1000
	s_addc_u32 s27, s27, 0
	s_waitcnt lgkmcnt(0)
	s_load_dwordx16 s[32:47], s[24:25], 0x800
	s_load_dwordx16 s[48:63], s[24:25], 0x840
	v_cvt_f32_f16_sdwa v113, v61 dst_sel:DWORD dst_unused:UNUSED_PAD src0_sel:WORD_1
	v_pk_mul_f32 v[104:105], v[56:57], v[2:3] op_sel:[1,0]
	v_mul_f32_e32 v112, v57, v113
	v_exp_f32_e32 v104, v104
	v_exp_f32_e32 v105, v105
	v_pk_mul_f32 v[106:107], v[56:57], v[4:5] op_sel:[1,0]
	v_pk_mul_f32 v[104:105], v[18:19], v[104:105]
	v_exp_f32_e32 v106, v106
	v_pk_fma_f32 v[18:19], v[112:113], s[64:65], v[104:105] op_sel_hi:[0,1,1]
	v_exp_f32_e32 v107, v107
	v_pk_fma_f32 v[114:115], s[80:81], v[18:19], 0 op_sel_hi:[1,1,0]
	v_pk_mul_f32 v[106:107], v[20:21], v[106:107]
	v_pk_mul_f32 v[108:109], v[56:57], v[6:7] op_sel:[1,0]
	v_pk_fma_f32 v[20:21], v[112:113], s[66:67], v[106:107] op_sel_hi:[0,1,1]
	v_exp_f32_e32 v108, v108
	v_pk_fma_f32 v[114:115], s[82:83], v[20:21], v[114:115]
	v_exp_f32_e32 v109, v109
	v_pk_mul_f32 v[110:111], v[56:57], v[8:9] op_sel:[1,0]
	v_pk_mul_f32 v[108:109], v[22:23], v[108:109]
	v_exp_f32_e32 v110, v110
	v_pk_fma_f32 v[22:23], v[112:113], s[68:69], v[108:109] op_sel_hi:[0,1,1]
	v_exp_f32_e32 v111, v111
	v_pk_fma_f32 v[114:115], s[84:85], v[22:23], v[114:115]
	v_pk_mul_f32 v[110:111], v[24:25], v[110:111]
	v_pk_mul_f32 v[104:105], v[56:57], v[10:11] op_sel:[1,0]
	v_pk_fma_f32 v[24:25], v[112:113], s[70:71], v[110:111] op_sel_hi:[0,1,1]
	v_exp_f32_e32 v104, v104
	v_pk_fma_f32 v[114:115], s[86:87], v[24:25], v[114:115]
	v_exp_f32_e32 v105, v105
	v_pk_mul_f32 v[106:107], v[56:57], v[12:13] op_sel:[1,0]
	v_pk_mul_f32 v[104:105], v[26:27], v[104:105]
	v_exp_f32_e32 v106, v106
	v_pk_fma_f32 v[26:27], v[112:113], s[72:73], v[104:105] op_sel_hi:[0,1,1]
	v_exp_f32_e32 v107, v107
	v_pk_fma_f32 v[114:115], s[88:89], v[26:27], v[114:115]
	v_pk_mul_f32 v[106:107], v[28:29], v[106:107]
	v_pk_mul_f32 v[108:109], v[56:57], v[14:15] op_sel:[1,0]
	v_pk_fma_f32 v[28:29], v[112:113], s[74:75], v[106:107] op_sel_hi:[0,1,1]
	v_exp_f32_e32 v108, v108
	v_pk_fma_f32 v[114:115], s[90:91], v[28:29], v[114:115]
	v_exp_f32_e32 v109, v109
	v_pk_mul_f32 v[110:111], v[56:57], v[16:17] op_sel:[1,0]
	v_pk_mul_f32 v[108:109], v[30:31], v[108:109]
	v_exp_f32_e32 v110, v110
	v_pk_fma_f32 v[30:31], v[112:113], s[76:77], v[108:109] op_sel_hi:[0,1,1]
	v_exp_f32_e32 v111, v111
	v_pk_fma_f32 v[114:115], s[92:93], v[30:31], v[114:115]
	v_pk_mul_f32 v[110:111], v[32:33], v[110:111]
	v_cvt_f32_f16_sdwa v117, v65 dst_sel:DWORD dst_unused:UNUSED_PAD src0_sel:WORD_1
	v_pk_fma_f32 v[32:33], v[112:113], s[78:79], v[110:111] op_sel_hi:[0,1,1]
	s_nop 0
	v_pk_fma_f32 v[114:115], s[94:95], v[32:33], v[114:115]
	s_nop 0
	v_add_f32_e32 v116, v114, v115
	v_fmac_f32_e32 v116, v98, v113
	v_mul_f32_e32 v116, v116, v117
	v_fma_mixlo_f16 v116, v116, s30, 0
	global_store_short v99, v116, s[26:27]
	s_add_u32 s26, s26, 0x1000
	s_addc_u32 s27, s27, 0
	s_waitcnt vmcnt(8)
	global_load_dwordx4 v[82:85], v102, s[0:1]
	s_add_u32 s0, s0, 0x8000
	s_addc_u32 s1, s1, 0
	global_load_dwordx4 v[90:93], v102, s[8:9]
	s_add_u32 s8, s8, 0x8000
	s_addc_u32 s9, s9, 0
	global_load_dwordx2 v[94:95], v103, s[2:3]
	s_add_u32 s2, s2, 0x8000
	s_addc_u32 s3, s3, 0
	global_load_dwordx4 v[86:89], v102, s[0:1]
	s_add_u32 s0, s0, 0x8000
	s_addc_u32 s1, s1, 0
	global_load_dwordx2 v[96:97], v103, s[2:3]
	s_add_u32 s2, s2, 0x8000
	s_addc_u32 s3, s3, 0
	s_waitcnt lgkmcnt(0)
	s_load_dwordx16 s[64:79], s[24:25], 0x880
	s_load_dwordx16 s[80:95], s[24:25], 0x8c0
	v_cvt_f32_f16_e32 v113, v74
	v_mul_f32_e32 v112, v66, v113
	v_pk_mul_f32 v[104:105], v[66:67], v[2:3] op_sel_hi:[0,1]
	v_pk_mul_f32 v[106:107], v[66:67], v[4:5] op_sel_hi:[0,1]
	v_exp_f32_e32 v104, v104
	v_exp_f32_e32 v105, v105
	v_exp_f32_e32 v106, v106
	v_pk_mul_f32 v[104:105], v[18:19], v[104:105]
	v_exp_f32_e32 v107, v107
	v_pk_fma_f32 v[18:19], v[112:113], s[32:33], v[104:105] op_sel_hi:[0,1,1]
	v_pk_mul_f32 v[106:107], v[20:21], v[106:107]
	v_pk_fma_f32 v[114:115], s[48:49], v[18:19], 0 op_sel_hi:[1,1,0]
	v_pk_fma_f32 v[20:21], v[112:113], s[34:35], v[106:107] op_sel_hi:[0,1,1]
	v_pk_mul_f32 v[108:109], v[66:67], v[6:7] op_sel_hi:[0,1]
	v_pk_fma_f32 v[114:115], s[50:51], v[20:21], v[114:115]
	v_exp_f32_e32 v108, v108
	v_exp_f32_e32 v109, v109
	v_pk_mul_f32 v[110:111], v[66:67], v[8:9] op_sel_hi:[0,1]
	v_pk_mul_f32 v[108:109], v[22:23], v[108:109]
	v_exp_f32_e32 v110, v110
	v_pk_fma_f32 v[22:23], v[112:113], s[36:37], v[108:109] op_sel_hi:[0,1,1]
	v_exp_f32_e32 v111, v111
	v_pk_fma_f32 v[114:115], s[52:53], v[22:23], v[114:115]
	v_pk_mul_f32 v[110:111], v[24:25], v[110:111]
	v_pk_mul_f32 v[104:105], v[66:67], v[10:11] op_sel_hi:[0,1]
	v_pk_fma_f32 v[24:25], v[112:113], s[38:39], v[110:111] op_sel_hi:[0,1,1]
	v_exp_f32_e32 v104, v104
	v_pk_fma_f32 v[114:115], s[54:55], v[24:25], v[114:115]
	v_exp_f32_e32 v105, v105
	v_pk_mul_f32 v[106:107], v[66:67], v[12:13] op_sel_hi:[0,1]
	v_pk_mul_f32 v[104:105], v[26:27], v[104:105]
	v_exp_f32_e32 v106, v106
	v_pk_fma_f32 v[26:27], v[112:113], s[40:41], v[104:105] op_sel_hi:[0,1,1]
	v_exp_f32_e32 v107, v107
	v_pk_fma_f32 v[114:115], s[56:57], v[26:27], v[114:115]
	v_pk_mul_f32 v[106:107], v[28:29], v[106:107]
	v_pk_mul_f32 v[108:109], v[66:67], v[14:15] op_sel_hi:[0,1]
	v_pk_fma_f32 v[28:29], v[112:113], s[42:43], v[106:107] op_sel_hi:[0,1,1]
	v_exp_f32_e32 v108, v108
	v_pk_fma_f32 v[114:115], s[58:59], v[28:29], v[114:115]
	v_exp_f32_e32 v109, v109
	v_pk_mul_f32 v[110:111], v[66:67], v[16:17] op_sel_hi:[0,1]
	v_pk_mul_f32 v[108:109], v[30:31], v[108:109]
	v_exp_f32_e32 v110, v110
	v_pk_fma_f32 v[30:31], v[112:113], s[44:45], v[108:109] op_sel_hi:[0,1,1]
	v_exp_f32_e32 v111, v111
	v_pk_fma_f32 v[114:115], s[60:61], v[30:31], v[114:115]
	v_pk_mul_f32 v[110:111], v[32:33], v[110:111]
	v_cvt_f32_f16_e32 v117, v78
	v_pk_fma_f32 v[32:33], v[112:113], s[46:47], v[110:111] op_sel_hi:[0,1,1]
	s_nop 0
	v_pk_fma_f32 v[114:115], s[62:63], v[32:33], v[114:115]
	s_nop 0
	v_add_f32_e32 v116, v114, v115
	v_fmac_f32_e32 v116, v98, v113
	v_mul_f32_e32 v116, v116, v117
	v_fma_mixlo_f16 v116, v116, s30, 0
	global_store_short v99, v116, s[26:27]
	s_add_u32 s26, s26, 0x1000
	s_addc_u32 s27, s27, 0
	s_waitcnt lgkmcnt(0)
	s_load_dwordx16 s[32:47], s[24:25], 0x900
	s_load_dwordx16 s[48:63], s[24:25], 0x940
	v_cvt_f32_f16_sdwa v113, v74 dst_sel:DWORD dst_unused:UNUSED_PAD src0_sel:WORD_1
	v_pk_mul_f32 v[104:105], v[66:67], v[2:3] op_sel:[1,0]
	v_mul_f32_e32 v112, v67, v113
	v_exp_f32_e32 v104, v104
	v_exp_f32_e32 v105, v105
	v_pk_mul_f32 v[106:107], v[66:67], v[4:5] op_sel:[1,0]
	v_pk_mul_f32 v[104:105], v[18:19], v[104:105]
	v_exp_f32_e32 v106, v106
	v_pk_fma_f32 v[18:19], v[112:113], s[64:65], v[104:105] op_sel_hi:[0,1,1]
	v_exp_f32_e32 v107, v107
	v_pk_fma_f32 v[114:115], s[80:81], v[18:19], 0 op_sel_hi:[1,1,0]
	v_pk_mul_f32 v[106:107], v[20:21], v[106:107]
	v_pk_mul_f32 v[108:109], v[66:67], v[6:7] op_sel:[1,0]
	v_pk_fma_f32 v[20:21], v[112:113], s[66:67], v[106:107] op_sel_hi:[0,1,1]
	v_exp_f32_e32 v108, v108
	v_pk_fma_f32 v[114:115], s[82:83], v[20:21], v[114:115]
	v_exp_f32_e32 v109, v109
	v_pk_mul_f32 v[110:111], v[66:67], v[8:9] op_sel:[1,0]
	v_pk_mul_f32 v[108:109], v[22:23], v[108:109]
	v_exp_f32_e32 v110, v110
	v_pk_fma_f32 v[22:23], v[112:113], s[68:69], v[108:109] op_sel_hi:[0,1,1]
	v_exp_f32_e32 v111, v111
	v_pk_fma_f32 v[114:115], s[84:85], v[22:23], v[114:115]
	v_pk_mul_f32 v[110:111], v[24:25], v[110:111]
	v_pk_mul_f32 v[104:105], v[66:67], v[10:11] op_sel:[1,0]
	v_pk_fma_f32 v[24:25], v[112:113], s[70:71], v[110:111] op_sel_hi:[0,1,1]
	v_exp_f32_e32 v104, v104
	v_pk_fma_f32 v[114:115], s[86:87], v[24:25], v[114:115]
	v_exp_f32_e32 v105, v105
	v_pk_mul_f32 v[106:107], v[66:67], v[12:13] op_sel:[1,0]
	v_pk_mul_f32 v[104:105], v[26:27], v[104:105]
	v_exp_f32_e32 v106, v106
	v_pk_fma_f32 v[26:27], v[112:113], s[72:73], v[104:105] op_sel_hi:[0,1,1]
	v_exp_f32_e32 v107, v107
	v_pk_fma_f32 v[114:115], s[88:89], v[26:27], v[114:115]
	v_pk_mul_f32 v[106:107], v[28:29], v[106:107]
	v_pk_mul_f32 v[108:109], v[66:67], v[14:15] op_sel:[1,0]
	v_pk_fma_f32 v[28:29], v[112:113], s[74:75], v[106:107] op_sel_hi:[0,1,1]
	v_exp_f32_e32 v108, v108
	v_pk_fma_f32 v[114:115], s[90:91], v[28:29], v[114:115]
	v_exp_f32_e32 v109, v109
	v_pk_mul_f32 v[110:111], v[66:67], v[16:17] op_sel:[1,0]
	v_pk_mul_f32 v[108:109], v[30:31], v[108:109]
	v_exp_f32_e32 v110, v110
	v_pk_fma_f32 v[30:31], v[112:113], s[76:77], v[108:109] op_sel_hi:[0,1,1]
	v_exp_f32_e32 v111, v111
	v_pk_fma_f32 v[114:115], s[92:93], v[30:31], v[114:115]
	v_pk_mul_f32 v[110:111], v[32:33], v[110:111]
	v_cvt_f32_f16_sdwa v117, v78 dst_sel:DWORD dst_unused:UNUSED_PAD src0_sel:WORD_1
	v_pk_fma_f32 v[32:33], v[112:113], s[78:79], v[110:111] op_sel_hi:[0,1,1]
	s_nop 0
	v_pk_fma_f32 v[114:115], s[94:95], v[32:33], v[114:115]
	s_nop 0
	v_add_f32_e32 v116, v114, v115
	v_fmac_f32_e32 v116, v98, v113
	v_mul_f32_e32 v116, v116, v117
	v_fma_mixlo_f16 v116, v116, s30, 0
	global_store_short v99, v116, s[26:27]
	s_add_u32 s26, s26, 0x1000
	s_addc_u32 s27, s27, 0
	s_waitcnt lgkmcnt(0)
	s_load_dwordx16 s[64:79], s[24:25], 0x980
	s_load_dwordx16 s[80:95], s[24:25], 0x9c0
	v_cvt_f32_f16_e32 v113, v75
	v_mul_f32_e32 v112, v68, v113
	v_pk_mul_f32 v[104:105], v[68:69], v[2:3] op_sel_hi:[0,1]
	v_pk_mul_f32 v[106:107], v[68:69], v[4:5] op_sel_hi:[0,1]
	v_exp_f32_e32 v104, v104
	v_exp_f32_e32 v105, v105
	v_exp_f32_e32 v106, v106
	v_pk_mul_f32 v[104:105], v[18:19], v[104:105]
	v_exp_f32_e32 v107, v107
	v_pk_fma_f32 v[18:19], v[112:113], s[32:33], v[104:105] op_sel_hi:[0,1,1]
	v_pk_mul_f32 v[106:107], v[20:21], v[106:107]
	v_pk_fma_f32 v[114:115], s[48:49], v[18:19], 0 op_sel_hi:[1,1,0]
	v_pk_fma_f32 v[20:21], v[112:113], s[34:35], v[106:107] op_sel_hi:[0,1,1]
	v_pk_mul_f32 v[108:109], v[68:69], v[6:7] op_sel_hi:[0,1]
	v_pk_fma_f32 v[114:115], s[50:51], v[20:21], v[114:115]
	v_exp_f32_e32 v108, v108
	v_exp_f32_e32 v109, v109
	v_pk_mul_f32 v[110:111], v[68:69], v[8:9] op_sel_hi:[0,1]
	v_pk_mul_f32 v[108:109], v[22:23], v[108:109]
	v_exp_f32_e32 v110, v110
	v_pk_fma_f32 v[22:23], v[112:113], s[36:37], v[108:109] op_sel_hi:[0,1,1]
	v_exp_f32_e32 v111, v111
	v_pk_fma_f32 v[114:115], s[52:53], v[22:23], v[114:115]
	v_pk_mul_f32 v[110:111], v[24:25], v[110:111]
	v_pk_mul_f32 v[104:105], v[68:69], v[10:11] op_sel_hi:[0,1]
	v_pk_fma_f32 v[24:25], v[112:113], s[38:39], v[110:111] op_sel_hi:[0,1,1]
	v_exp_f32_e32 v104, v104
	v_pk_fma_f32 v[114:115], s[54:55], v[24:25], v[114:115]
	v_exp_f32_e32 v105, v105
	v_pk_mul_f32 v[106:107], v[68:69], v[12:13] op_sel_hi:[0,1]
	v_pk_mul_f32 v[104:105], v[26:27], v[104:105]
	v_exp_f32_e32 v106, v106
	v_pk_fma_f32 v[26:27], v[112:113], s[40:41], v[104:105] op_sel_hi:[0,1,1]
	v_exp_f32_e32 v107, v107
	v_pk_fma_f32 v[114:115], s[56:57], v[26:27], v[114:115]
	v_pk_mul_f32 v[106:107], v[28:29], v[106:107]
	v_pk_mul_f32 v[108:109], v[68:69], v[14:15] op_sel_hi:[0,1]
	v_pk_fma_f32 v[28:29], v[112:113], s[42:43], v[106:107] op_sel_hi:[0,1,1]
	v_exp_f32_e32 v108, v108
	v_pk_fma_f32 v[114:115], s[58:59], v[28:29], v[114:115]
	v_exp_f32_e32 v109, v109
	v_pk_mul_f32 v[110:111], v[68:69], v[16:17] op_sel_hi:[0,1]
	v_pk_mul_f32 v[108:109], v[30:31], v[108:109]
	v_exp_f32_e32 v110, v110
	v_pk_fma_f32 v[30:31], v[112:113], s[44:45], v[108:109] op_sel_hi:[0,1,1]
	v_exp_f32_e32 v111, v111
	v_pk_fma_f32 v[114:115], s[60:61], v[30:31], v[114:115]
	v_pk_mul_f32 v[110:111], v[32:33], v[110:111]
	v_cvt_f32_f16_e32 v117, v79
	v_pk_fma_f32 v[32:33], v[112:113], s[46:47], v[110:111] op_sel_hi:[0,1,1]
	s_nop 0
	v_pk_fma_f32 v[114:115], s[62:63], v[32:33], v[114:115]
	s_nop 0
	v_add_f32_e32 v116, v114, v115
	v_fmac_f32_e32 v116, v98, v113
	v_mul_f32_e32 v116, v116, v117
	v_fma_mixlo_f16 v116, v116, s30, 0
	global_store_short v99, v116, s[26:27]
	s_add_u32 s26, s26, 0x1000
	s_addc_u32 s27, s27, 0
	s_waitcnt lgkmcnt(0)
	s_load_dwordx16 s[32:47], s[24:25], 0xa00
	s_load_dwordx16 s[48:63], s[24:25], 0xa40
	v_cvt_f32_f16_sdwa v113, v75 dst_sel:DWORD dst_unused:UNUSED_PAD src0_sel:WORD_1
	v_pk_mul_f32 v[104:105], v[68:69], v[2:3] op_sel:[1,0]
	v_mul_f32_e32 v112, v69, v113
	v_exp_f32_e32 v104, v104
	v_exp_f32_e32 v105, v105
	v_pk_mul_f32 v[106:107], v[68:69], v[4:5] op_sel:[1,0]
	v_pk_mul_f32 v[104:105], v[18:19], v[104:105]
	v_exp_f32_e32 v106, v106
	v_pk_fma_f32 v[18:19], v[112:113], s[64:65], v[104:105] op_sel_hi:[0,1,1]
	v_exp_f32_e32 v107, v107
	v_pk_fma_f32 v[114:115], s[80:81], v[18:19], 0 op_sel_hi:[1,1,0]
	v_pk_mul_f32 v[106:107], v[20:21], v[106:107]
	v_pk_mul_f32 v[108:109], v[68:69], v[6:7] op_sel:[1,0]
	v_pk_fma_f32 v[20:21], v[112:113], s[66:67], v[106:107] op_sel_hi:[0,1,1]
	v_exp_f32_e32 v108, v108
	v_pk_fma_f32 v[114:115], s[82:83], v[20:21], v[114:115]
	v_exp_f32_e32 v109, v109
	v_pk_mul_f32 v[110:111], v[68:69], v[8:9] op_sel:[1,0]
	v_pk_mul_f32 v[108:109], v[22:23], v[108:109]
	v_exp_f32_e32 v110, v110
	v_pk_fma_f32 v[22:23], v[112:113], s[68:69], v[108:109] op_sel_hi:[0,1,1]
	v_exp_f32_e32 v111, v111
	v_pk_fma_f32 v[114:115], s[84:85], v[22:23], v[114:115]
	v_pk_mul_f32 v[110:111], v[24:25], v[110:111]
	v_pk_mul_f32 v[104:105], v[68:69], v[10:11] op_sel:[1,0]
	v_pk_fma_f32 v[24:25], v[112:113], s[70:71], v[110:111] op_sel_hi:[0,1,1]
	v_exp_f32_e32 v104, v104
	v_pk_fma_f32 v[114:115], s[86:87], v[24:25], v[114:115]
	v_exp_f32_e32 v105, v105
	v_pk_mul_f32 v[106:107], v[68:69], v[12:13] op_sel:[1,0]
	v_pk_mul_f32 v[104:105], v[26:27], v[104:105]
	v_exp_f32_e32 v106, v106
	v_pk_fma_f32 v[26:27], v[112:113], s[72:73], v[104:105] op_sel_hi:[0,1,1]
	v_exp_f32_e32 v107, v107
	v_pk_fma_f32 v[114:115], s[88:89], v[26:27], v[114:115]
	v_pk_mul_f32 v[106:107], v[28:29], v[106:107]
	v_pk_mul_f32 v[108:109], v[68:69], v[14:15] op_sel:[1,0]
	v_pk_fma_f32 v[28:29], v[112:113], s[74:75], v[106:107] op_sel_hi:[0,1,1]
	v_exp_f32_e32 v108, v108
	v_pk_fma_f32 v[114:115], s[90:91], v[28:29], v[114:115]
	v_exp_f32_e32 v109, v109
	v_pk_mul_f32 v[110:111], v[68:69], v[16:17] op_sel:[1,0]
	v_pk_mul_f32 v[108:109], v[30:31], v[108:109]
	v_exp_f32_e32 v110, v110
	v_pk_fma_f32 v[30:31], v[112:113], s[76:77], v[108:109] op_sel_hi:[0,1,1]
	v_exp_f32_e32 v111, v111
	v_pk_fma_f32 v[114:115], s[92:93], v[30:31], v[114:115]
	v_pk_mul_f32 v[110:111], v[32:33], v[110:111]
	v_cvt_f32_f16_sdwa v117, v79 dst_sel:DWORD dst_unused:UNUSED_PAD src0_sel:WORD_1
	v_pk_fma_f32 v[32:33], v[112:113], s[78:79], v[110:111] op_sel_hi:[0,1,1]
	s_nop 0
	v_pk_fma_f32 v[114:115], s[94:95], v[32:33], v[114:115]
	s_nop 0
	v_add_f32_e32 v116, v114, v115
	v_fmac_f32_e32 v116, v98, v113
	v_mul_f32_e32 v116, v116, v117
	v_fma_mixlo_f16 v116, v116, s30, 0
	global_store_short v99, v116, s[26:27]
	s_add_u32 s26, s26, 0x1000
	s_addc_u32 s27, s27, 0
	s_waitcnt lgkmcnt(0)
	s_load_dwordx16 s[64:79], s[24:25], 0xa80
	s_load_dwordx16 s[80:95], s[24:25], 0xac0
	v_cvt_f32_f16_e32 v113, v76
	v_mul_f32_e32 v112, v70, v113
	v_pk_mul_f32 v[104:105], v[70:71], v[2:3] op_sel_hi:[0,1]
	v_pk_mul_f32 v[106:107], v[70:71], v[4:5] op_sel_hi:[0,1]
	v_exp_f32_e32 v104, v104
	v_exp_f32_e32 v105, v105
	v_exp_f32_e32 v106, v106
	v_pk_mul_f32 v[104:105], v[18:19], v[104:105]
	v_exp_f32_e32 v107, v107
	v_pk_fma_f32 v[18:19], v[112:113], s[32:33], v[104:105] op_sel_hi:[0,1,1]
	v_pk_mul_f32 v[106:107], v[20:21], v[106:107]
	v_pk_fma_f32 v[114:115], s[48:49], v[18:19], 0 op_sel_hi:[1,1,0]
	v_pk_fma_f32 v[20:21], v[112:113], s[34:35], v[106:107] op_sel_hi:[0,1,1]
	v_pk_mul_f32 v[108:109], v[70:71], v[6:7] op_sel_hi:[0,1]
	v_pk_fma_f32 v[114:115], s[50:51], v[20:21], v[114:115]
	v_exp_f32_e32 v108, v108
	v_exp_f32_e32 v109, v109
	v_pk_mul_f32 v[110:111], v[70:71], v[8:9] op_sel_hi:[0,1]
	v_pk_mul_f32 v[108:109], v[22:23], v[108:109]
	v_exp_f32_e32 v110, v110
	v_pk_fma_f32 v[22:23], v[112:113], s[36:37], v[108:109] op_sel_hi:[0,1,1]
	v_exp_f32_e32 v111, v111
	v_pk_fma_f32 v[114:115], s[52:53], v[22:23], v[114:115]
	v_pk_mul_f32 v[110:111], v[24:25], v[110:111]
	v_pk_mul_f32 v[104:105], v[70:71], v[10:11] op_sel_hi:[0,1]
	v_pk_fma_f32 v[24:25], v[112:113], s[38:39], v[110:111] op_sel_hi:[0,1,1]
	v_exp_f32_e32 v104, v104
	v_pk_fma_f32 v[114:115], s[54:55], v[24:25], v[114:115]
	v_exp_f32_e32 v105, v105
	v_pk_mul_f32 v[106:107], v[70:71], v[12:13] op_sel_hi:[0,1]
	v_pk_mul_f32 v[104:105], v[26:27], v[104:105]
	v_exp_f32_e32 v106, v106
	v_pk_fma_f32 v[26:27], v[112:113], s[40:41], v[104:105] op_sel_hi:[0,1,1]
	v_exp_f32_e32 v107, v107
	v_pk_fma_f32 v[114:115], s[56:57], v[26:27], v[114:115]
	v_pk_mul_f32 v[106:107], v[28:29], v[106:107]
	v_pk_mul_f32 v[108:109], v[70:71], v[14:15] op_sel_hi:[0,1]
	v_pk_fma_f32 v[28:29], v[112:113], s[42:43], v[106:107] op_sel_hi:[0,1,1]
	v_exp_f32_e32 v108, v108
	v_pk_fma_f32 v[114:115], s[58:59], v[28:29], v[114:115]
	v_exp_f32_e32 v109, v109
	v_pk_mul_f32 v[110:111], v[70:71], v[16:17] op_sel_hi:[0,1]
	v_pk_mul_f32 v[108:109], v[30:31], v[108:109]
	v_exp_f32_e32 v110, v110
	v_pk_fma_f32 v[30:31], v[112:113], s[44:45], v[108:109] op_sel_hi:[0,1,1]
	v_exp_f32_e32 v111, v111
	v_pk_fma_f32 v[114:115], s[60:61], v[30:31], v[114:115]
	v_pk_mul_f32 v[110:111], v[32:33], v[110:111]
	v_cvt_f32_f16_e32 v117, v80
	v_pk_fma_f32 v[32:33], v[112:113], s[46:47], v[110:111] op_sel_hi:[0,1,1]
	s_nop 0
	v_pk_fma_f32 v[114:115], s[62:63], v[32:33], v[114:115]
	s_nop 0
	v_add_f32_e32 v116, v114, v115
	v_fmac_f32_e32 v116, v98, v113
	v_mul_f32_e32 v116, v116, v117
	v_fma_mixlo_f16 v116, v116, s30, 0
	global_store_short v99, v116, s[26:27]
	s_add_u32 s26, s26, 0x1000
	s_addc_u32 s27, s27, 0
	s_waitcnt lgkmcnt(0)
	s_load_dwordx16 s[32:47], s[24:25], 0xb00
	s_load_dwordx16 s[48:63], s[24:25], 0xb40
	v_cvt_f32_f16_sdwa v113, v76 dst_sel:DWORD dst_unused:UNUSED_PAD src0_sel:WORD_1
	v_pk_mul_f32 v[104:105], v[70:71], v[2:3] op_sel:[1,0]
	v_mul_f32_e32 v112, v71, v113
	v_exp_f32_e32 v104, v104
	v_exp_f32_e32 v105, v105
	v_pk_mul_f32 v[106:107], v[70:71], v[4:5] op_sel:[1,0]
	v_pk_mul_f32 v[104:105], v[18:19], v[104:105]
	v_exp_f32_e32 v106, v106
	v_pk_fma_f32 v[18:19], v[112:113], s[64:65], v[104:105] op_sel_hi:[0,1,1]
	v_exp_f32_e32 v107, v107
	v_pk_fma_f32 v[114:115], s[80:81], v[18:19], 0 op_sel_hi:[1,1,0]
	v_pk_mul_f32 v[106:107], v[20:21], v[106:107]
	v_pk_mul_f32 v[108:109], v[70:71], v[6:7] op_sel:[1,0]
	v_pk_fma_f32 v[20:21], v[112:113], s[66:67], v[106:107] op_sel_hi:[0,1,1]
	v_exp_f32_e32 v108, v108
	v_pk_fma_f32 v[114:115], s[82:83], v[20:21], v[114:115]
	v_exp_f32_e32 v109, v109
	v_pk_mul_f32 v[110:111], v[70:71], v[8:9] op_sel:[1,0]
	v_pk_mul_f32 v[108:109], v[22:23], v[108:109]
	v_exp_f32_e32 v110, v110
	v_pk_fma_f32 v[22:23], v[112:113], s[68:69], v[108:109] op_sel_hi:[0,1,1]
	v_exp_f32_e32 v111, v111
	v_pk_fma_f32 v[114:115], s[84:85], v[22:23], v[114:115]
	v_pk_mul_f32 v[110:111], v[24:25], v[110:111]
	v_pk_mul_f32 v[104:105], v[70:71], v[10:11] op_sel:[1,0]
	v_pk_fma_f32 v[24:25], v[112:113], s[70:71], v[110:111] op_sel_hi:[0,1,1]
	v_exp_f32_e32 v104, v104
	v_pk_fma_f32 v[114:115], s[86:87], v[24:25], v[114:115]
	v_exp_f32_e32 v105, v105
	v_pk_mul_f32 v[106:107], v[70:71], v[12:13] op_sel:[1,0]
	v_pk_mul_f32 v[104:105], v[26:27], v[104:105]
	v_exp_f32_e32 v106, v106
	v_pk_fma_f32 v[26:27], v[112:113], s[72:73], v[104:105] op_sel_hi:[0,1,1]
	v_exp_f32_e32 v107, v107
	v_pk_fma_f32 v[114:115], s[88:89], v[26:27], v[114:115]
	v_pk_mul_f32 v[106:107], v[28:29], v[106:107]
	v_pk_mul_f32 v[108:109], v[70:71], v[14:15] op_sel:[1,0]
	v_pk_fma_f32 v[28:29], v[112:113], s[74:75], v[106:107] op_sel_hi:[0,1,1]
	v_exp_f32_e32 v108, v108
	v_pk_fma_f32 v[114:115], s[90:91], v[28:29], v[114:115]
	v_exp_f32_e32 v109, v109
	v_pk_mul_f32 v[110:111], v[70:71], v[16:17] op_sel:[1,0]
	v_pk_mul_f32 v[108:109], v[30:31], v[108:109]
	v_exp_f32_e32 v110, v110
	v_pk_fma_f32 v[30:31], v[112:113], s[76:77], v[108:109] op_sel_hi:[0,1,1]
	v_exp_f32_e32 v111, v111
	v_pk_fma_f32 v[114:115], s[92:93], v[30:31], v[114:115]
	v_pk_mul_f32 v[110:111], v[32:33], v[110:111]
	v_cvt_f32_f16_sdwa v117, v80 dst_sel:DWORD dst_unused:UNUSED_PAD src0_sel:WORD_1
	v_pk_fma_f32 v[32:33], v[112:113], s[78:79], v[110:111] op_sel_hi:[0,1,1]
	s_nop 0
	v_pk_fma_f32 v[114:115], s[94:95], v[32:33], v[114:115]
	s_nop 0
	v_add_f32_e32 v116, v114, v115
	v_fmac_f32_e32 v116, v98, v113
	v_mul_f32_e32 v116, v116, v117
	v_fma_mixlo_f16 v116, v116, s30, 0
	global_store_short v99, v116, s[26:27]
	s_add_u32 s26, s26, 0x1000
	s_addc_u32 s27, s27, 0
	s_waitcnt lgkmcnt(0)
	s_load_dwordx16 s[64:79], s[24:25], 0xb80
	s_load_dwordx16 s[80:95], s[24:25], 0xbc0
	v_cvt_f32_f16_e32 v113, v77
	v_mul_f32_e32 v112, v72, v113
	v_pk_mul_f32 v[104:105], v[72:73], v[2:3] op_sel_hi:[0,1]
	v_pk_mul_f32 v[106:107], v[72:73], v[4:5] op_sel_hi:[0,1]
	v_exp_f32_e32 v104, v104
	v_exp_f32_e32 v105, v105
	v_exp_f32_e32 v106, v106
	v_pk_mul_f32 v[104:105], v[18:19], v[104:105]
	v_exp_f32_e32 v107, v107
	v_pk_fma_f32 v[18:19], v[112:113], s[32:33], v[104:105] op_sel_hi:[0,1,1]
	v_pk_mul_f32 v[106:107], v[20:21], v[106:107]
	v_pk_fma_f32 v[114:115], s[48:49], v[18:19], 0 op_sel_hi:[1,1,0]
	v_pk_fma_f32 v[20:21], v[112:113], s[34:35], v[106:107] op_sel_hi:[0,1,1]
	v_pk_mul_f32 v[108:109], v[72:73], v[6:7] op_sel_hi:[0,1]
	v_pk_fma_f32 v[114:115], s[50:51], v[20:21], v[114:115]
	v_exp_f32_e32 v108, v108
	v_exp_f32_e32 v109, v109
	v_pk_mul_f32 v[110:111], v[72:73], v[8:9] op_sel_hi:[0,1]
	v_pk_mul_f32 v[108:109], v[22:23], v[108:109]
	v_exp_f32_e32 v110, v110
	v_pk_fma_f32 v[22:23], v[112:113], s[36:37], v[108:109] op_sel_hi:[0,1,1]
	v_exp_f32_e32 v111, v111
	v_pk_fma_f32 v[114:115], s[52:53], v[22:23], v[114:115]
	v_pk_mul_f32 v[110:111], v[24:25], v[110:111]
	v_pk_mul_f32 v[104:105], v[72:73], v[10:11] op_sel_hi:[0,1]
	v_pk_fma_f32 v[24:25], v[112:113], s[38:39], v[110:111] op_sel_hi:[0,1,1]
	v_exp_f32_e32 v104, v104
	v_pk_fma_f32 v[114:115], s[54:55], v[24:25], v[114:115]
	v_exp_f32_e32 v105, v105
	v_pk_mul_f32 v[106:107], v[72:73], v[12:13] op_sel_hi:[0,1]
	v_pk_mul_f32 v[104:105], v[26:27], v[104:105]
	v_exp_f32_e32 v106, v106
	v_pk_fma_f32 v[26:27], v[112:113], s[40:41], v[104:105] op_sel_hi:[0,1,1]
	v_exp_f32_e32 v107, v107
	v_pk_fma_f32 v[114:115], s[56:57], v[26:27], v[114:115]
	v_pk_mul_f32 v[106:107], v[28:29], v[106:107]
	v_pk_mul_f32 v[108:109], v[72:73], v[14:15] op_sel_hi:[0,1]
	v_pk_fma_f32 v[28:29], v[112:113], s[42:43], v[106:107] op_sel_hi:[0,1,1]
	v_exp_f32_e32 v108, v108
	v_pk_fma_f32 v[114:115], s[58:59], v[28:29], v[114:115]
	v_exp_f32_e32 v109, v109
	v_pk_mul_f32 v[110:111], v[72:73], v[16:17] op_sel_hi:[0,1]
	v_pk_mul_f32 v[108:109], v[30:31], v[108:109]
	v_exp_f32_e32 v110, v110
	v_pk_fma_f32 v[30:31], v[112:113], s[44:45], v[108:109] op_sel_hi:[0,1,1]
	v_exp_f32_e32 v111, v111
	v_pk_fma_f32 v[114:115], s[60:61], v[30:31], v[114:115]
	v_pk_mul_f32 v[110:111], v[32:33], v[110:111]
	v_cvt_f32_f16_e32 v117, v81
	v_pk_fma_f32 v[32:33], v[112:113], s[46:47], v[110:111] op_sel_hi:[0,1,1]
	s_nop 0
	v_pk_fma_f32 v[114:115], s[62:63], v[32:33], v[114:115]
	s_nop 0
	v_add_f32_e32 v116, v114, v115
	v_fmac_f32_e32 v116, v98, v113
	v_mul_f32_e32 v116, v116, v117
	v_fma_mixlo_f16 v116, v116, s30, 0
	global_store_short v99, v116, s[26:27]
	s_add_u32 s26, s26, 0x1000
	s_addc_u32 s27, s27, 0
	s_waitcnt lgkmcnt(0)
	s_load_dwordx16 s[32:47], s[24:25], 0xc00
	s_load_dwordx16 s[48:63], s[24:25], 0xc40
	v_cvt_f32_f16_sdwa v113, v77 dst_sel:DWORD dst_unused:UNUSED_PAD src0_sel:WORD_1
	v_pk_mul_f32 v[104:105], v[72:73], v[2:3] op_sel:[1,0]
	v_mul_f32_e32 v112, v73, v113
	v_exp_f32_e32 v104, v104
	v_exp_f32_e32 v105, v105
	v_pk_mul_f32 v[106:107], v[72:73], v[4:5] op_sel:[1,0]
	v_pk_mul_f32 v[104:105], v[18:19], v[104:105]
	v_exp_f32_e32 v106, v106
	v_pk_fma_f32 v[18:19], v[112:113], s[64:65], v[104:105] op_sel_hi:[0,1,1]
	v_exp_f32_e32 v107, v107
	v_pk_fma_f32 v[114:115], s[80:81], v[18:19], 0 op_sel_hi:[1,1,0]
	v_pk_mul_f32 v[106:107], v[20:21], v[106:107]
	v_pk_mul_f32 v[108:109], v[72:73], v[6:7] op_sel:[1,0]
	v_pk_fma_f32 v[20:21], v[112:113], s[66:67], v[106:107] op_sel_hi:[0,1,1]
	v_exp_f32_e32 v108, v108
	v_pk_fma_f32 v[114:115], s[82:83], v[20:21], v[114:115]
	v_exp_f32_e32 v109, v109
	v_pk_mul_f32 v[110:111], v[72:73], v[8:9] op_sel:[1,0]
	v_pk_mul_f32 v[108:109], v[22:23], v[108:109]
	v_exp_f32_e32 v110, v110
	v_pk_fma_f32 v[22:23], v[112:113], s[68:69], v[108:109] op_sel_hi:[0,1,1]
	v_exp_f32_e32 v111, v111
	v_pk_fma_f32 v[114:115], s[84:85], v[22:23], v[114:115]
	v_pk_mul_f32 v[110:111], v[24:25], v[110:111]
	v_pk_mul_f32 v[104:105], v[72:73], v[10:11] op_sel:[1,0]
	v_pk_fma_f32 v[24:25], v[112:113], s[70:71], v[110:111] op_sel_hi:[0,1,1]
	v_exp_f32_e32 v104, v104
	v_pk_fma_f32 v[114:115], s[86:87], v[24:25], v[114:115]
	v_exp_f32_e32 v105, v105
	v_pk_mul_f32 v[106:107], v[72:73], v[12:13] op_sel:[1,0]
	v_pk_mul_f32 v[104:105], v[26:27], v[104:105]
	v_exp_f32_e32 v106, v106
	v_pk_fma_f32 v[26:27], v[112:113], s[72:73], v[104:105] op_sel_hi:[0,1,1]
	v_exp_f32_e32 v107, v107
	v_pk_fma_f32 v[114:115], s[88:89], v[26:27], v[114:115]
	v_pk_mul_f32 v[106:107], v[28:29], v[106:107]
	v_pk_mul_f32 v[108:109], v[72:73], v[14:15] op_sel:[1,0]
	v_pk_fma_f32 v[28:29], v[112:113], s[74:75], v[106:107] op_sel_hi:[0,1,1]
	v_exp_f32_e32 v108, v108
	v_pk_fma_f32 v[114:115], s[90:91], v[28:29], v[114:115]
	v_exp_f32_e32 v109, v109
	v_pk_mul_f32 v[110:111], v[72:73], v[16:17] op_sel:[1,0]
	v_pk_mul_f32 v[108:109], v[30:31], v[108:109]
	v_exp_f32_e32 v110, v110
	v_pk_fma_f32 v[30:31], v[112:113], s[76:77], v[108:109] op_sel_hi:[0,1,1]
	v_exp_f32_e32 v111, v111
	v_pk_fma_f32 v[114:115], s[92:93], v[30:31], v[114:115]
	v_pk_mul_f32 v[110:111], v[32:33], v[110:111]
	v_cvt_f32_f16_sdwa v117, v81 dst_sel:DWORD dst_unused:UNUSED_PAD src0_sel:WORD_1
	v_pk_fma_f32 v[32:33], v[112:113], s[78:79], v[110:111] op_sel_hi:[0,1,1]
	s_nop 0
	v_pk_fma_f32 v[114:115], s[94:95], v[32:33], v[114:115]
	s_nop 0
	v_add_f32_e32 v116, v114, v115
	v_fmac_f32_e32 v116, v98, v113
	v_mul_f32_e32 v116, v116, v117
	v_fma_mixlo_f16 v116, v116, s30, 0
	global_store_short v99, v116, s[26:27]
	s_add_u32 s26, s26, 0x1000
	s_addc_u32 s27, s27, 0
	s_waitcnt vmcnt(8)
	s_waitcnt lgkmcnt(0)
	s_load_dwordx16 s[64:79], s[24:25], 0xc80
	s_load_dwordx16 s[80:95], s[24:25], 0xcc0
	v_cvt_f32_f16_e32 v113, v90
	v_mul_f32_e32 v112, v82, v113
	v_pk_mul_f32 v[104:105], v[82:83], v[2:3] op_sel_hi:[0,1]
	v_pk_mul_f32 v[106:107], v[82:83], v[4:5] op_sel_hi:[0,1]
	v_exp_f32_e32 v104, v104
	v_exp_f32_e32 v105, v105
	v_exp_f32_e32 v106, v106
	v_pk_mul_f32 v[104:105], v[18:19], v[104:105]
	v_exp_f32_e32 v107, v107
	v_pk_fma_f32 v[18:19], v[112:113], s[32:33], v[104:105] op_sel_hi:[0,1,1]
	v_pk_mul_f32 v[106:107], v[20:21], v[106:107]
	v_pk_fma_f32 v[114:115], s[48:49], v[18:19], 0 op_sel_hi:[1,1,0]
	v_pk_fma_f32 v[20:21], v[112:113], s[34:35], v[106:107] op_sel_hi:[0,1,1]
	v_pk_mul_f32 v[108:109], v[82:83], v[6:7] op_sel_hi:[0,1]
	v_pk_fma_f32 v[114:115], s[50:51], v[20:21], v[114:115]
	v_exp_f32_e32 v108, v108
	v_exp_f32_e32 v109, v109
	v_pk_mul_f32 v[110:111], v[82:83], v[8:9] op_sel_hi:[0,1]
	v_pk_mul_f32 v[108:109], v[22:23], v[108:109]
	v_exp_f32_e32 v110, v110
	v_pk_fma_f32 v[22:23], v[112:113], s[36:37], v[108:109] op_sel_hi:[0,1,1]
	v_exp_f32_e32 v111, v111
	v_pk_fma_f32 v[114:115], s[52:53], v[22:23], v[114:115]
	v_pk_mul_f32 v[110:111], v[24:25], v[110:111]
	v_pk_mul_f32 v[104:105], v[82:83], v[10:11] op_sel_hi:[0,1]
	v_pk_fma_f32 v[24:25], v[112:113], s[38:39], v[110:111] op_sel_hi:[0,1,1]
	v_exp_f32_e32 v104, v104
	v_pk_fma_f32 v[114:115], s[54:55], v[24:25], v[114:115]
	v_exp_f32_e32 v105, v105
	v_pk_mul_f32 v[106:107], v[82:83], v[12:13] op_sel_hi:[0,1]
	v_pk_mul_f32 v[104:105], v[26:27], v[104:105]
	v_exp_f32_e32 v106, v106
	v_pk_fma_f32 v[26:27], v[112:113], s[40:41], v[104:105] op_sel_hi:[0,1,1]
	v_exp_f32_e32 v107, v107
	v_pk_fma_f32 v[114:115], s[56:57], v[26:27], v[114:115]
	v_pk_mul_f32 v[106:107], v[28:29], v[106:107]
	v_pk_mul_f32 v[108:109], v[82:83], v[14:15] op_sel_hi:[0,1]
	v_pk_fma_f32 v[28:29], v[112:113], s[42:43], v[106:107] op_sel_hi:[0,1,1]
	v_exp_f32_e32 v108, v108
	v_pk_fma_f32 v[114:115], s[58:59], v[28:29], v[114:115]
	v_exp_f32_e32 v109, v109
	v_pk_mul_f32 v[110:111], v[82:83], v[16:17] op_sel_hi:[0,1]
	v_pk_mul_f32 v[108:109], v[30:31], v[108:109]
	v_exp_f32_e32 v110, v110
	v_pk_fma_f32 v[30:31], v[112:113], s[44:45], v[108:109] op_sel_hi:[0,1,1]
	v_exp_f32_e32 v111, v111
	v_pk_fma_f32 v[114:115], s[60:61], v[30:31], v[114:115]
	v_pk_mul_f32 v[110:111], v[32:33], v[110:111]
	v_cvt_f32_f16_e32 v117, v94
	v_pk_fma_f32 v[32:33], v[112:113], s[46:47], v[110:111] op_sel_hi:[0,1,1]
	s_nop 0
	v_pk_fma_f32 v[114:115], s[62:63], v[32:33], v[114:115]
	s_nop 0
	v_add_f32_e32 v116, v114, v115
	v_fmac_f32_e32 v116, v98, v113
	v_mul_f32_e32 v116, v116, v117
	v_fma_mixlo_f16 v116, v116, s30, 0
	global_store_short v99, v116, s[26:27]
	s_add_u32 s26, s26, 0x1000
	s_addc_u32 s27, s27, 0
	s_waitcnt lgkmcnt(0)
	s_load_dwordx16 s[32:47], s[24:25], 0xd00
	s_load_dwordx16 s[48:63], s[24:25], 0xd40
	v_cvt_f32_f16_sdwa v113, v90 dst_sel:DWORD dst_unused:UNUSED_PAD src0_sel:WORD_1
	v_pk_mul_f32 v[104:105], v[82:83], v[2:3] op_sel:[1,0]
	v_mul_f32_e32 v112, v83, v113
	v_exp_f32_e32 v104, v104
	v_exp_f32_e32 v105, v105
	v_pk_mul_f32 v[106:107], v[82:83], v[4:5] op_sel:[1,0]
	v_pk_mul_f32 v[104:105], v[18:19], v[104:105]
	v_exp_f32_e32 v106, v106
	v_pk_fma_f32 v[18:19], v[112:113], s[64:65], v[104:105] op_sel_hi:[0,1,1]
	v_exp_f32_e32 v107, v107
	v_pk_fma_f32 v[114:115], s[80:81], v[18:19], 0 op_sel_hi:[1,1,0]
	v_pk_mul_f32 v[106:107], v[20:21], v[106:107]
	v_pk_mul_f32 v[108:109], v[82:83], v[6:7] op_sel:[1,0]
	v_pk_fma_f32 v[20:21], v[112:113], s[66:67], v[106:107] op_sel_hi:[0,1,1]
	v_exp_f32_e32 v108, v108
	v_pk_fma_f32 v[114:115], s[82:83], v[20:21], v[114:115]
	v_exp_f32_e32 v109, v109
	v_pk_mul_f32 v[110:111], v[82:83], v[8:9] op_sel:[1,0]
	v_pk_mul_f32 v[108:109], v[22:23], v[108:109]
	v_exp_f32_e32 v110, v110
	v_pk_fma_f32 v[22:23], v[112:113], s[68:69], v[108:109] op_sel_hi:[0,1,1]
	v_exp_f32_e32 v111, v111
	v_pk_fma_f32 v[114:115], s[84:85], v[22:23], v[114:115]
	v_pk_mul_f32 v[110:111], v[24:25], v[110:111]
	v_pk_mul_f32 v[104:105], v[82:83], v[10:11] op_sel:[1,0]
	v_pk_fma_f32 v[24:25], v[112:113], s[70:71], v[110:111] op_sel_hi:[0,1,1]
	v_exp_f32_e32 v104, v104
	v_pk_fma_f32 v[114:115], s[86:87], v[24:25], v[114:115]
	v_exp_f32_e32 v105, v105
	v_pk_mul_f32 v[106:107], v[82:83], v[12:13] op_sel:[1,0]
	v_pk_mul_f32 v[104:105], v[26:27], v[104:105]
	v_exp_f32_e32 v106, v106
	v_pk_fma_f32 v[26:27], v[112:113], s[72:73], v[104:105] op_sel_hi:[0,1,1]
	v_exp_f32_e32 v107, v107
	v_pk_fma_f32 v[114:115], s[88:89], v[26:27], v[114:115]
	v_pk_mul_f32 v[106:107], v[28:29], v[106:107]
	v_pk_mul_f32 v[108:109], v[82:83], v[14:15] op_sel:[1,0]
	v_pk_fma_f32 v[28:29], v[112:113], s[74:75], v[106:107] op_sel_hi:[0,1,1]
	v_exp_f32_e32 v108, v108
	v_pk_fma_f32 v[114:115], s[90:91], v[28:29], v[114:115]
	v_exp_f32_e32 v109, v109
	v_pk_mul_f32 v[110:111], v[82:83], v[16:17] op_sel:[1,0]
	v_pk_mul_f32 v[108:109], v[30:31], v[108:109]
	v_exp_f32_e32 v110, v110
	v_pk_fma_f32 v[30:31], v[112:113], s[76:77], v[108:109] op_sel_hi:[0,1,1]
	v_exp_f32_e32 v111, v111
	v_pk_fma_f32 v[114:115], s[92:93], v[30:31], v[114:115]
	v_pk_mul_f32 v[110:111], v[32:33], v[110:111]
	v_cvt_f32_f16_sdwa v117, v94 dst_sel:DWORD dst_unused:UNUSED_PAD src0_sel:WORD_1
	v_pk_fma_f32 v[32:33], v[112:113], s[78:79], v[110:111] op_sel_hi:[0,1,1]
	s_nop 0
	v_pk_fma_f32 v[114:115], s[94:95], v[32:33], v[114:115]
	s_nop 0
	v_add_f32_e32 v116, v114, v115
	v_fmac_f32_e32 v116, v98, v113
	v_mul_f32_e32 v116, v116, v117
	v_fma_mixlo_f16 v116, v116, s30, 0
	global_store_short v99, v116, s[26:27]
	s_add_u32 s26, s26, 0x1000
	s_addc_u32 s27, s27, 0
	s_waitcnt lgkmcnt(0)
	s_load_dwordx16 s[64:79], s[24:25], 0xd80
	s_load_dwordx16 s[80:95], s[24:25], 0xdc0
	v_cvt_f32_f16_e32 v113, v91
	v_mul_f32_e32 v112, v84, v113
	v_pk_mul_f32 v[104:105], v[84:85], v[2:3] op_sel_hi:[0,1]
	v_pk_mul_f32 v[106:107], v[84:85], v[4:5] op_sel_hi:[0,1]
	v_exp_f32_e32 v104, v104
	v_exp_f32_e32 v105, v105
	v_exp_f32_e32 v106, v106
	v_pk_mul_f32 v[104:105], v[18:19], v[104:105]
	v_exp_f32_e32 v107, v107
	v_pk_fma_f32 v[18:19], v[112:113], s[32:33], v[104:105] op_sel_hi:[0,1,1]
	v_pk_mul_f32 v[106:107], v[20:21], v[106:107]
	v_pk_fma_f32 v[114:115], s[48:49], v[18:19], 0 op_sel_hi:[1,1,0]
	v_pk_fma_f32 v[20:21], v[112:113], s[34:35], v[106:107] op_sel_hi:[0,1,1]
	v_pk_mul_f32 v[108:109], v[84:85], v[6:7] op_sel_hi:[0,1]
	v_pk_fma_f32 v[114:115], s[50:51], v[20:21], v[114:115]
	v_exp_f32_e32 v108, v108
	v_exp_f32_e32 v109, v109
	v_pk_mul_f32 v[110:111], v[84:85], v[8:9] op_sel_hi:[0,1]
	v_pk_mul_f32 v[108:109], v[22:23], v[108:109]
	v_exp_f32_e32 v110, v110
	v_pk_fma_f32 v[22:23], v[112:113], s[36:37], v[108:109] op_sel_hi:[0,1,1]
	v_exp_f32_e32 v111, v111
	v_pk_fma_f32 v[114:115], s[52:53], v[22:23], v[114:115]
	v_pk_mul_f32 v[110:111], v[24:25], v[110:111]
	v_pk_mul_f32 v[104:105], v[84:85], v[10:11] op_sel_hi:[0,1]
	v_pk_fma_f32 v[24:25], v[112:113], s[38:39], v[110:111] op_sel_hi:[0,1,1]
	v_exp_f32_e32 v104, v104
	v_pk_fma_f32 v[114:115], s[54:55], v[24:25], v[114:115]
	v_exp_f32_e32 v105, v105
	v_pk_mul_f32 v[106:107], v[84:85], v[12:13] op_sel_hi:[0,1]
	v_pk_mul_f32 v[104:105], v[26:27], v[104:105]
	v_exp_f32_e32 v106, v106
	v_pk_fma_f32 v[26:27], v[112:113], s[40:41], v[104:105] op_sel_hi:[0,1,1]
	v_exp_f32_e32 v107, v107
	v_pk_fma_f32 v[114:115], s[56:57], v[26:27], v[114:115]
	v_pk_mul_f32 v[106:107], v[28:29], v[106:107]
	v_pk_mul_f32 v[108:109], v[84:85], v[14:15] op_sel_hi:[0,1]
	v_pk_fma_f32 v[28:29], v[112:113], s[42:43], v[106:107] op_sel_hi:[0,1,1]
	v_exp_f32_e32 v108, v108
	v_pk_fma_f32 v[114:115], s[58:59], v[28:29], v[114:115]
	v_exp_f32_e32 v109, v109
	v_pk_mul_f32 v[110:111], v[84:85], v[16:17] op_sel_hi:[0,1]
	v_pk_mul_f32 v[108:109], v[30:31], v[108:109]
	v_exp_f32_e32 v110, v110
	v_pk_fma_f32 v[30:31], v[112:113], s[44:45], v[108:109] op_sel_hi:[0,1,1]
	v_exp_f32_e32 v111, v111
	v_pk_fma_f32 v[114:115], s[60:61], v[30:31], v[114:115]
	v_pk_mul_f32 v[110:111], v[32:33], v[110:111]
	v_cvt_f32_f16_e32 v117, v95
	v_pk_fma_f32 v[32:33], v[112:113], s[46:47], v[110:111] op_sel_hi:[0,1,1]
	s_nop 0
	v_pk_fma_f32 v[114:115], s[62:63], v[32:33], v[114:115]
	s_nop 0
	v_add_f32_e32 v116, v114, v115
	v_fmac_f32_e32 v116, v98, v113
	v_mul_f32_e32 v116, v116, v117
	v_fma_mixlo_f16 v116, v116, s30, 0
	global_store_short v99, v116, s[26:27]
	s_add_u32 s26, s26, 0x1000
	s_addc_u32 s27, s27, 0
	s_waitcnt lgkmcnt(0)
	s_load_dwordx16 s[32:47], s[24:25], 0xe00
	s_load_dwordx16 s[48:63], s[24:25], 0xe40
	v_cvt_f32_f16_sdwa v113, v91 dst_sel:DWORD dst_unused:UNUSED_PAD src0_sel:WORD_1
	v_pk_mul_f32 v[104:105], v[84:85], v[2:3] op_sel:[1,0]
	v_mul_f32_e32 v112, v85, v113
	v_exp_f32_e32 v104, v104
	v_exp_f32_e32 v105, v105
	v_pk_mul_f32 v[106:107], v[84:85], v[4:5] op_sel:[1,0]
	v_pk_mul_f32 v[104:105], v[18:19], v[104:105]
	v_exp_f32_e32 v106, v106
	v_pk_fma_f32 v[18:19], v[112:113], s[64:65], v[104:105] op_sel_hi:[0,1,1]
	v_exp_f32_e32 v107, v107
	v_pk_fma_f32 v[114:115], s[80:81], v[18:19], 0 op_sel_hi:[1,1,0]
	v_pk_mul_f32 v[106:107], v[20:21], v[106:107]
	v_pk_mul_f32 v[108:109], v[84:85], v[6:7] op_sel:[1,0]
	v_pk_fma_f32 v[20:21], v[112:113], s[66:67], v[106:107] op_sel_hi:[0,1,1]
	v_exp_f32_e32 v108, v108
	v_pk_fma_f32 v[114:115], s[82:83], v[20:21], v[114:115]
	v_exp_f32_e32 v109, v109
	v_pk_mul_f32 v[110:111], v[84:85], v[8:9] op_sel:[1,0]
	v_pk_mul_f32 v[108:109], v[22:23], v[108:109]
	v_exp_f32_e32 v110, v110
	v_pk_fma_f32 v[22:23], v[112:113], s[68:69], v[108:109] op_sel_hi:[0,1,1]
	v_exp_f32_e32 v111, v111
	v_pk_fma_f32 v[114:115], s[84:85], v[22:23], v[114:115]
	v_pk_mul_f32 v[110:111], v[24:25], v[110:111]
	v_pk_mul_f32 v[104:105], v[84:85], v[10:11] op_sel:[1,0]
	v_pk_fma_f32 v[24:25], v[112:113], s[70:71], v[110:111] op_sel_hi:[0,1,1]
	v_exp_f32_e32 v104, v104
	v_pk_fma_f32 v[114:115], s[86:87], v[24:25], v[114:115]
	v_exp_f32_e32 v105, v105
	v_pk_mul_f32 v[106:107], v[84:85], v[12:13] op_sel:[1,0]
	v_pk_mul_f32 v[104:105], v[26:27], v[104:105]
	v_exp_f32_e32 v106, v106
	v_pk_fma_f32 v[26:27], v[112:113], s[72:73], v[104:105] op_sel_hi:[0,1,1]
	v_exp_f32_e32 v107, v107
	v_pk_fma_f32 v[114:115], s[88:89], v[26:27], v[114:115]
	v_pk_mul_f32 v[106:107], v[28:29], v[106:107]
	v_pk_mul_f32 v[108:109], v[84:85], v[14:15] op_sel:[1,0]
	v_pk_fma_f32 v[28:29], v[112:113], s[74:75], v[106:107] op_sel_hi:[0,1,1]
	v_exp_f32_e32 v108, v108
	v_pk_fma_f32 v[114:115], s[90:91], v[28:29], v[114:115]
	v_exp_f32_e32 v109, v109
	v_pk_mul_f32 v[110:111], v[84:85], v[16:17] op_sel:[1,0]
	v_pk_mul_f32 v[108:109], v[30:31], v[108:109]
	v_exp_f32_e32 v110, v110
	v_pk_fma_f32 v[30:31], v[112:113], s[76:77], v[108:109] op_sel_hi:[0,1,1]
	v_exp_f32_e32 v111, v111
	v_pk_fma_f32 v[114:115], s[92:93], v[30:31], v[114:115]
	v_pk_mul_f32 v[110:111], v[32:33], v[110:111]
	v_cvt_f32_f16_sdwa v117, v95 dst_sel:DWORD dst_unused:UNUSED_PAD src0_sel:WORD_1
	v_pk_fma_f32 v[32:33], v[112:113], s[78:79], v[110:111] op_sel_hi:[0,1,1]
	s_nop 0
	v_pk_fma_f32 v[114:115], s[94:95], v[32:33], v[114:115]
	s_nop 0
	v_add_f32_e32 v116, v114, v115
	v_fmac_f32_e32 v116, v98, v113
	v_mul_f32_e32 v116, v116, v117
	v_fma_mixlo_f16 v116, v116, s30, 0
	global_store_short v99, v116, s[26:27]
	s_add_u32 s26, s26, 0x1000
	s_addc_u32 s27, s27, 0
	s_waitcnt lgkmcnt(0)
	s_load_dwordx16 s[64:79], s[24:25], 0xe80
	s_load_dwordx16 s[80:95], s[24:25], 0xec0
	v_cvt_f32_f16_e32 v113, v92
	v_mul_f32_e32 v112, v86, v113
	v_pk_mul_f32 v[104:105], v[86:87], v[2:3] op_sel_hi:[0,1]
	v_pk_mul_f32 v[106:107], v[86:87], v[4:5] op_sel_hi:[0,1]
	v_exp_f32_e32 v104, v104
	v_exp_f32_e32 v105, v105
	v_exp_f32_e32 v106, v106
	v_pk_mul_f32 v[104:105], v[18:19], v[104:105]
	v_exp_f32_e32 v107, v107
	v_pk_fma_f32 v[18:19], v[112:113], s[32:33], v[104:105] op_sel_hi:[0,1,1]
	v_pk_mul_f32 v[106:107], v[20:21], v[106:107]
	v_pk_fma_f32 v[114:115], s[48:49], v[18:19], 0 op_sel_hi:[1,1,0]
	v_pk_fma_f32 v[20:21], v[112:113], s[34:35], v[106:107] op_sel_hi:[0,1,1]
	v_pk_mul_f32 v[108:109], v[86:87], v[6:7] op_sel_hi:[0,1]
	v_pk_fma_f32 v[114:115], s[50:51], v[20:21], v[114:115]
	v_exp_f32_e32 v108, v108
	v_exp_f32_e32 v109, v109
	v_pk_mul_f32 v[110:111], v[86:87], v[8:9] op_sel_hi:[0,1]
	v_pk_mul_f32 v[108:109], v[22:23], v[108:109]
	v_exp_f32_e32 v110, v110
	v_pk_fma_f32 v[22:23], v[112:113], s[36:37], v[108:109] op_sel_hi:[0,1,1]
	v_exp_f32_e32 v111, v111
	v_pk_fma_f32 v[114:115], s[52:53], v[22:23], v[114:115]
	v_pk_mul_f32 v[110:111], v[24:25], v[110:111]
	v_pk_mul_f32 v[104:105], v[86:87], v[10:11] op_sel_hi:[0,1]
	v_pk_fma_f32 v[24:25], v[112:113], s[38:39], v[110:111] op_sel_hi:[0,1,1]
	v_exp_f32_e32 v104, v104
	v_pk_fma_f32 v[114:115], s[54:55], v[24:25], v[114:115]
	v_exp_f32_e32 v105, v105
	v_pk_mul_f32 v[106:107], v[86:87], v[12:13] op_sel_hi:[0,1]
	v_pk_mul_f32 v[104:105], v[26:27], v[104:105]
	v_exp_f32_e32 v106, v106
	v_pk_fma_f32 v[26:27], v[112:113], s[40:41], v[104:105] op_sel_hi:[0,1,1]
	v_exp_f32_e32 v107, v107
	v_pk_fma_f32 v[114:115], s[56:57], v[26:27], v[114:115]
	v_pk_mul_f32 v[106:107], v[28:29], v[106:107]
	v_pk_mul_f32 v[108:109], v[86:87], v[14:15] op_sel_hi:[0,1]
	v_pk_fma_f32 v[28:29], v[112:113], s[42:43], v[106:107] op_sel_hi:[0,1,1]
	v_exp_f32_e32 v108, v108
	v_pk_fma_f32 v[114:115], s[58:59], v[28:29], v[114:115]
	v_exp_f32_e32 v109, v109
	v_pk_mul_f32 v[110:111], v[86:87], v[16:17] op_sel_hi:[0,1]
	v_pk_mul_f32 v[108:109], v[30:31], v[108:109]
	v_exp_f32_e32 v110, v110
	v_pk_fma_f32 v[30:31], v[112:113], s[44:45], v[108:109] op_sel_hi:[0,1,1]
	v_exp_f32_e32 v111, v111
	v_pk_fma_f32 v[114:115], s[60:61], v[30:31], v[114:115]
	v_pk_mul_f32 v[110:111], v[32:33], v[110:111]
	v_cvt_f32_f16_e32 v117, v96
	v_pk_fma_f32 v[32:33], v[112:113], s[46:47], v[110:111] op_sel_hi:[0,1,1]
	s_nop 0
	v_pk_fma_f32 v[114:115], s[62:63], v[32:33], v[114:115]
	s_nop 0
	v_add_f32_e32 v116, v114, v115
	v_fmac_f32_e32 v116, v98, v113
	v_mul_f32_e32 v116, v116, v117
	v_fma_mixlo_f16 v116, v116, s30, 0
	global_store_short v99, v116, s[26:27]
	s_add_u32 s26, s26, 0x1000
	s_addc_u32 s27, s27, 0
	s_waitcnt lgkmcnt(0)
	s_load_dwordx16 s[32:47], s[24:25], 0xf00
	s_load_dwordx16 s[48:63], s[24:25], 0xf40
	v_cvt_f32_f16_sdwa v113, v92 dst_sel:DWORD dst_unused:UNUSED_PAD src0_sel:WORD_1
	v_pk_mul_f32 v[104:105], v[86:87], v[2:3] op_sel:[1,0]
	v_mul_f32_e32 v112, v87, v113
	v_exp_f32_e32 v104, v104
	v_exp_f32_e32 v105, v105
	v_pk_mul_f32 v[106:107], v[86:87], v[4:5] op_sel:[1,0]
	v_pk_mul_f32 v[104:105], v[18:19], v[104:105]
	v_exp_f32_e32 v106, v106
	v_pk_fma_f32 v[18:19], v[112:113], s[64:65], v[104:105] op_sel_hi:[0,1,1]
	v_exp_f32_e32 v107, v107
	v_pk_fma_f32 v[114:115], s[80:81], v[18:19], 0 op_sel_hi:[1,1,0]
	v_pk_mul_f32 v[106:107], v[20:21], v[106:107]
	v_pk_mul_f32 v[108:109], v[86:87], v[6:7] op_sel:[1,0]
	v_pk_fma_f32 v[20:21], v[112:113], s[66:67], v[106:107] op_sel_hi:[0,1,1]
	v_exp_f32_e32 v108, v108
	v_pk_fma_f32 v[114:115], s[82:83], v[20:21], v[114:115]
	v_exp_f32_e32 v109, v109
	v_pk_mul_f32 v[110:111], v[86:87], v[8:9] op_sel:[1,0]
	v_pk_mul_f32 v[108:109], v[22:23], v[108:109]
	v_exp_f32_e32 v110, v110
	v_pk_fma_f32 v[22:23], v[112:113], s[68:69], v[108:109] op_sel_hi:[0,1,1]
	v_exp_f32_e32 v111, v111
	v_pk_fma_f32 v[114:115], s[84:85], v[22:23], v[114:115]
	v_pk_mul_f32 v[110:111], v[24:25], v[110:111]
	v_pk_mul_f32 v[104:105], v[86:87], v[10:11] op_sel:[1,0]
	v_pk_fma_f32 v[24:25], v[112:113], s[70:71], v[110:111] op_sel_hi:[0,1,1]
	v_exp_f32_e32 v104, v104
	v_pk_fma_f32 v[114:115], s[86:87], v[24:25], v[114:115]
	v_exp_f32_e32 v105, v105
	v_pk_mul_f32 v[106:107], v[86:87], v[12:13] op_sel:[1,0]
	v_pk_mul_f32 v[104:105], v[26:27], v[104:105]
	v_exp_f32_e32 v106, v106
	v_pk_fma_f32 v[26:27], v[112:113], s[72:73], v[104:105] op_sel_hi:[0,1,1]
	v_exp_f32_e32 v107, v107
	v_pk_fma_f32 v[114:115], s[88:89], v[26:27], v[114:115]
	v_pk_mul_f32 v[106:107], v[28:29], v[106:107]
	v_pk_mul_f32 v[108:109], v[86:87], v[14:15] op_sel:[1,0]
	v_pk_fma_f32 v[28:29], v[112:113], s[74:75], v[106:107] op_sel_hi:[0,1,1]
	v_exp_f32_e32 v108, v108
	v_pk_fma_f32 v[114:115], s[90:91], v[28:29], v[114:115]
	v_exp_f32_e32 v109, v109
	v_pk_mul_f32 v[110:111], v[86:87], v[16:17] op_sel:[1,0]
	v_pk_mul_f32 v[108:109], v[30:31], v[108:109]
	v_exp_f32_e32 v110, v110
	v_pk_fma_f32 v[30:31], v[112:113], s[76:77], v[108:109] op_sel_hi:[0,1,1]
	v_exp_f32_e32 v111, v111
	v_pk_fma_f32 v[114:115], s[92:93], v[30:31], v[114:115]
	v_pk_mul_f32 v[110:111], v[32:33], v[110:111]
	v_cvt_f32_f16_sdwa v117, v96 dst_sel:DWORD dst_unused:UNUSED_PAD src0_sel:WORD_1
	v_pk_fma_f32 v[32:33], v[112:113], s[78:79], v[110:111] op_sel_hi:[0,1,1]
	s_nop 0
	v_pk_fma_f32 v[114:115], s[94:95], v[32:33], v[114:115]
	s_nop 0
	v_add_f32_e32 v116, v114, v115
	v_fmac_f32_e32 v116, v98, v113
	v_mul_f32_e32 v116, v116, v117
	v_fma_mixlo_f16 v116, v116, s30, 0
	global_store_short v99, v116, s[26:27]
	s_add_u32 s26, s26, 0x1000
	s_addc_u32 s27, s27, 0
	s_waitcnt lgkmcnt(0)
	s_load_dwordx16 s[64:79], s[24:25], 0xf80
	s_load_dwordx16 s[80:95], s[24:25], 0xfc0
	v_cvt_f32_f16_e32 v113, v93
	v_mul_f32_e32 v112, v88, v113
	v_pk_mul_f32 v[104:105], v[88:89], v[2:3] op_sel_hi:[0,1]
	v_pk_mul_f32 v[106:107], v[88:89], v[4:5] op_sel_hi:[0,1]
	v_exp_f32_e32 v104, v104
	v_exp_f32_e32 v105, v105
	v_exp_f32_e32 v106, v106
	v_pk_mul_f32 v[104:105], v[18:19], v[104:105]
	v_exp_f32_e32 v107, v107
	v_pk_fma_f32 v[18:19], v[112:113], s[32:33], v[104:105] op_sel_hi:[0,1,1]
	v_pk_mul_f32 v[106:107], v[20:21], v[106:107]
	v_pk_fma_f32 v[114:115], s[48:49], v[18:19], 0 op_sel_hi:[1,1,0]
	v_pk_fma_f32 v[20:21], v[112:113], s[34:35], v[106:107] op_sel_hi:[0,1,1]
	v_pk_mul_f32 v[108:109], v[88:89], v[6:7] op_sel_hi:[0,1]
	v_pk_fma_f32 v[114:115], s[50:51], v[20:21], v[114:115]
	v_exp_f32_e32 v108, v108
	v_exp_f32_e32 v109, v109
	v_pk_mul_f32 v[110:111], v[88:89], v[8:9] op_sel_hi:[0,1]
	v_pk_mul_f32 v[108:109], v[22:23], v[108:109]
	v_exp_f32_e32 v110, v110
	v_pk_fma_f32 v[22:23], v[112:113], s[36:37], v[108:109] op_sel_hi:[0,1,1]
	v_exp_f32_e32 v111, v111
	v_pk_fma_f32 v[114:115], s[52:53], v[22:23], v[114:115]
	v_pk_mul_f32 v[110:111], v[24:25], v[110:111]
	v_pk_mul_f32 v[104:105], v[88:89], v[10:11] op_sel_hi:[0,1]
	v_pk_fma_f32 v[24:25], v[112:113], s[38:39], v[110:111] op_sel_hi:[0,1,1]
	v_exp_f32_e32 v104, v104
	v_pk_fma_f32 v[114:115], s[54:55], v[24:25], v[114:115]
	v_exp_f32_e32 v105, v105
	v_pk_mul_f32 v[106:107], v[88:89], v[12:13] op_sel_hi:[0,1]
	v_pk_mul_f32 v[104:105], v[26:27], v[104:105]
	v_exp_f32_e32 v106, v106
	v_pk_fma_f32 v[26:27], v[112:113], s[40:41], v[104:105] op_sel_hi:[0,1,1]
	v_exp_f32_e32 v107, v107
	v_pk_fma_f32 v[114:115], s[56:57], v[26:27], v[114:115]
	v_pk_mul_f32 v[106:107], v[28:29], v[106:107]
	v_pk_mul_f32 v[108:109], v[88:89], v[14:15] op_sel_hi:[0,1]
	v_pk_fma_f32 v[28:29], v[112:113], s[42:43], v[106:107] op_sel_hi:[0,1,1]
	v_exp_f32_e32 v108, v108
	v_pk_fma_f32 v[114:115], s[58:59], v[28:29], v[114:115]
	v_exp_f32_e32 v109, v109
	v_pk_mul_f32 v[110:111], v[88:89], v[16:17] op_sel_hi:[0,1]
	v_pk_mul_f32 v[108:109], v[30:31], v[108:109]
	v_exp_f32_e32 v110, v110
	v_pk_fma_f32 v[30:31], v[112:113], s[44:45], v[108:109] op_sel_hi:[0,1,1]
	v_exp_f32_e32 v111, v111
	v_pk_fma_f32 v[114:115], s[60:61], v[30:31], v[114:115]
	v_pk_mul_f32 v[110:111], v[32:33], v[110:111]
	v_cvt_f32_f16_e32 v117, v97
	v_pk_fma_f32 v[32:33], v[112:113], s[46:47], v[110:111] op_sel_hi:[0,1,1]
	s_nop 0
	v_pk_fma_f32 v[114:115], s[62:63], v[32:33], v[114:115]
	s_nop 0
	v_add_f32_e32 v116, v114, v115
	v_fmac_f32_e32 v116, v98, v113
	v_mul_f32_e32 v116, v116, v117
	v_fma_mixlo_f16 v116, v116, s30, 0
	global_store_short v99, v116, s[26:27]
	s_add_u32 s26, s26, 0x1000
	s_addc_u32 s27, s27, 0
	s_waitcnt lgkmcnt(0)
	v_cvt_f32_f16_sdwa v113, v93 dst_sel:DWORD dst_unused:UNUSED_PAD src0_sel:WORD_1
	v_pk_mul_f32 v[104:105], v[88:89], v[2:3] op_sel:[1,0]
	v_mul_f32_e32 v112, v89, v113
	v_exp_f32_e32 v104, v104
	v_exp_f32_e32 v105, v105
	v_pk_mul_f32 v[106:107], v[88:89], v[4:5] op_sel:[1,0]
	v_pk_mul_f32 v[104:105], v[18:19], v[104:105]
	v_exp_f32_e32 v106, v106
	v_pk_fma_f32 v[18:19], v[112:113], s[64:65], v[104:105] op_sel_hi:[0,1,1]
	v_exp_f32_e32 v107, v107
	v_pk_fma_f32 v[114:115], s[80:81], v[18:19], 0 op_sel_hi:[1,1,0]
	v_pk_mul_f32 v[106:107], v[20:21], v[106:107]
	v_pk_mul_f32 v[108:109], v[88:89], v[6:7] op_sel:[1,0]
	v_pk_fma_f32 v[20:21], v[112:113], s[66:67], v[106:107] op_sel_hi:[0,1,1]
	v_exp_f32_e32 v108, v108
	v_pk_fma_f32 v[114:115], s[82:83], v[20:21], v[114:115]
	v_exp_f32_e32 v109, v109
	v_pk_mul_f32 v[110:111], v[88:89], v[8:9] op_sel:[1,0]
	v_pk_mul_f32 v[108:109], v[22:23], v[108:109]
	v_exp_f32_e32 v110, v110
	v_pk_fma_f32 v[22:23], v[112:113], s[68:69], v[108:109] op_sel_hi:[0,1,1]
	v_exp_f32_e32 v111, v111
	v_pk_fma_f32 v[114:115], s[84:85], v[22:23], v[114:115]
	v_pk_mul_f32 v[110:111], v[24:25], v[110:111]
	v_pk_mul_f32 v[104:105], v[88:89], v[10:11] op_sel:[1,0]
	v_pk_fma_f32 v[24:25], v[112:113], s[70:71], v[110:111] op_sel_hi:[0,1,1]
	v_exp_f32_e32 v104, v104
	v_pk_fma_f32 v[114:115], s[86:87], v[24:25], v[114:115]
	v_exp_f32_e32 v105, v105
	v_pk_mul_f32 v[106:107], v[88:89], v[12:13] op_sel:[1,0]
	v_pk_mul_f32 v[104:105], v[26:27], v[104:105]
	v_exp_f32_e32 v106, v106
	v_pk_fma_f32 v[26:27], v[112:113], s[72:73], v[104:105] op_sel_hi:[0,1,1]
	v_exp_f32_e32 v107, v107
	v_pk_fma_f32 v[114:115], s[88:89], v[26:27], v[114:115]
	v_pk_mul_f32 v[106:107], v[28:29], v[106:107]
	v_pk_mul_f32 v[108:109], v[88:89], v[14:15] op_sel:[1,0]
	v_pk_fma_f32 v[28:29], v[112:113], s[74:75], v[106:107] op_sel_hi:[0,1,1]
	v_exp_f32_e32 v108, v108
	v_pk_fma_f32 v[114:115], s[90:91], v[28:29], v[114:115]
	v_exp_f32_e32 v109, v109
	v_pk_mul_f32 v[110:111], v[88:89], v[16:17] op_sel:[1,0]
	v_pk_mul_f32 v[108:109], v[30:31], v[108:109]
	v_exp_f32_e32 v110, v110
	v_pk_fma_f32 v[30:31], v[112:113], s[76:77], v[108:109] op_sel_hi:[0,1,1]
	v_exp_f32_e32 v111, v111
	v_pk_fma_f32 v[114:115], s[92:93], v[30:31], v[114:115]
	v_pk_mul_f32 v[110:111], v[32:33], v[110:111]
	v_cvt_f32_f16_sdwa v117, v97 dst_sel:DWORD dst_unused:UNUSED_PAD src0_sel:WORD_1
	v_pk_fma_f32 v[32:33], v[112:113], s[78:79], v[110:111] op_sel_hi:[0,1,1]
	s_nop 0
	v_pk_fma_f32 v[114:115], s[94:95], v[32:33], v[114:115]
	s_nop 0
	v_add_f32_e32 v116, v114, v115
	v_fmac_f32_e32 v116, v98, v113
	v_mul_f32_e32 v116, v116, v117
	v_fma_mixlo_f16 v116, v116, s30, 0
	global_store_short v99, v116, s[26:27]
	s_endpgm
	.p2alignl 8, 3212836864

amdhsa.kernels:
  - .agpr_count:     0
    .args:
      - .address_space:  global
        .offset:         0
        .size:           8
        .value_kind:     global_buffer
      - .address_space:  global
        .offset:         8
        .size:           8
        .value_kind:     global_buffer
      - .offset:         16
        .size:           8
        .value_kind:     by_value
      - .address_space:  global
        .offset:         24
        .size:           8
        .value_kind:     global_buffer
      - .address_space:  global
        .offset:         32
        .size:           8
        .value_kind:     global_buffer
      - .offset:         40
        .size:           8
        .value_kind:     by_value
      - .address_space:  global
        .offset:         48
        .size:           8
        .value_kind:     global_buffer
      - .address_space:  global
        .offset:         56
        .size:           8
        .value_kind:     global_buffer
      - .offset:         64
        .size:           8
        .value_kind:     by_value
      - .address_space:  global
        .offset:         72
        .size:           8
        .value_kind:     global_buffer
      - .address_space:  global
        .offset:         80
        .size:           8
        .value_kind:     global_buffer
      - .offset:         88
        .size:           8
        .value_kind:     by_value
      - .address_space:  global
        .offset:         96
        .size:           8
        .value_kind:     global_buffer
      - .address_space:  global
        .offset:         104
        .size:           8
        .value_kind:     global_buffer
      - .offset:         112
        .size:           8
        .value_kind:     by_value
      - .address_space:  global
        .offset:         120
        .size:           8
        .value_kind:     global_buffer
      - .actual_access:  read_only
        .address_space:  global
        .offset:         128
        .size:           8
        .value_kind:     global_buffer
      - .actual_access:  write_only
        .address_space:  global
        .offset:         136
        .size:           8
        .value_kind:     global_buffer
    .group_segment_fixed_size: 0
    .kernarg_segment_align: 8
    .kernarg_segment_size: 144
    .language:       OpenCL C
    .language_version:
      - 2
      - 0
    .max_flat_workgroup_size: 256
    .name:           _Z10cvt_kernelPKfPDF16_lS0_S1_lS0_S1_lS0_S1_lS0_S1_lPjS0_Pf
    .private_segment_fixed_size: 0
    .sgpr_count:     58
    .sgpr_spill_count: 0
    .symbol:         _Z10cvt_kernelPKfPDF16_lS0_S1_lS0_S1_lS0_S1_lS0_S1_lPjS0_Pf.kd
    .uniform_work_group_size: 1
    .uses_dynamic_stack: false
    .vgpr_count:     18
    .vgpr_spill_count: 0
    .wavefront_size: 64
  - .agpr_count:     0
    .args:
      - .actual_access:  read_only
        .address_space:  global
        .offset:         0
        .size:           8
        .value_kind:     global_buffer
      - .actual_access:  read_only
        .address_space:  global
        .offset:         8
        .size:           8
        .value_kind:     global_buffer
      - .actual_access:  read_only
        .address_space:  global
        .offset:         16
        .size:           8
        .value_kind:     global_buffer
      - .actual_access:  read_only
        .address_space:  global
        .offset:         24
        .size:           8
        .value_kind:     global_buffer
      - .actual_access:  write_only
        .address_space:  global
        .offset:         32
        .size:           8
        .value_kind:     global_buffer
      - .actual_access:  write_only
        .address_space:  global
        .offset:         40
        .size:           8
        .value_kind:     global_buffer
      - .actual_access:  write_only
        .address_space:  global
        .offset:         48
        .size:           8
        .value_kind:     global_buffer
    .group_segment_fixed_size: 65792
    .kernarg_segment_align: 8
    .kernarg_segment_size: 56
    .language:       OpenCL C
    .language_version:
      - 2
      - 0
    .max_flat_workgroup_size: 1024
    .name:           _Z17conv_xproj_kernelPKDF16_PKfS2_S0_PDF16_S3_Pf
    .private_segment_fixed_size: 0
    .sgpr_count:     26
    .sgpr_spill_count: 0
    .symbol:         _Z17conv_xproj_kernelPKDF16_PKfS2_S0_PDF16_S3_Pf.kd
    .uniform_work_group_size: 1
    .uses_dynamic_stack: false
    .vgpr_count:     128
    .vgpr_spill_count: 0
    .wavefront_size: 64
  - .agpr_count:     0
    .args:
      - .actual_access:  read_only
        .address_space:  global
        .offset:         0
        .size:           8
        .value_kind:     global_buffer
      - .actual_access:  read_only
        .address_space:  global
        .offset:         8
        .size:           8
        .value_kind:     global_buffer
      - .actual_access:  read_only
        .address_space:  global
        .offset:         16
        .size:           8
        .value_kind:     global_buffer
      - .actual_access:  read_only
        .address_space:  global
        .offset:         24
        .size:           8
        .value_kind:     global_buffer
      - .actual_access:  read_only
        .address_space:  global
        .offset:         32
        .size:           8
        .value_kind:     global_buffer
      - .actual_access:  read_only
        .address_space:  global
        .offset:         40
        .size:           8
        .value_kind:     global_buffer
      - .actual_access:  write_only
        .address_space:  global
        .offset:         48
        .size:           8
        .value_kind:     global_buffer
      - .actual_access:  write_only
        .address_space:  global
        .offset:         56
        .size:           8
        .value_kind:     global_buffer
      - .actual_access:  write_only
        .address_space:  global
        .offset:         64
        .size:           8
        .value_kind:     global_buffer
      - .actual_access:  read_only
        .address_space:  global
        .offset:         72
        .size:           8
        .value_kind:     global_buffer
      - .actual_access:  write_only
        .address_space:  global
        .offset:         80
        .size:           8
        .value_kind:     global_buffer
    .group_segment_fixed_size: 4096
    .kernarg_segment_align: 8
    .kernarg_segment_size: 88
    .language:       OpenCL C
    .language_version:
      - 2
      - 0
    .max_flat_workgroup_size: 256
    .name:           _Z10scan_pass1PKDF16_S0_PKfS0_S2_S2_PDF16_PfS4_S2_S3_
    .private_segment_fixed_size: 0
    .sgpr_count:     94
    .sgpr_spill_count: 0
    .symbol:         _Z10scan_pass1PKDF16_S0_PKfS0_S2_S2_PDF16_PfS4_S2_S3_.kd
    .uniform_work_group_size: 1
    .uses_dynamic_stack: false
    .vgpr_count:     128
    .vgpr_spill_count: 0
    .wavefront_size: 64
  - .agpr_count:     0
    .args:
      - .actual_access:  read_only
        .address_space:  global
        .offset:         0
        .size:           8
        .value_kind:     global_buffer
      - .actual_access:  read_only
        .address_space:  global
        .offset:         8
        .size:           8
        .value_kind:     global_buffer
      - .actual_access:  read_only
        .address_space:  global
        .offset:         16
        .size:           8
        .value_kind:     global_buffer
      - .actual_access:  read_only
        .address_space:  global
        .offset:         24
        .size:           8
        .value_kind:     global_buffer
      - .actual_access:  read_only
        .address_space:  global
        .offset:         32
        .size:           8
        .value_kind:     global_buffer
      - .actual_access:  read_only
        .address_space:  global
        .offset:         40
        .size:           8
        .value_kind:     global_buffer
      - .actual_access:  write_only
        .address_space:  global
        .offset:         48
        .size:           8
        .value_kind:     global_buffer
      - .actual_access:  read_only
        .address_space:  global
        .offset:         56
        .size:           8
        .value_kind:     global_buffer
    .group_segment_fixed_size: 4096
    .kernarg_segment_align: 8
    .kernarg_segment_size: 64
    .language:       OpenCL C
    .language_version:
      - 2
      - 0
    .max_flat_workgroup_size: 256
    .name:           _Z10scan_pass2PKDF16_PKfS2_S0_S2_S0_PDF16_S2_
    .private_segment_fixed_size: 0
    .sgpr_count:     104
    .sgpr_spill_count: 0
    .symbol:         _Z10scan_pass2PKDF16_PKfS2_S0_S2_S0_PDF16_S2_.kd
    .uniform_work_group_size: 1
    .uses_dynamic_stack: false
    .vgpr_count:     118
    .vgpr_spill_count: 0
    .wavefront_size: 64
  - .agpr_count:     0
    .args:
      - .actual_access:  read_only
        .address_space:  global
        .offset:         0
        .size:           8
        .value_kind:     global_buffer
      - .actual_access:  read_only
        .address_space:  global
        .offset:         8
        .size:           8
        .value_kind:     global_buffer
      - .actual_access:  read_only
        .address_space:  global
        .offset:         16
        .size:           8
        .value_kind:     global_buffer
      - .actual_access:  write_only
        .address_space:  global
        .offset:         24
        .size:           8
        .value_kind:     global_buffer
    .group_segment_fixed_size: 8192
    .kernarg_segment_align: 8
    .kernarg_segment_size: 32
    .language:       OpenCL C
    .language_version:
      - 2
      - 0
    .max_flat_workgroup_size: 512
    .name:           _Z12scan_combinePKfPKDF16_S0_PDF16_
    .private_segment_fixed_size: 0
    .sgpr_count:     20
    .sgpr_spill_count: 0
    .symbol:         _Z12scan_combinePKfPKDF16_S0_PDF16_.kd
    .uniform_work_group_size: 1
    .uses_dynamic_stack: false
    .vgpr_count:     66
    .vgpr_spill_count: 0
    .wavefront_size: 64
  - .agpr_count:     0
    .args:
      - .address_space:  global
        .offset:         0
        .size:           8
        .value_kind:     global_buffer
      - .address_space:  global
        .offset:         8
        .size:           8
        .value_kind:     global_buffer
      - .actual_access:  write_only
        .address_space:  global
        .offset:         16
        .size:           8
        .value_kind:     global_buffer
      - .actual_access:  read_only
        .address_space:  global
        .offset:         24
        .size:           8
        .value_kind:     global_buffer
      - .offset:         32
        .size:           4
        .value_kind:     by_value
      - .actual_access:  read_only
        .address_space:  global
        .offset:         40
        .size:           8
        .value_kind:     global_buffer
    .group_segment_fixed_size: 0
    .kernarg_segment_align: 8
    .kernarg_segment_size: 48
    .language:       OpenCL C
    .language_version:
      - 2
      - 0
    .max_flat_workgroup_size: 512
    .name:           _Z11gemm_8phaseILi0ELi16ELi16ELi1024ELi1024ELi4096ELi1EEvPKDF16_S1_PvS2_fPj
    .private_segment_fixed_size: 0
    .sgpr_count:     38
    .sgpr_spill_count: 0
    .symbol:         _Z11gemm_8phaseILi0ELi16ELi16ELi1024ELi1024ELi4096ELi1EEvPKDF16_S1_PvS2_fPj.kd
    .uniform_work_group_size: 1
    .uses_dynamic_stack: false
    .vgpr_count:     236
    .vgpr_spill_count: 0
    .wavefront_size: 64
  - .agpr_count:     0
    .args:
      - .address_space:  global
        .offset:         0
        .size:           8
        .value_kind:     global_buffer
      - .address_space:  global
        .offset:         8
        .size:           8
        .value_kind:     global_buffer
      - .actual_access:  write_only
        .address_space:  global
        .offset:         16
        .size:           8
        .value_kind:     global_buffer
      - .address_space:  global
        .offset:         24
        .size:           8
        .value_kind:     global_buffer
      - .offset:         32
        .size:           4
        .value_kind:     by_value
      - .address_space:  global
        .offset:         40
        .size:           8
        .value_kind:     global_buffer
    .group_segment_fixed_size: 0
    .kernarg_segment_align: 8
    .kernarg_segment_size: 48
    .language:       OpenCL C
    .language_version:
      - 2
      - 0
    .max_flat_workgroup_size: 512
    .name:           _Z11gemm_8phaseILi1ELi16ELi4ELi512ELi2048ELi1024ELi4EEvPKDF16_S1_PvS2_fPj
    .private_segment_fixed_size: 0
    .sgpr_count:     41
    .sgpr_spill_count: 0
    .symbol:         _Z11gemm_8phaseILi1ELi16ELi4ELi512ELi2048ELi1024ELi4EEvPKDF16_S1_PvS2_fPj.kd
    .uniform_work_group_size: 1
    .uses_dynamic_stack: false
    .vgpr_count:     236
    .vgpr_spill_count: 0
    .wavefront_size: 64
  - .agpr_count:     0
    .args:
      - .address_space:  global
        .offset:         0
        .size:           8
        .value_kind:     global_buffer
      - .address_space:  global
        .offset:         8
        .size:           8
        .value_kind:     global_buffer
      - .actual_access:  write_only
        .address_space:  global
        .offset:         16
        .size:           8
        .value_kind:     global_buffer
      - .address_space:  global
        .offset:         24
        .size:           8
        .value_kind:     global_buffer
      - .offset:         32
        .size:           4
        .value_kind:     by_value
      - .address_space:  global
        .offset:         40
        .size:           8
        .value_kind:     global_buffer
    .group_segment_fixed_size: 0
    .kernarg_segment_align: 8
    .kernarg_segment_size: 48
    .language:       OpenCL C
    .language_version:
      - 2
      - 0
    .max_flat_workgroup_size: 512
    .name:           _Z11gemm_8phaseILi2ELi16ELi4ELi512ELi2048ELi1024ELi4EEvPKDF16_S1_PvS2_fPj
    .private_segment_fixed_size: 0
    .sgpr_count:     41
    .sgpr_spill_count: 0
    .symbol:         _Z11gemm_8phaseILi2ELi16ELi4ELi512ELi2048ELi1024ELi4EEvPKDF16_S1_PvS2_fPj.kd
    .uniform_work_group_size: 1
    .uses_dynamic_stack: false
    .vgpr_count:     236
    .vgpr_spill_count: 0
    .wavefront_size: 64
